# GEMM K-loops: LDS-DMA pieces issued before the fragment reads in every load phase
# speedup vs baseline: 1.0044x; 1.0044x over previous
; #define GM_STAGE(bufoff, gbase, voff) do { _Pragma("unroll") for (int _i = 0; _i < 2; ++_i) \
;         __builtin_amdgcn_global_load_lds((const unsigned*)((const char*)(gbase) + (voff)[_i]), (LAS unsigned*)(lds + (bufoff) + ldsw + _i * 8192), 16, 0, 0); } while (0)
; #define GM_LDA(dst, b, h) do { _Pragma("unroll") for (int m = 0; m < 4; ++m) _Pragma("unroll") for (int k = 0; k < 2; ++k) dst[m][k] = *(const LAS s16x8*)(lds + GM_SA(b, h) + aoff + m * 2048 + k * 1024); } while (0)
; #define GM_LDB(dst, b, h) do { _Pragma("unroll") for (int n = 0; n < 2; ++n) _Pragma("unroll") for (int k = 0; k < 2; ++k) dst[n][k] = *(const LAS s16x8*)(lds + GM_SB(b, h) + boff + n * 2048 + k * 1024); } while (0)
; #define GM_MMA(ai, bj, At, Bt) do { __builtin_amdgcn_s_setprio(1); _Pragma("unroll") for (int m = 0; m < 4; ++m) _Pragma("unroll") for (int n = 0; n < 2; ++n) _Pragma("unroll") for (int k = 0; k < 2; ++k) \
;         acc[ai][bj][m][n] = mma16<BF>(Bt[n][k], At[m][k], acc[ai][bj][m][n]); __builtin_amdgcn_s_setprio(0); } while (0)
; #define GM_WAIT_V(n) asm volatile("s_waitcnt vmcnt(" #n ")" ::: "memory")
; #define GM_BAR __builtin_amdgcn_s_barrier()
; template <bool BF, bool GATHER = false, class Epi, class Hook>
; __device__ __forceinline__ void gemm_phase(LAS unsigned char* lds, const Gemm g, const Order& S, const Epi& E, Hook& HK) {
;     ...
;         for (int t = 0; t < nt; t += 2) {
;             const bool last = (t == nt - 2);
;             const char* a1 = cA + (size_t)(t + 1) * kstep;
;             const char* a2 = last ? nA : cA + (size_t)(t + 2) * kstep; const char* b2 = last ? nB : cB + (size_t)(t + 2) * kstep;
;             const char* a3 = a2 + kstep; const char* b3 = b2 + kstep;
;             unsigned s0[2], s1[2];
;             if constexpr (GATHER) { s0[0] = last ? nA0[0] : gA0[0]; s0[1] = last ? nA0[1] : gA0[1]; s1[0] = last ? nA1[0] : gA1[0]; s1[1] = last ? nA1[1] : gA1[1]; }
;             GM_LDB(B0, 0, 0); GM_LDB(B1, 0, 1); GM_SCHED; GM_LDA(At, 0, 0); GM_STA_H1(GM_SA(1, 1), a1, gA1);
;             GM_WAIT_V(8); GM_WAIT_L(0); GM_BAR; GM_MMA(0, 0, At, B0); GM_MMA(0, 1, At, B1); GM_BAR; GM_SCHED;
;             GM_LDA(At, 0, 1); GM_STAGE(GM_SB(0, 0), b2, voffB); GM_STAGE(GM_SB(0, 1), b2 + hstepB, voffB); GM_STA_H0(GM_SA(0, 0), a2, s0);
;             GM_WAIT_V(8); GM_WAIT_L(0); GM_BAR; GM_MMA(1, 0, At, B0); GM_MMA(1, 1, At, B1); GM_BAR; GM_SCHED;
.LBB0_380:
	s_add_u32 s28, s2, 0xfffc0080
	s_addc_u32 s29, s3, -1
	s_cmp_eq_u32 s51, 12
	s_cselect_b32 s31, s9, s29
	s_cselect_b32 s30, s19, s28
	s_cselect_b32 s29, s21, s50
	s_cselect_b32 s28, s48, s49
	v_lshl_add_u64 v[150:151], s[2:3], 0, v[138:139]
	s_add_i32 m0, s27, 0xc000
	global_load_lds_dwordx4 v[150:151], off
	v_lshl_add_u64 v[150:151], s[2:3], 0, v[140:141]
	s_add_i32 m0, s27, 0xe000
	s_nop 0
	global_load_lds_dwordx4 v[150:151], off
	ds_read_b128 v[146:149], v158
	ds_read_b128 v[162:165], v158 offset:1024
	ds_read_b128 v[166:169], v158 offset:2048
	ds_read_b128 v[170:173], v158 offset:3072
	ds_read_b128 v[174:177], v159
	ds_read_b128 v[178:181], v159 offset:1024
	ds_read_b128 v[182:185], v159 offset:2048
	ds_read_b128 v[186:189], v159 offset:3072
	ds_read_b128 v[190:193], v160
	ds_read_b128 v[194:197], v160 offset:1024
	ds_read_b128 v[198:201], v160 offset:2048
	ds_read_b128 v[202:205], v160 offset:3072
	ds_read_b128 v[206:209], v160 offset:4096
	ds_read_b128 v[210:213], v160 offset:5120
	ds_read_b128 v[214:217], v160 offset:6144
	ds_read_b128 v[218:221], v160 offset:7168
	s_waitcnt vmcnt(8)
	s_waitcnt lgkmcnt(0)
	s_barrier
	s_setprio 1
	s_waitcnt lgkmcnt(0)
	v_mfma_f32_16x16x32_f16 v[126:129], v[146:149], v[190:193], v[126:129]
	v_mfma_f32_16x16x32_f16 v[122:125], v[166:169], v[190:193], v[122:125]
	v_mfma_f32_16x16x32_f16 v[110:113], v[146:149], v[198:201], v[110:113]
	v_mfma_f32_16x16x32_f16 v[106:109], v[166:169], v[198:201], v[106:109]
	v_mfma_f32_16x16x32_f16 v[94:97], v[146:149], v[206:209], v[94:97]
	v_mfma_f32_16x16x32_f16 v[90:93], v[166:169], v[206:209], v[90:93]
	v_mfma_f32_16x16x32_f16 v[78:81], v[146:149], v[214:217], v[78:81]
	v_mfma_f32_16x16x32_f16 v[74:77], v[166:169], v[214:217], v[74:77]
	v_mfma_f32_16x16x32_f16 v[126:129], v[162:165], v[194:197], v[126:129]
	v_mfma_f32_16x16x32_f16 v[122:125], v[170:173], v[194:197], v[122:125]
	v_mfma_f32_16x16x32_f16 v[110:113], v[162:165], v[202:205], v[110:113]
	v_mfma_f32_16x16x32_f16 v[106:109], v[170:173], v[202:205], v[106:109]
	v_mfma_f32_16x16x32_f16 v[94:97], v[162:165], v[210:213], v[94:97]
	v_mfma_f32_16x16x32_f16 v[90:93], v[170:173], v[210:213], v[90:93]
	v_mfma_f32_16x16x32_f16 v[78:81], v[162:165], v[218:221], v[78:81]
	v_mfma_f32_16x16x32_f16 v[74:77], v[170:173], v[218:221], v[74:77]
	s_setprio 0
	s_setprio 1
	v_mfma_f32_16x16x32_f16 v[118:121], v[174:177], v[190:193], v[118:121]
	v_mfma_f32_16x16x32_f16 v[114:117], v[182:185], v[190:193], v[114:117]
	v_mfma_f32_16x16x32_f16 v[102:105], v[174:177], v[198:201], v[102:105]
	v_mfma_f32_16x16x32_f16 v[98:101], v[182:185], v[198:201], v[98:101]
	v_mfma_f32_16x16x32_f16 v[86:89], v[174:177], v[206:209], v[86:89]
	v_mfma_f32_16x16x32_f16 v[82:85], v[182:185], v[206:209], v[82:85]
	v_mfma_f32_16x16x32_f16 v[70:73], v[174:177], v[214:217], v[70:73]
	v_mfma_f32_16x16x32_f16 v[66:69], v[182:185], v[214:217], v[66:69]
	v_mfma_f32_16x16x32_f16 v[118:121], v[178:181], v[194:197], v[118:121]
	v_mfma_f32_16x16x32_f16 v[114:117], v[186:189], v[194:197], v[114:117]
	v_mfma_f32_16x16x32_f16 v[102:105], v[178:181], v[202:205], v[102:105]
	v_mfma_f32_16x16x32_f16 v[98:101], v[186:189], v[202:205], v[98:101]
	v_mfma_f32_16x16x32_f16 v[86:89], v[178:181], v[210:213], v[86:89]
	v_mfma_f32_16x16x32_f16 v[82:85], v[186:189], v[210:213], v[82:85]
	v_mfma_f32_16x16x32_f16 v[70:73], v[178:181], v[218:221], v[70:73]
	v_mfma_f32_16x16x32_f16 v[66:69], v[186:189], v[218:221], v[66:69]
	s_setprio 0
	s_barrier
	s_add_i32 s52, s45, s35
	v_lshl_add_u64 v[150:151], s[28:29], 0, v[132:133]
	s_mov_b32 m0, s52
	global_load_lds_dwordx4 v[150:151], off
	s_add_i32 m0, s52, 0x2000
	s_add_u32 s52, s28, 0x40000
	v_lshl_add_u64 v[222:223], s[28:29], 0, v[136:137]
	s_addc_u32 s53, s29, 0
	s_add_i32 s54, s46, s35
	global_load_lds_dwordx4 v[222:223], off
	v_lshl_add_u64 v[224:225], s[52:53], 0, v[132:133]
	s_mov_b32 m0, s54
	v_lshl_add_u64 v[226:227], s[30:31], 0, v[134:135]
	global_load_lds_dwordx4 v[224:225], off
	v_lshl_add_u64 v[224:225], s[52:53], 0, v[136:137]
	s_add_i32 m0, s54, 0x2000
	s_nop 0
	global_load_lds_dwordx4 v[224:225], off
	v_lshl_add_u64 v[224:225], s[30:31], 0, v[130:131]
	s_mov_b32 m0, s27
	s_nop 0
	global_load_lds_dwordx4 v[224:225], off
	s_mov_b32 m0, s36
	s_nop 0
	global_load_lds_dwordx4 v[226:227], off
	ds_read_b128 v[190:193], v160 offset:16384
	ds_read_b128 v[194:197], v160 offset:17408
	ds_read_b128 v[198:201], v160 offset:18432
	ds_read_b128 v[202:205], v160 offset:19456
	ds_read_b128 v[206:209], v160 offset:20480
	ds_read_b128 v[210:213], v160 offset:21504
	ds_read_b128 v[214:217], v160 offset:22528
	ds_read_b128 v[218:221], v160 offset:23552
	s_waitcnt vmcnt(8)
	s_waitcnt lgkmcnt(0)
	s_barrier
; #define GM_LDA(dst, b, h) do { _Pragma("unroll") for (int m = 0; m < 4; ++m) _Pragma("unroll") for (int k = 0; k < 2; ++k) dst[m][k] = *(const LAS s16x8*)(lds + GM_SA(b, h) + aoff + m * 2048 + k * 1024); } while (0)
; #define GM_LDB(dst, b, h) do { _Pragma("unroll") for (int n = 0; n < 2; ++n) _Pragma("unroll") for (int k = 0; k < 2; ++k) dst[n][k] = *(const LAS s16x8*)(lds + GM_SB(b, h) + boff + n * 2048 + k * 1024); } while (0)
; #define GM_MMA(ai, bj, At, Bt) do { __builtin_amdgcn_s_setprio(1); _Pragma("unroll") for (int m = 0; m < 4; ++m) _Pragma("unroll") for (int n = 0; n < 2; ++n) _Pragma("unroll") for (int k = 0; k < 2; ++k) \
;         acc[ai][bj][m][n] = mma16<BF>(Bt[n][k], At[m][k], acc[ai][bj][m][n]); __builtin_amdgcn_s_setprio(0); } while (0)
; #define GM_WAIT_V(n) asm volatile("s_waitcnt vmcnt(" #n ")" ::: "memory")
; #define GM_WAIT_L(n) asm volatile("s_waitcnt lgkmcnt(" #n ")" ::: "memory")
; #define GM_BAR __builtin_amdgcn_s_barrier()
; #define GM_SCHED __builtin_amdgcn_sched_barrier(0)
; #define GM_STA_H1(buf, p, o1) do { if constexpr (GATHER) GM_STAGE(buf, p, o1); else GM_STAGE(buf, (p) + hstepB, voffA); } while (0)
; template <bool BF, bool GATHER = false, class Epi, class Hook>
; __device__ __forceinline__ void gemm_phase(LAS unsigned char* lds, const Gemm g, const Order& S, const Epi& E, Hook& HK) {
;     ...
;             GM_WAIT_V(8); GM_WAIT_L(0); GM_BAR; GM_MMA(1, 0, At, B0); GM_MMA(1, 1, At, B1); GM_BAR; GM_SCHED;
;             GM_LDB(B0, 1, 0); GM_LDB(B1, 1, 1); GM_SCHED; GM_LDA(At, 1, 0); GM_STA_H1(GM_SA(0, 1), a2, s1);
;             GM_WAIT_V(8); GM_WAIT_L(0); GM_BAR; GM_MMA(0, 0, At, B0); GM_MMA(0, 1, At, B1); GM_BAR; GM_SCHED;
	s_setprio 1
	s_waitcnt lgkmcnt(0)
	v_mfma_f32_16x16x32_f16 v[62:65], v[146:149], v[190:193], v[62:65]
	v_mfma_f32_16x16x32_f16 v[58:61], v[166:169], v[190:193], v[58:61]
	v_mfma_f32_16x16x32_f16 v[46:49], v[146:149], v[198:201], v[46:49]
	v_mfma_f32_16x16x32_f16 v[42:45], v[166:169], v[198:201], v[42:45]
	v_mfma_f32_16x16x32_f16 v[30:33], v[146:149], v[206:209], v[30:33]
	v_mfma_f32_16x16x32_f16 v[26:29], v[166:169], v[206:209], v[26:29]
	v_mfma_f32_16x16x32_f16 v[14:17], v[146:149], v[214:217], v[14:17]
	v_mfma_f32_16x16x32_f16 v[10:13], v[166:169], v[214:217], v[10:13]
	v_mfma_f32_16x16x32_f16 v[62:65], v[162:165], v[194:197], v[62:65]
	v_mfma_f32_16x16x32_f16 v[58:61], v[170:173], v[194:197], v[58:61]
	v_mfma_f32_16x16x32_f16 v[46:49], v[162:165], v[202:205], v[46:49]
	v_mfma_f32_16x16x32_f16 v[42:45], v[170:173], v[202:205], v[42:45]
	v_mfma_f32_16x16x32_f16 v[30:33], v[162:165], v[210:213], v[30:33]
	v_mfma_f32_16x16x32_f16 v[26:29], v[170:173], v[210:213], v[26:29]
	v_mfma_f32_16x16x32_f16 v[14:17], v[162:165], v[218:221], v[14:17]
	v_mfma_f32_16x16x32_f16 v[10:13], v[170:173], v[218:221], v[10:13]
	s_setprio 0
	s_setprio 1
	v_mfma_f32_16x16x32_f16 v[54:57], v[174:177], v[190:193], v[54:57]
	v_mfma_f32_16x16x32_f16 v[50:53], v[182:185], v[190:193], v[50:53]
	v_mfma_f32_16x16x32_f16 v[38:41], v[174:177], v[198:201], v[38:41]
	v_mfma_f32_16x16x32_f16 v[34:37], v[182:185], v[198:201], v[34:37]
	v_mfma_f32_16x16x32_f16 v[22:25], v[174:177], v[206:209], v[22:25]
	v_mfma_f32_16x16x32_f16 v[18:21], v[182:185], v[206:209], v[18:21]
	v_mfma_f32_16x16x32_f16 v[6:9], v[174:177], v[214:217], v[6:9]
	v_mfma_f32_16x16x32_f16 v[2:5], v[182:185], v[214:217], v[2:5]
	v_mfma_f32_16x16x32_f16 v[54:57], v[178:181], v[194:197], v[54:57]
	v_mfma_f32_16x16x32_f16 v[50:53], v[186:189], v[194:197], v[50:53]
	v_mfma_f32_16x16x32_f16 v[38:41], v[178:181], v[202:205], v[38:41]
	v_mfma_f32_16x16x32_f16 v[34:37], v[186:189], v[202:205], v[34:37]
	v_mfma_f32_16x16x32_f16 v[22:25], v[178:181], v[210:213], v[22:25]
	v_mfma_f32_16x16x32_f16 v[18:21], v[186:189], v[210:213], v[18:21]
	v_mfma_f32_16x16x32_f16 v[6:9], v[178:181], v[218:221], v[6:9]
	v_mfma_f32_16x16x32_f16 v[2:5], v[186:189], v[218:221], v[2:5]
	s_setprio 0
	s_barrier
	s_add_u32 s30, s30, 0x40000
	s_addc_u32 s31, s31, 0
	s_mov_b32 m0, s37
	v_lshl_add_u64 v[228:229], s[30:31], 0, v[130:131]
	global_load_lds_dwordx4 v[228:229], off
	v_lshl_add_u64 v[228:229], s[30:31], 0, v[134:135]
	s_mov_b32 m0, s38
	s_nop 0
	global_load_lds_dwordx4 v[228:229], off
	s_mov_b32 s53, 0x1c000
	s_mov_b32 s52, 0x18000
	v_add_u32_e32 v244, s52, v153
	v_add_u32_e32 v245, s53, v153
	ds_read_b128 v[146:149], v244
	ds_read_b128 v[162:165], v244 offset:1024
	ds_read_b128 v[166:169], v244 offset:2048
	ds_read_b128 v[170:173], v244 offset:3072
	ds_read_b128 v[174:177], v245
	ds_read_b128 v[178:181], v245 offset:1024
	ds_read_b128 v[182:185], v245 offset:2048
	ds_read_b128 v[186:189], v245 offset:3072
	ds_read_b128 v[190:193], v160 offset:32768
	ds_read_b128 v[194:197], v160 offset:33792
	ds_read_b128 v[198:201], v160 offset:34816
	ds_read_b128 v[202:205], v160 offset:35840
	ds_read_b128 v[206:209], v160 offset:36864
	ds_read_b128 v[210:213], v160 offset:37888
	ds_read_b128 v[214:217], v160 offset:38912
	ds_read_b128 v[218:221], v160 offset:39936
	s_waitcnt vmcnt(8)
	s_waitcnt lgkmcnt(0)
	s_barrier
	s_setprio 1
	s_waitcnt lgkmcnt(0)
	v_mfma_f32_16x16x32_f16 v[126:129], v[146:149], v[190:193], v[126:129]
	v_mfma_f32_16x16x32_f16 v[122:125], v[166:169], v[190:193], v[122:125]
	v_mfma_f32_16x16x32_f16 v[110:113], v[146:149], v[198:201], v[110:113]
	v_mfma_f32_16x16x32_f16 v[106:109], v[166:169], v[198:201], v[106:109]
	v_mfma_f32_16x16x32_f16 v[94:97], v[146:149], v[206:209], v[94:97]
	v_mfma_f32_16x16x32_f16 v[90:93], v[166:169], v[206:209], v[90:93]
	v_mfma_f32_16x16x32_f16 v[78:81], v[146:149], v[214:217], v[78:81]
	v_mfma_f32_16x16x32_f16 v[74:77], v[166:169], v[214:217], v[74:77]
	v_mfma_f32_16x16x32_f16 v[126:129], v[162:165], v[194:197], v[126:129]
	v_mfma_f32_16x16x32_f16 v[122:125], v[170:173], v[194:197], v[122:125]
	v_mfma_f32_16x16x32_f16 v[110:113], v[162:165], v[202:205], v[110:113]
	v_mfma_f32_16x16x32_f16 v[106:109], v[170:173], v[202:205], v[106:109]
	v_mfma_f32_16x16x32_f16 v[94:97], v[162:165], v[210:213], v[94:97]
	v_mfma_f32_16x16x32_f16 v[90:93], v[170:173], v[210:213], v[90:93]
	v_mfma_f32_16x16x32_f16 v[78:81], v[162:165], v[218:221], v[78:81]
	v_mfma_f32_16x16x32_f16 v[74:77], v[170:173], v[218:221], v[74:77]
	s_setprio 0
	s_setprio 1
	v_mfma_f32_16x16x32_f16 v[118:121], v[174:177], v[190:193], v[118:121]
	v_mfma_f32_16x16x32_f16 v[114:117], v[182:185], v[190:193], v[114:117]
	v_mfma_f32_16x16x32_f16 v[102:105], v[174:177], v[198:201], v[102:105]
	v_mfma_f32_16x16x32_f16 v[98:101], v[182:185], v[198:201], v[98:101]
	v_mfma_f32_16x16x32_f16 v[86:89], v[174:177], v[206:209], v[86:89]
	v_mfma_f32_16x16x32_f16 v[82:85], v[182:185], v[206:209], v[82:85]
	v_mfma_f32_16x16x32_f16 v[70:73], v[174:177], v[214:217], v[70:73]
	v_mfma_f32_16x16x32_f16 v[66:69], v[182:185], v[214:217], v[66:69]
	v_mfma_f32_16x16x32_f16 v[118:121], v[178:181], v[194:197], v[118:121]
	v_mfma_f32_16x16x32_f16 v[114:117], v[186:189], v[194:197], v[114:117]
	v_mfma_f32_16x16x32_f16 v[102:105], v[178:181], v[202:205], v[102:105]
	v_mfma_f32_16x16x32_f16 v[98:101], v[186:189], v[202:205], v[98:101]
	v_mfma_f32_16x16x32_f16 v[86:89], v[178:181], v[210:213], v[86:89]
	v_mfma_f32_16x16x32_f16 v[82:85], v[186:189], v[210:213], v[82:85]
	v_mfma_f32_16x16x32_f16 v[70:73], v[178:181], v[218:221], v[70:73]
	v_mfma_f32_16x16x32_f16 v[66:69], v[186:189], v[218:221], v[66:69]
	s_setprio 0
	s_barrier
; #define GM_STAGE(bufoff, gbase, voff) do { _Pragma("unroll") for (int _i = 0; _i < 2; ++_i) \
;         __builtin_amdgcn_global_load_lds((const unsigned*)((const char*)(gbase) + (voff)[_i]), (LAS unsigned*)(lds + (bufoff) + ldsw + _i * 8192), 16, 0, 0); } while (0)
; #define GM_LDA(dst, b, h) do { _Pragma("unroll") for (int m = 0; m < 4; ++m) _Pragma("unroll") for (int k = 0; k < 2; ++k) dst[m][k] = *(const LAS s16x8*)(lds + GM_SA(b, h) + aoff + m * 2048 + k * 1024); } while (0)
; #define GM_MMA(ai, bj, At, Bt) do { __builtin_amdgcn_s_setprio(1); _Pragma("unroll") for (int m = 0; m < 4; ++m) _Pragma("unroll") for (int n = 0; n < 2; ++n) _Pragma("unroll") for (int k = 0; k < 2; ++k) \
;         acc[ai][bj][m][n] = mma16<BF>(Bt[n][k], At[m][k], acc[ai][bj][m][n]); __builtin_amdgcn_s_setprio(0); } while (0)
; #define GM_WAIT_V(n) asm volatile("s_waitcnt vmcnt(" #n ")" ::: "memory")
; #define GM_WAIT_L(n) asm volatile("s_waitcnt lgkmcnt(" #n ")" ::: "memory")
; #define GM_BAR __builtin_amdgcn_s_barrier()
; #define GM_SCHED __builtin_amdgcn_sched_barrier(0)
; #define GM_STA_H0(buf, p, o0) do { if constexpr (GATHER) GM_STAGE(buf, p, o0); else GM_STAGE(buf, p, voffA); } while (0)
; template <bool BF, bool GATHER = false, class Epi, class Hook>
; __device__ __forceinline__ void gemm_phase(LAS unsigned char* lds, const Gemm g, const Order& S, const Epi& E, Hook& HK) {
;     ...
;             GM_LDA(At, 1, 1); GM_STAGE(GM_SB(1, 0), b3, voffB); GM_STAGE(GM_SB(1, 1), b3 + hstepB, voffB); GM_STA_H0(GM_SA(1, 0), a3, s0);
;             GM_WAIT_V(8); GM_WAIT_L(0); GM_BAR; GM_MMA(1, 0, At, B0); GM_MMA(1, 1, At, B1); GM_BAR; GM_SCHED;
;         }
;         if (wr == 0) GM_BAR;
	s_add_i32 s30, s52, s35
	v_lshl_add_u64 v[150:151], v[150:151], 0, s[14:15]
	s_mov_b32 m0, s30
	global_load_lds_dwordx4 v[150:151], off
	s_add_i32 m0, s30, 0x2000
	s_add_u32 s28, s28, 0x40080
	v_lshl_add_u64 v[150:151], v[222:223], 0, s[14:15]
	s_addc_u32 s29, s29, 0
	s_add_i32 s30, s53, s35
	global_load_lds_dwordx4 v[150:151], off
	v_lshl_add_u64 v[150:151], s[28:29], 0, v[132:133]
	s_mov_b32 m0, s30
	s_nop 0
	global_load_lds_dwordx4 v[150:151], off
	v_lshl_add_u64 v[150:151], s[28:29], 0, v[136:137]
	s_add_i32 m0, s30, 0x2000
	s_nop 0
	global_load_lds_dwordx4 v[150:151], off
	v_lshl_add_u64 v[150:151], v[224:225], 0, s[14:15]
	s_mov_b32 m0, s42
	s_nop 0
	global_load_lds_dwordx4 v[150:151], off
	v_lshl_add_u64 v[150:151], v[226:227], 0, s[14:15]
	s_mov_b32 m0, s43
	s_nop 0
	global_load_lds_dwordx4 v[150:151], off
	ds_read_b128 v[190:193], v160 offset:49152
	ds_read_b128 v[194:197], v160 offset:50176
	ds_read_b128 v[198:201], v160 offset:51200
	ds_read_b128 v[202:205], v160 offset:52224
	ds_read_b128 v[206:209], v160 offset:53248
	ds_read_b128 v[210:213], v160 offset:54272
	ds_read_b128 v[214:217], v160 offset:55296
	ds_read_b128 v[218:221], v160 offset:56320
	s_waitcnt vmcnt(8)
	s_waitcnt lgkmcnt(0)
	s_barrier
	s_setprio 1
	s_waitcnt lgkmcnt(0)
	v_mfma_f32_16x16x32_f16 v[62:65], v[146:149], v[190:193], v[62:65]
	v_mfma_f32_16x16x32_f16 v[58:61], v[166:169], v[190:193], v[58:61]
	v_mfma_f32_16x16x32_f16 v[46:49], v[146:149], v[198:201], v[46:49]
	v_mfma_f32_16x16x32_f16 v[42:45], v[166:169], v[198:201], v[42:45]
	v_mfma_f32_16x16x32_f16 v[30:33], v[146:149], v[206:209], v[30:33]
	v_mfma_f32_16x16x32_f16 v[26:29], v[166:169], v[206:209], v[26:29]
	v_mfma_f32_16x16x32_f16 v[14:17], v[146:149], v[214:217], v[14:17]
	v_mfma_f32_16x16x32_f16 v[10:13], v[166:169], v[214:217], v[10:13]
	v_mfma_f32_16x16x32_f16 v[62:65], v[162:165], v[194:197], v[62:65]
	v_mfma_f32_16x16x32_f16 v[58:61], v[170:173], v[194:197], v[58:61]
	v_mfma_f32_16x16x32_f16 v[46:49], v[162:165], v[202:205], v[46:49]
	v_mfma_f32_16x16x32_f16 v[42:45], v[170:173], v[202:205], v[42:45]
	v_mfma_f32_16x16x32_f16 v[30:33], v[162:165], v[210:213], v[30:33]
	v_mfma_f32_16x16x32_f16 v[26:29], v[170:173], v[210:213], v[26:29]
	v_mfma_f32_16x16x32_f16 v[14:17], v[162:165], v[218:221], v[14:17]
	v_mfma_f32_16x16x32_f16 v[10:13], v[170:173], v[218:221], v[10:13]
	s_setprio 0
	s_setprio 1
	v_mfma_f32_16x16x32_f16 v[54:57], v[174:177], v[190:193], v[54:57]
	v_mfma_f32_16x16x32_f16 v[50:53], v[182:185], v[190:193], v[50:53]
	v_mfma_f32_16x16x32_f16 v[38:41], v[174:177], v[198:201], v[38:41]
	v_mfma_f32_16x16x32_f16 v[34:37], v[182:185], v[198:201], v[34:37]
	v_mfma_f32_16x16x32_f16 v[22:25], v[174:177], v[206:209], v[22:25]
	v_mfma_f32_16x16x32_f16 v[18:21], v[182:185], v[206:209], v[18:21]
	v_mfma_f32_16x16x32_f16 v[6:9], v[174:177], v[214:217], v[6:9]
	v_mfma_f32_16x16x32_f16 v[2:5], v[182:185], v[214:217], v[2:5]
	v_mfma_f32_16x16x32_f16 v[54:57], v[178:181], v[194:197], v[54:57]
	v_mfma_f32_16x16x32_f16 v[50:53], v[186:189], v[194:197], v[50:53]
	v_mfma_f32_16x16x32_f16 v[38:41], v[178:181], v[202:205], v[38:41]
	v_mfma_f32_16x16x32_f16 v[34:37], v[186:189], v[202:205], v[34:37]
	v_mfma_f32_16x16x32_f16 v[22:25], v[178:181], v[210:213], v[22:25]
	v_mfma_f32_16x16x32_f16 v[18:21], v[186:189], v[210:213], v[18:21]
	v_mfma_f32_16x16x32_f16 v[6:9], v[178:181], v[218:221], v[6:9]
	v_mfma_f32_16x16x32_f16 v[2:5], v[186:189], v[218:221], v[2:5]
	s_setprio 0
	s_barrier
	s_add_i32 s51, s51, 2
	s_add_u32 s2, s2, 0x100
	s_addc_u32 s3, s3, 0
	s_add_u32 s49, s49, 0x100
	s_addc_u32 s50, s50, 0
	s_cmp_gt_u32 s51, 13
	s_cbranch_scc0 .LBB0_380
	s_and_b64 vcc, exec, s[16:17]
	s_cbranch_vccz .LBB0_383
	s_barrier

; #define GM_STAGE(bufoff, gbase, voff) do { _Pragma("unroll") for (int _i = 0; _i < 2; ++_i) \
;         __builtin_amdgcn_global_load_lds((const unsigned*)((const char*)(gbase) + (voff)[_i]), (LAS unsigned*)(lds + (bufoff) + ldsw + _i * 8192), 16, 0, 0); } while (0)
; #define GM_LDA(dst, b, h) do { _Pragma("unroll") for (int m = 0; m < 4; ++m) _Pragma("unroll") for (int k = 0; k < 2; ++k) dst[m][k] = *(const LAS s16x8*)(lds + GM_SA(b, h) + aoff + m * 2048 + k * 1024); } while (0)
; #define GM_LDB(dst, b, h) do { _Pragma("unroll") for (int n = 0; n < 2; ++n) _Pragma("unroll") for (int k = 0; k < 2; ++k) dst[n][k] = *(const LAS s16x8*)(lds + GM_SB(b, h) + boff + n * 2048 + k * 1024); } while (0)
; #define GM_MMA(ai, bj, At, Bt) do { __builtin_amdgcn_s_setprio(1); _Pragma("unroll") for (int m = 0; m < 4; ++m) _Pragma("unroll") for (int n = 0; n < 2; ++n) _Pragma("unroll") for (int k = 0; k < 2; ++k) \
;         acc[ai][bj][m][n] = mma16<BF>(Bt[n][k], At[m][k], acc[ai][bj][m][n]); __builtin_amdgcn_s_setprio(0); } while (0)
; #define GM_WAIT_V(n) asm volatile("s_waitcnt vmcnt(" #n ")" ::: "memory")
; #define GM_BAR __builtin_amdgcn_s_barrier()
; template <bool BF, bool GATHER = false, class Epi, class Hook>
; __device__ __forceinline__ void gemm_phase(LAS unsigned char* lds, const Gemm g, const Order& S, const Epi& E, Hook& HK) {
;     ...
;         for (int t = 0; t < nt; t += 2) {
;             const bool last = (t == nt - 2);
;             const char* a1 = cA + (size_t)(t + 1) * kstep;
;             const char* a2 = last ? nA : cA + (size_t)(t + 2) * kstep; const char* b2 = last ? nB : cB + (size_t)(t + 2) * kstep;
;             const char* a3 = a2 + kstep; const char* b3 = b2 + kstep;
;             unsigned s0[2], s1[2];
;             if constexpr (GATHER) { s0[0] = last ? nA0[0] : gA0[0]; s0[1] = last ? nA0[1] : gA0[1]; s1[0] = last ? nA1[0] : gA1[0]; s1[1] = last ? nA1[1] : gA1[1]; }
;             GM_LDB(B0, 0, 0); GM_LDB(B1, 0, 1); GM_SCHED; GM_LDA(At, 0, 0); GM_STA_H1(GM_SA(1, 1), a1, gA1);
;             GM_WAIT_V(8); GM_WAIT_L(0); GM_BAR; GM_MMA(0, 0, At, B0); GM_MMA(0, 1, At, B1); GM_BAR; GM_SCHED;
;             GM_LDA(At, 0, 1); GM_STAGE(GM_SB(0, 0), b2, voffB); GM_STAGE(GM_SB(0, 1), b2 + hstepB, voffB); GM_STA_H0(GM_SA(0, 0), a2, s0);
;             GM_WAIT_V(8); GM_WAIT_L(0); GM_BAR; GM_MMA(1, 0, At, B0); GM_MMA(1, 1, At, B1); GM_BAR; GM_SCHED;
.LBB0_715:
	s_add_u32 s22, s20, 0xfffc0080
	s_addc_u32 s23, s21, -1
	s_cmp_eq_u32 s47, 12
	s_cselect_b32 s25, s13, s23
	s_cselect_b32 s24, s43, s22
	s_cselect_b32 s23, s15, s46
	s_cselect_b32 s22, s44, s45
	v_lshl_add_u64 v[216:217], s[20:21], 0, v[154:155]
	s_add_i32 m0, s30, 0xc000
	global_load_lds_dwordx4 v[216:217], off
	v_lshl_add_u64 v[216:217], s[20:21], 0, v[156:157]
	s_add_i32 m0, s30, 0xe000
	s_nop 0
	global_load_lds_dwordx4 v[216:217], off
	ds_read_b128 v[130:133], v168
	ds_read_b128 v[134:137], v168 offset:1024
	ds_read_b128 v[138:141], v168 offset:2048
	ds_read_b128 v[142:145], v168 offset:3072
	ds_read_b128 v[162:165], v169
	ds_read_b128 v[172:175], v169 offset:1024
	ds_read_b128 v[176:179], v169 offset:2048
	ds_read_b128 v[180:183], v169 offset:3072
	ds_read_b128 v[184:187], v170
	ds_read_b128 v[188:191], v170 offset:1024
	ds_read_b128 v[192:195], v170 offset:2048
	ds_read_b128 v[196:199], v170 offset:3072
	ds_read_b128 v[200:203], v170 offset:4096
	ds_read_b128 v[204:207], v170 offset:5120
	ds_read_b128 v[208:211], v170 offset:6144
	ds_read_b128 v[212:215], v170 offset:7168
	s_waitcnt vmcnt(8)
	s_waitcnt lgkmcnt(0)
	s_barrier
	s_setprio 1
	s_waitcnt lgkmcnt(0)
	v_mfma_f32_16x16x32_f16 v[126:129], v[130:133], v[184:187], v[126:129]
	v_mfma_f32_16x16x32_f16 v[122:125], v[138:141], v[184:187], v[122:125]
	v_mfma_f32_16x16x32_f16 v[110:113], v[130:133], v[192:195], v[110:113]
	v_mfma_f32_16x16x32_f16 v[106:109], v[138:141], v[192:195], v[106:109]
	v_mfma_f32_16x16x32_f16 v[94:97], v[130:133], v[200:203], v[94:97]
	v_mfma_f32_16x16x32_f16 v[90:93], v[138:141], v[200:203], v[90:93]
	v_mfma_f32_16x16x32_f16 v[78:81], v[130:133], v[208:211], v[78:81]
	v_mfma_f32_16x16x32_f16 v[74:77], v[138:141], v[208:211], v[74:77]
	v_mfma_f32_16x16x32_f16 v[126:129], v[134:137], v[188:191], v[126:129]
	v_mfma_f32_16x16x32_f16 v[122:125], v[142:145], v[188:191], v[122:125]
	v_mfma_f32_16x16x32_f16 v[110:113], v[134:137], v[196:199], v[110:113]
	v_mfma_f32_16x16x32_f16 v[106:109], v[142:145], v[196:199], v[106:109]
	v_mfma_f32_16x16x32_f16 v[94:97], v[134:137], v[204:207], v[94:97]
	v_mfma_f32_16x16x32_f16 v[90:93], v[142:145], v[204:207], v[90:93]
	v_mfma_f32_16x16x32_f16 v[78:81], v[134:137], v[212:215], v[78:81]
	v_mfma_f32_16x16x32_f16 v[74:77], v[142:145], v[212:215], v[74:77]
	s_setprio 0
	s_setprio 1
	v_mfma_f32_16x16x32_f16 v[118:121], v[162:165], v[184:187], v[118:121]
	v_mfma_f32_16x16x32_f16 v[114:117], v[176:179], v[184:187], v[114:117]
	v_mfma_f32_16x16x32_f16 v[102:105], v[162:165], v[192:195], v[102:105]
	v_mfma_f32_16x16x32_f16 v[98:101], v[176:179], v[192:195], v[98:101]
	v_mfma_f32_16x16x32_f16 v[86:89], v[162:165], v[200:203], v[86:89]
	v_mfma_f32_16x16x32_f16 v[82:85], v[176:179], v[200:203], v[82:85]
	v_mfma_f32_16x16x32_f16 v[70:73], v[162:165], v[208:211], v[70:73]
	v_mfma_f32_16x16x32_f16 v[66:69], v[176:179], v[208:211], v[66:69]
	v_mfma_f32_16x16x32_f16 v[118:121], v[172:175], v[188:191], v[118:121]
	v_mfma_f32_16x16x32_f16 v[114:117], v[180:183], v[188:191], v[114:117]
	v_mfma_f32_16x16x32_f16 v[102:105], v[172:175], v[196:199], v[102:105]
	v_mfma_f32_16x16x32_f16 v[98:101], v[180:183], v[196:199], v[98:101]
	v_mfma_f32_16x16x32_f16 v[86:89], v[172:175], v[204:207], v[86:89]
	v_mfma_f32_16x16x32_f16 v[82:85], v[180:183], v[204:207], v[82:85]
	v_mfma_f32_16x16x32_f16 v[70:73], v[172:175], v[212:215], v[70:73]
	v_mfma_f32_16x16x32_f16 v[66:69], v[180:183], v[212:215], v[66:69]
	s_setprio 0
	s_barrier
	s_add_i32 s48, s41, s29
	v_lshl_add_u64 v[216:217], s[22:23], 0, v[148:149]
	s_mov_b32 m0, s48
	global_load_lds_dwordx4 v[216:217], off
	s_add_i32 m0, s48, 0x2000
	s_add_u32 s48, s22, 0x40000
	v_lshl_add_u64 v[218:219], s[22:23], 0, v[152:153]
	s_addc_u32 s49, s23, 0
	s_add_i32 s50, s42, s29
	global_load_lds_dwordx4 v[218:219], off
	v_lshl_add_u64 v[220:221], s[48:49], 0, v[148:149]
	s_mov_b32 m0, s50
	v_lshl_add_u64 v[222:223], s[24:25], 0, v[150:151]
	global_load_lds_dwordx4 v[220:221], off
	v_lshl_add_u64 v[220:221], s[48:49], 0, v[152:153]
	s_add_i32 m0, s50, 0x2000
	s_nop 0
	global_load_lds_dwordx4 v[220:221], off
	v_lshl_add_u64 v[220:221], s[24:25], 0, v[146:147]
	s_mov_b32 m0, s30
	s_nop 0
	global_load_lds_dwordx4 v[220:221], off
	s_mov_b32 m0, s31
	s_nop 0
	global_load_lds_dwordx4 v[222:223], off
	ds_read_b128 v[184:187], v170 offset:16384
	ds_read_b128 v[188:191], v170 offset:17408
	ds_read_b128 v[192:195], v170 offset:18432
	ds_read_b128 v[196:199], v170 offset:19456
	ds_read_b128 v[200:203], v170 offset:20480
	ds_read_b128 v[204:207], v170 offset:21504
	ds_read_b128 v[208:211], v170 offset:22528
	ds_read_b128 v[212:215], v170 offset:23552
	s_waitcnt vmcnt(8)
	s_waitcnt lgkmcnt(0)
	s_barrier
; #define GM_LDA(dst, b, h) do { _Pragma("unroll") for (int m = 0; m < 4; ++m) _Pragma("unroll") for (int k = 0; k < 2; ++k) dst[m][k] = *(const LAS s16x8*)(lds + GM_SA(b, h) + aoff + m * 2048 + k * 1024); } while (0)
; #define GM_LDB(dst, b, h) do { _Pragma("unroll") for (int n = 0; n < 2; ++n) _Pragma("unroll") for (int k = 0; k < 2; ++k) dst[n][k] = *(const LAS s16x8*)(lds + GM_SB(b, h) + boff + n * 2048 + k * 1024); } while (0)
; #define GM_MMA(ai, bj, At, Bt) do { __builtin_amdgcn_s_setprio(1); _Pragma("unroll") for (int m = 0; m < 4; ++m) _Pragma("unroll") for (int n = 0; n < 2; ++n) _Pragma("unroll") for (int k = 0; k < 2; ++k) \
;         acc[ai][bj][m][n] = mma16<BF>(Bt[n][k], At[m][k], acc[ai][bj][m][n]); __builtin_amdgcn_s_setprio(0); } while (0)
; #define GM_WAIT_V(n) asm volatile("s_waitcnt vmcnt(" #n ")" ::: "memory")
; #define GM_WAIT_L(n) asm volatile("s_waitcnt lgkmcnt(" #n ")" ::: "memory")
; #define GM_BAR __builtin_amdgcn_s_barrier()
; #define GM_SCHED __builtin_amdgcn_sched_barrier(0)
; #define GM_STA_H1(buf, p, o1) do { if constexpr (GATHER) GM_STAGE(buf, p, o1); else GM_STAGE(buf, (p) + hstepB, voffA); } while (0)
; template <bool BF, bool GATHER = false, class Epi, class Hook>
; __device__ __forceinline__ void gemm_phase(LAS unsigned char* lds, const Gemm g, const Order& S, const Epi& E, Hook& HK) {
;     ...
;             GM_WAIT_V(8); GM_WAIT_L(0); GM_BAR; GM_MMA(1, 0, At, B0); GM_MMA(1, 1, At, B1); GM_BAR; GM_SCHED;
;             GM_LDB(B0, 1, 0); GM_LDB(B1, 1, 1); GM_SCHED; GM_LDA(At, 1, 0); GM_STA_H1(GM_SA(0, 1), a2, s1);
;             GM_WAIT_V(8); GM_WAIT_L(0); GM_BAR; GM_MMA(0, 0, At, B0); GM_MMA(0, 1, At, B1); GM_BAR; GM_SCHED;
	s_setprio 1
	s_waitcnt lgkmcnt(0)
	v_mfma_f32_16x16x32_f16 v[62:65], v[130:133], v[184:187], v[62:65]
	v_mfma_f32_16x16x32_f16 v[58:61], v[138:141], v[184:187], v[58:61]
	v_mfma_f32_16x16x32_f16 v[46:49], v[130:133], v[192:195], v[46:49]
	v_mfma_f32_16x16x32_f16 v[42:45], v[138:141], v[192:195], v[42:45]
	v_mfma_f32_16x16x32_f16 v[30:33], v[130:133], v[200:203], v[30:33]
	v_mfma_f32_16x16x32_f16 v[26:29], v[138:141], v[200:203], v[26:29]
	v_mfma_f32_16x16x32_f16 v[14:17], v[130:133], v[208:211], v[14:17]
	v_mfma_f32_16x16x32_f16 v[10:13], v[138:141], v[208:211], v[10:13]
	v_mfma_f32_16x16x32_f16 v[62:65], v[134:137], v[188:191], v[62:65]
	v_mfma_f32_16x16x32_f16 v[58:61], v[142:145], v[188:191], v[58:61]
	v_mfma_f32_16x16x32_f16 v[46:49], v[134:137], v[196:199], v[46:49]
	v_mfma_f32_16x16x32_f16 v[42:45], v[142:145], v[196:199], v[42:45]
	v_mfma_f32_16x16x32_f16 v[30:33], v[134:137], v[204:207], v[30:33]
	v_mfma_f32_16x16x32_f16 v[26:29], v[142:145], v[204:207], v[26:29]
	v_mfma_f32_16x16x32_f16 v[14:17], v[134:137], v[212:215], v[14:17]
	v_mfma_f32_16x16x32_f16 v[10:13], v[142:145], v[212:215], v[10:13]
	s_setprio 0
	s_setprio 1
	v_mfma_f32_16x16x32_f16 v[54:57], v[162:165], v[184:187], v[54:57]
	v_mfma_f32_16x16x32_f16 v[50:53], v[176:179], v[184:187], v[50:53]
	v_mfma_f32_16x16x32_f16 v[38:41], v[162:165], v[192:195], v[38:41]
	v_mfma_f32_16x16x32_f16 v[34:37], v[176:179], v[192:195], v[34:37]
	v_mfma_f32_16x16x32_f16 v[22:25], v[162:165], v[200:203], v[22:25]
	v_mfma_f32_16x16x32_f16 v[18:21], v[176:179], v[200:203], v[18:21]
	v_mfma_f32_16x16x32_f16 v[6:9], v[162:165], v[208:211], v[6:9]
	v_mfma_f32_16x16x32_f16 v[2:5], v[176:179], v[208:211], v[2:5]
	v_mfma_f32_16x16x32_f16 v[54:57], v[172:175], v[188:191], v[54:57]
	v_mfma_f32_16x16x32_f16 v[50:53], v[180:183], v[188:191], v[50:53]
	v_mfma_f32_16x16x32_f16 v[38:41], v[172:175], v[196:199], v[38:41]
	v_mfma_f32_16x16x32_f16 v[34:37], v[180:183], v[196:199], v[34:37]
	v_mfma_f32_16x16x32_f16 v[22:25], v[172:175], v[204:207], v[22:25]
	v_mfma_f32_16x16x32_f16 v[18:21], v[180:183], v[204:207], v[18:21]
	v_mfma_f32_16x16x32_f16 v[6:9], v[172:175], v[212:215], v[6:9]
	v_mfma_f32_16x16x32_f16 v[2:5], v[180:183], v[212:215], v[2:5]
	s_setprio 0
	s_barrier
	s_add_u32 s24, s24, 0x40000
	s_addc_u32 s25, s25, 0
	s_mov_b32 m0, s33
	v_lshl_add_u64 v[224:225], s[24:25], 0, v[146:147]
	global_load_lds_dwordx4 v[224:225], off
	v_lshl_add_u64 v[224:225], s[24:25], 0, v[150:151]
	s_mov_b32 m0, s34
	s_nop 0
	global_load_lds_dwordx4 v[224:225], off
	s_mov_b32 s49, 0x1c000
	s_mov_b32 s48, 0x18000
	v_add_u32_e32 v244, s48, v166
	v_add_u32_e32 v245, s49, v166
	ds_read_b128 v[130:133], v244
	ds_read_b128 v[134:137], v244 offset:1024
	ds_read_b128 v[138:141], v244 offset:2048
	ds_read_b128 v[142:145], v244 offset:3072
	ds_read_b128 v[162:165], v245
	ds_read_b128 v[172:175], v245 offset:1024
	ds_read_b128 v[176:179], v245 offset:2048
	ds_read_b128 v[180:183], v245 offset:3072
	ds_read_b128 v[184:187], v170 offset:32768
	ds_read_b128 v[188:191], v170 offset:33792
	ds_read_b128 v[192:195], v170 offset:34816
	ds_read_b128 v[196:199], v170 offset:35840
	ds_read_b128 v[200:203], v170 offset:36864
	ds_read_b128 v[204:207], v170 offset:37888
	ds_read_b128 v[208:211], v170 offset:38912
	ds_read_b128 v[212:215], v170 offset:39936
	s_waitcnt vmcnt(8)
	s_waitcnt lgkmcnt(0)
	s_barrier
	s_setprio 1
	s_waitcnt lgkmcnt(0)
	v_mfma_f32_16x16x32_f16 v[126:129], v[130:133], v[184:187], v[126:129]
	v_mfma_f32_16x16x32_f16 v[122:125], v[138:141], v[184:187], v[122:125]
	v_mfma_f32_16x16x32_f16 v[110:113], v[130:133], v[192:195], v[110:113]
	v_mfma_f32_16x16x32_f16 v[106:109], v[138:141], v[192:195], v[106:109]
	v_mfma_f32_16x16x32_f16 v[94:97], v[130:133], v[200:203], v[94:97]
	v_mfma_f32_16x16x32_f16 v[90:93], v[138:141], v[200:203], v[90:93]
	v_mfma_f32_16x16x32_f16 v[78:81], v[130:133], v[208:211], v[78:81]
	v_mfma_f32_16x16x32_f16 v[74:77], v[138:141], v[208:211], v[74:77]
	v_mfma_f32_16x16x32_f16 v[126:129], v[134:137], v[188:191], v[126:129]
	v_mfma_f32_16x16x32_f16 v[122:125], v[142:145], v[188:191], v[122:125]
	v_mfma_f32_16x16x32_f16 v[110:113], v[134:137], v[196:199], v[110:113]
	v_mfma_f32_16x16x32_f16 v[106:109], v[142:145], v[196:199], v[106:109]
	v_mfma_f32_16x16x32_f16 v[94:97], v[134:137], v[204:207], v[94:97]
	v_mfma_f32_16x16x32_f16 v[90:93], v[142:145], v[204:207], v[90:93]
	v_mfma_f32_16x16x32_f16 v[78:81], v[134:137], v[212:215], v[78:81]
	v_mfma_f32_16x16x32_f16 v[74:77], v[142:145], v[212:215], v[74:77]
	s_setprio 0
	s_setprio 1
	v_mfma_f32_16x16x32_f16 v[118:121], v[162:165], v[184:187], v[118:121]
	v_mfma_f32_16x16x32_f16 v[114:117], v[176:179], v[184:187], v[114:117]
	v_mfma_f32_16x16x32_f16 v[102:105], v[162:165], v[192:195], v[102:105]
	v_mfma_f32_16x16x32_f16 v[98:101], v[176:179], v[192:195], v[98:101]
	v_mfma_f32_16x16x32_f16 v[86:89], v[162:165], v[200:203], v[86:89]
	v_mfma_f32_16x16x32_f16 v[82:85], v[176:179], v[200:203], v[82:85]
	v_mfma_f32_16x16x32_f16 v[70:73], v[162:165], v[208:211], v[70:73]
	v_mfma_f32_16x16x32_f16 v[66:69], v[176:179], v[208:211], v[66:69]
	v_mfma_f32_16x16x32_f16 v[118:121], v[172:175], v[188:191], v[118:121]
	v_mfma_f32_16x16x32_f16 v[114:117], v[180:183], v[188:191], v[114:117]
	v_mfma_f32_16x16x32_f16 v[102:105], v[172:175], v[196:199], v[102:105]
	v_mfma_f32_16x16x32_f16 v[98:101], v[180:183], v[196:199], v[98:101]
	v_mfma_f32_16x16x32_f16 v[86:89], v[172:175], v[204:207], v[86:89]
	v_mfma_f32_16x16x32_f16 v[82:85], v[180:183], v[204:207], v[82:85]
	v_mfma_f32_16x16x32_f16 v[70:73], v[172:175], v[212:215], v[70:73]
	v_mfma_f32_16x16x32_f16 v[66:69], v[180:183], v[212:215], v[66:69]
	s_setprio 0
	s_barrier
; #define GM_STAGE(bufoff, gbase, voff) do { _Pragma("unroll") for (int _i = 0; _i < 2; ++_i) \
;         __builtin_amdgcn_global_load_lds((const unsigned*)((const char*)(gbase) + (voff)[_i]), (LAS unsigned*)(lds + (bufoff) + ldsw + _i * 8192), 16, 0, 0); } while (0)
; #define GM_WAIT_V(n) asm volatile("s_waitcnt vmcnt(" #n ")" ::: "memory")
; #define GM_WAIT_L(n) asm volatile("s_waitcnt lgkmcnt(" #n ")" ::: "memory")
;     __device__ __forceinline__ void operator()(const Acc& acc, const Unit& u, int wr, int wc, int fr, int fq) const {
;         const int col0 = u.pn * BM + wc * 32 + 8 * fq; const int b = (u.pm * BM) / SEQ;
;         f32x4 gv[2][2];
; #pragma unroll
;         for (int bj = 0; bj < 2; ++bj)
; #pragma unroll
;             for (int n = 0; n < 2; ++n) gv[bj][n] = *(const f32x4*)(gate + (size_t)b * gstride + col0 + bj * HALF + 4 * n);
; #pragma unroll
;         for (int ai = 0; ai < 2; ++ai)
; #pragma unroll
;             for (int m = 0; m < 4; ++m) { const size_t off = (size_t)(u.pm * BM + ai * HALF + wr * 64 + m * 16 + fr) * DM + col0;
; #pragma unroll
;                 for (int bj = 0; bj < 2; ++bj) { f32x4 b0, b1;
;                     if constexpr (BASE16) { const f16x8 bv = *(const f16x8*)((const f16*)base + off + bj * HALF);
;                         b0 = (f32x4){(float)bv[0], (float)bv[1], (float)bv[2], (float)bv[3]}; b1 = (f32x4){(float)bv[4], (float)bv[5], (float)bv[6], (float)bv[7]}; }
;                     else { b0 = *(const f32x4*)((const float*)base + off + bj * HALF); b1 = *(const f32x4*)((const float*)base + off + bj * HALF + 4); }
;                     const f32x4 v0 = b0 + gv[bj][0] * acc[ai][bj][m][0], v1 = b1 + gv[bj][1] * acc[ai][bj][m][1];
;                     u32x4 w; w.x = pkh(v0[0], v0[1]); w.y = pkh(v0[2], v0[3]); w.z = pkh(v1[0], v1[1]); w.w = pkh(v1[2], v1[3]);
;                     *(u32x4*)(out + off + bj * HALF) = w; }
; template <bool BF, bool GATHER = false, class Epi, class Hook>
; __device__ __forceinline__ void gemm_phase(LAS unsigned char* lds, const Gemm g, const Order& S, const Epi& E, Hook& HK) {
;     ...
;             GM_LDA(At, 1, 1); GM_STAGE(GM_SB(1, 0), b3, voffB); GM_STAGE(GM_SB(1, 1), b3 + hstepB, voffB); GM_STA_H0(GM_SA(1, 0), a3, s0);
;             GM_WAIT_V(8); GM_WAIT_L(0); GM_BAR; GM_MMA(1, 0, At, B0); GM_MMA(1, 1, At, B1); GM_BAR; GM_SCHED;
;         }
;         if (wr == 0) GM_BAR;
	s_add_i32 s24, s48, s29
	v_lshl_add_u64 v[216:217], v[216:217], 0, s[8:9]
	s_mov_b32 m0, s24
	global_load_lds_dwordx4 v[216:217], off
	s_add_i32 m0, s24, 0x2000
	s_add_u32 s22, s22, 0x40080
	v_lshl_add_u64 v[216:217], v[218:219], 0, s[8:9]
	s_addc_u32 s23, s23, 0
	s_add_i32 s24, s49, s29
	global_load_lds_dwordx4 v[216:217], off
	v_lshl_add_u64 v[216:217], s[22:23], 0, v[148:149]
	s_mov_b32 m0, s24
	s_nop 0
	global_load_lds_dwordx4 v[216:217], off
	v_lshl_add_u64 v[216:217], s[22:23], 0, v[152:153]
	s_add_i32 m0, s24, 0x2000
	s_nop 0
	global_load_lds_dwordx4 v[216:217], off
	v_lshl_add_u64 v[216:217], v[220:221], 0, s[8:9]
	s_mov_b32 m0, s38
	s_nop 0
	global_load_lds_dwordx4 v[216:217], off
	v_lshl_add_u64 v[216:217], v[222:223], 0, s[8:9]
	s_mov_b32 m0, s39
	s_nop 0
	global_load_lds_dwordx4 v[216:217], off
	ds_read_b128 v[184:187], v170 offset:49152
	ds_read_b128 v[188:191], v170 offset:50176
	ds_read_b128 v[192:195], v170 offset:51200
	ds_read_b128 v[196:199], v170 offset:52224
	ds_read_b128 v[200:203], v170 offset:53248
	ds_read_b128 v[204:207], v170 offset:54272
	ds_read_b128 v[208:211], v170 offset:55296
	ds_read_b128 v[212:215], v170 offset:56320
	s_waitcnt vmcnt(8)
	s_waitcnt lgkmcnt(0)
	s_barrier
	s_setprio 1
	s_waitcnt lgkmcnt(0)
	v_mfma_f32_16x16x32_f16 v[62:65], v[130:133], v[184:187], v[62:65]
	v_mfma_f32_16x16x32_f16 v[58:61], v[138:141], v[184:187], v[58:61]
	v_mfma_f32_16x16x32_f16 v[46:49], v[130:133], v[192:195], v[46:49]
	v_mfma_f32_16x16x32_f16 v[42:45], v[138:141], v[192:195], v[42:45]
	v_mfma_f32_16x16x32_f16 v[30:33], v[130:133], v[200:203], v[30:33]
	v_mfma_f32_16x16x32_f16 v[26:29], v[138:141], v[200:203], v[26:29]
	v_mfma_f32_16x16x32_f16 v[14:17], v[130:133], v[208:211], v[14:17]
	v_mfma_f32_16x16x32_f16 v[10:13], v[138:141], v[208:211], v[10:13]
	v_mfma_f32_16x16x32_f16 v[62:65], v[134:137], v[188:191], v[62:65]
	v_mfma_f32_16x16x32_f16 v[58:61], v[142:145], v[188:191], v[58:61]
	v_mfma_f32_16x16x32_f16 v[46:49], v[134:137], v[196:199], v[46:49]
	v_mfma_f32_16x16x32_f16 v[42:45], v[142:145], v[196:199], v[42:45]
	v_mfma_f32_16x16x32_f16 v[30:33], v[134:137], v[204:207], v[30:33]
	v_mfma_f32_16x16x32_f16 v[26:29], v[142:145], v[204:207], v[26:29]
	v_mfma_f32_16x16x32_f16 v[14:17], v[134:137], v[212:215], v[14:17]
	v_mfma_f32_16x16x32_f16 v[10:13], v[142:145], v[212:215], v[10:13]
	s_setprio 0
	s_setprio 1
	v_mfma_f32_16x16x32_f16 v[54:57], v[162:165], v[184:187], v[54:57]
	v_mfma_f32_16x16x32_f16 v[50:53], v[176:179], v[184:187], v[50:53]
	v_mfma_f32_16x16x32_f16 v[38:41], v[162:165], v[192:195], v[38:41]
	v_mfma_f32_16x16x32_f16 v[34:37], v[176:179], v[192:195], v[34:37]
	v_mfma_f32_16x16x32_f16 v[22:25], v[162:165], v[200:203], v[22:25]
	v_mfma_f32_16x16x32_f16 v[18:21], v[176:179], v[200:203], v[18:21]
	v_mfma_f32_16x16x32_f16 v[6:9], v[162:165], v[208:211], v[6:9]
	v_mfma_f32_16x16x32_f16 v[2:5], v[176:179], v[208:211], v[2:5]
	v_mfma_f32_16x16x32_f16 v[54:57], v[172:175], v[188:191], v[54:57]
	v_mfma_f32_16x16x32_f16 v[50:53], v[180:183], v[188:191], v[50:53]
	v_mfma_f32_16x16x32_f16 v[38:41], v[172:175], v[196:199], v[38:41]
	v_mfma_f32_16x16x32_f16 v[34:37], v[180:183], v[196:199], v[34:37]
	v_mfma_f32_16x16x32_f16 v[22:25], v[172:175], v[204:207], v[22:25]
	v_mfma_f32_16x16x32_f16 v[18:21], v[180:183], v[204:207], v[18:21]
	v_mfma_f32_16x16x32_f16 v[6:9], v[172:175], v[212:215], v[6:9]
	v_mfma_f32_16x16x32_f16 v[2:5], v[180:183], v[212:215], v[2:5]
	s_setprio 0
	s_barrier
	s_add_i32 s47, s47, 2
	s_add_u32 s20, s20, 0x100
	s_addc_u32 s21, s21, 0
	s_add_u32 s45, s45, 0x100
	s_addc_u32 s46, s46, 0
	s_cmp_gt_u32 s47, 13
	s_cbranch_scc0 .LBB0_715
	s_and_b64 vcc, exec, s[10:11]
	s_cbranch_vccz .LBB0_718
	s_barrier
.LBB0_718:
	v_lshl_or_b32 v162, s3, 8, v167
	s_ashr_i32 s3, s2, 31
	s_lshr_b32 s3, s3, 29
	s_add_i32 s3, s2, s3
	s_ashr_i32 s3, s3, 3
	v_lshl_add_u32 v164, s2, 8, v1
	s_mul_hi_i32 s13, s3, 0x6000
	s_mulk_i32 s3, 0x6000
	v_ashrrev_i32_e32 v165, 31, v164
	s_add_u32 s20, s36, s3
	v_ashrrev_i32_e32 v163, 31, v162
	v_lshlrev_b64 v[134:135], 10, v[164:165]
	v_readlane_b32 s44, v251, 60
	s_addc_u32 s21, s37, s13
	v_lshl_add_u64 v[138:139], v[134:135], 0, v[162:163]
	v_readlane_b32 s45, v251, 61
	v_lshl_add_u64 v[142:143], v[162:163], 2, s[20:21]
	global_load_dwordx4 v[130:133], v[142:143], off
	v_lshl_add_u64 v[180:181], v[138:139], 2, s[44:45]
	global_load_dwordx4 v[172:175], v[180:181], off
	global_load_dwordx4 v[176:179], v[180:181], off offset:16
	global_load_dwordx4 v[134:137], v[142:143], off offset:16
	v_lshl_add_u64 v[182:183], v[138:139], 1, s[66:67]
	global_load_dwordx4 v[138:141], v[142:143], off offset:528
	s_nop 0
	global_load_dwordx4 v[142:145], v[142:143], off offset:512
	s_andn2_b64 vcc, exec, s[4:5]
	s_mov_b64 s[2:3], -1
	v_readlane_b32 s46, v251, 62
	v_readlane_b32 s47, v251, 63
	v_readlane_b32 s48, v250, 0
	v_readlane_b32 s49, v250, 1
	v_readlane_b32 s50, v250, 2
	v_readlane_b32 s51, v250, 3
	v_readlane_b32 s52, v250, 4
	v_readlane_b32 s53, v250, 5
	v_readlane_b32 s54, v250, 6
	v_readlane_b32 s55, v250, 7
	v_readlane_b32 s56, v250, 8
	v_readlane_b32 s57, v250, 9
	v_readlane_b32 s58, v250, 10
	v_readlane_b32 s59, v250, 11
	s_waitcnt vmcnt(0)
	v_pk_fma_f32 v[128:129], v[128:129], v[132:133], v[174:175]
	v_pk_fma_f32 v[126:127], v[126:127], v[130:131], v[172:173]
	v_pk_fma_f32 v[172:173], v[124:125], v[136:137], v[178:179]
	v_pk_fma_f32 v[124:125], v[122:123], v[134:135], v[176:177]
	v_cvt_pk_f16_f32 v122, v126, v127
	v_cvt_pk_f16_f32 v123, v128, v129
	v_cvt_pk_f16_f32 v124, v124, v125
	v_cvt_pk_f16_f32 v125, v172, v173
	global_store_dwordx4 v[182:183], v[122:125], off
	global_load_dwordx4 v[122:125], v[180:181], off offset:512
	s_nop 0
	global_load_dwordx4 v[126:129], v[180:181], off offset:528
	v_or_b32_e32 v172, 16, v164
	v_ashrrev_i32_e32 v173, 31, v172
	v_lshlrev_b64 v[172:173], 10, v[172:173]
	v_lshl_add_u64 v[172:173], v[172:173], 0, v[162:163]
	v_lshl_add_u64 v[174:175], v[172:173], 2, s[44:45]
	s_waitcnt vmcnt(1)
;     __device__ __forceinline__ void operator()(const Acc& acc, const Unit& u, int wr, int wc, int fr, int fq) const {
;     ...
;         for (int ai = 0; ai < 2; ++ai)
; #pragma unroll
;             for (int m = 0; m < 4; ++m) { const size_t off = (size_t)(u.pm * BM + ai * HALF + wr * 64 + m * 16 + fr) * DM + col0;
; #pragma unroll
;                 for (int bj = 0; bj < 2; ++bj) { f32x4 b0, b1;
;                     if constexpr (BASE16) { const f16x8 bv = *(const f16x8*)((const f16*)base + off + bj * HALF);
;                         b0 = (f32x4){(float)bv[0], (float)bv[1], (float)bv[2], (float)bv[3]}; b1 = (f32x4){(float)bv[4], (float)bv[5], (float)bv[6], (float)bv[7]}; }
;                     else { b0 = *(const f32x4*)((const float*)base + off + bj * HALF); b1 = *(const f32x4*)((const float*)base + off + bj * HALF + 4); }
;                     const f32x4 v0 = b0 + gv[bj][0] * acc[ai][bj][m][0], v1 = b1 + gv[bj][1] * acc[ai][bj][m][1];
;                     u32x4 w; w.x = pkh(v0[0], v0[1]); w.y = pkh(v0[2], v0[3]); w.z = pkh(v1[0], v1[1]); w.w = pkh(v1[2], v1[3]);
;                     *(u32x4*)(out + off + bj * HALF) = w; }
	v_pk_fma_f32 v[120:121], v[120:121], v[144:145], v[124:125]
	v_pk_fma_f32 v[118:119], v[118:119], v[142:143], v[122:123]
	s_waitcnt vmcnt(0)
	v_pk_fma_f32 v[122:123], v[116:117], v[140:141], v[128:129]
	v_pk_fma_f32 v[116:117], v[114:115], v[138:139], v[126:127]
	v_cvt_pk_f16_f32 v114, v118, v119
	v_cvt_pk_f16_f32 v115, v120, v121
	v_cvt_pk_f16_f32 v116, v116, v117
	v_cvt_pk_f16_f32 v117, v122, v123
	global_store_dwordx4 v[182:183], v[114:117], off offset:256
	global_load_dwordx4 v[114:117], v[174:175], off
	s_nop 0
	global_load_dwordx4 v[118:121], v[174:175], off offset:16
	v_lshl_add_u64 v[122:123], v[172:173], 1, s[66:67]
	s_waitcnt vmcnt(1)
	v_pk_fma_f32 v[112:113], v[112:113], v[132:133], v[116:117]
	v_pk_fma_f32 v[110:111], v[110:111], v[130:131], v[114:115]
	s_waitcnt vmcnt(0)
	v_pk_fma_f32 v[114:115], v[108:109], v[136:137], v[120:121]
	v_pk_fma_f32 v[108:109], v[106:107], v[134:135], v[118:119]
	v_cvt_pk_f16_f32 v106, v110, v111
	v_cvt_pk_f16_f32 v107, v112, v113
	v_cvt_pk_f16_f32 v108, v108, v109
	v_cvt_pk_f16_f32 v109, v114, v115
	global_store_dwordx4 v[122:123], v[106:109], off
	global_load_dwordx4 v[106:109], v[174:175], off offset:512
	s_nop 0
	global_load_dwordx4 v[110:113], v[174:175], off offset:528
	v_or_b32_e32 v114, 32, v164
	v_ashrrev_i32_e32 v115, 31, v114
	v_lshlrev_b64 v[114:115], 10, v[114:115]
	v_lshl_add_u64 v[114:115], v[114:115], 0, v[162:163]
	v_lshl_add_u64 v[116:117], v[114:115], 2, s[44:45]
	s_waitcnt vmcnt(1)
	v_pk_fma_f32 v[104:105], v[104:105], v[144:145], v[108:109]
	v_pk_fma_f32 v[102:103], v[102:103], v[142:143], v[106:107]
	s_waitcnt vmcnt(0)
	v_pk_fma_f32 v[106:107], v[100:101], v[140:141], v[112:113]
	v_pk_fma_f32 v[100:101], v[98:99], v[138:139], v[110:111]
	v_cvt_pk_f16_f32 v98, v102, v103
	v_cvt_pk_f16_f32 v99, v104, v105
	v_cvt_pk_f16_f32 v100, v100, v101
	v_cvt_pk_f16_f32 v101, v106, v107
	global_store_dwordx4 v[122:123], v[98:101], off offset:256
	global_load_dwordx4 v[98:101], v[116:117], off
	global_load_dwordx4 v[102:105], v[116:117], off offset:16
	v_lshl_add_u64 v[106:107], v[114:115], 1, s[66:67]
	s_waitcnt vmcnt(1)
	v_pk_fma_f32 v[96:97], v[96:97], v[132:133], v[100:101]
	v_pk_fma_f32 v[94:95], v[94:95], v[130:131], v[98:99]
	s_waitcnt vmcnt(0)
	v_pk_fma_f32 v[98:99], v[92:93], v[136:137], v[104:105]
	v_pk_fma_f32 v[92:93], v[90:91], v[134:135], v[102:103]
	v_cvt_pk_f16_f32 v90, v94, v95
	v_cvt_pk_f16_f32 v91, v96, v97
	v_cvt_pk_f16_f32 v92, v92, v93
	v_cvt_pk_f16_f32 v93, v98, v99
	global_store_dwordx4 v[106:107], v[90:93], off
	global_load_dwordx4 v[90:93], v[116:117], off offset:512
	s_nop 0
	global_load_dwordx4 v[94:97], v[116:117], off offset:528
	v_or_b32_e32 v98, 48, v164
	v_ashrrev_i32_e32 v99, 31, v98
	v_lshlrev_b64 v[98:99], 10, v[98:99]
	v_lshl_add_u64 v[98:99], v[98:99], 0, v[162:163]
	v_lshl_add_u64 v[100:101], v[98:99], 2, s[44:45]
	s_waitcnt vmcnt(1)
	v_pk_fma_f32 v[88:89], v[88:89], v[144:145], v[92:93]
	v_pk_fma_f32 v[86:87], v[86:87], v[142:143], v[90:91]
	s_waitcnt vmcnt(0)
	v_pk_fma_f32 v[90:91], v[84:85], v[140:141], v[96:97]
	v_pk_fma_f32 v[84:85], v[82:83], v[138:139], v[94:95]
	v_cvt_pk_f16_f32 v82, v86, v87
	v_cvt_pk_f16_f32 v83, v88, v89
	v_cvt_pk_f16_f32 v84, v84, v85
	v_cvt_pk_f16_f32 v85, v90, v91
	global_store_dwordx4 v[106:107], v[82:85], off offset:256
	global_load_dwordx4 v[82:85], v[100:101], off
	s_nop 0
	global_load_dwordx4 v[86:89], v[100:101], off offset:16
	v_lshl_add_u64 v[90:91], v[98:99], 1, s[66:67]
	s_waitcnt vmcnt(1)
	v_pk_fma_f32 v[80:81], v[80:81], v[132:133], v[84:85]
	v_pk_fma_f32 v[78:79], v[78:79], v[130:131], v[82:83]
	s_waitcnt vmcnt(0)
	v_pk_fma_f32 v[82:83], v[76:77], v[136:137], v[88:89]
	v_pk_fma_f32 v[76:77], v[74:75], v[134:135], v[86:87]
	v_cvt_pk_f16_f32 v74, v78, v79
	v_cvt_pk_f16_f32 v75, v80, v81
	v_cvt_pk_f16_f32 v76, v76, v77
	v_cvt_pk_f16_f32 v77, v82, v83
	global_store_dwordx4 v[90:91], v[74:77], off
	global_load_dwordx4 v[74:77], v[100:101], off offset:512
	s_nop 0
	global_load_dwordx4 v[78:81], v[100:101], off offset:528
	v_add_u32_e32 v82, 0x80, v164
	v_ashrrev_i32_e32 v83, 31, v82
	v_lshlrev_b64 v[82:83], 10, v[82:83]
	v_lshl_add_u64 v[82:83], v[82:83], 0, v[162:163]
	v_lshl_add_u64 v[84:85], v[82:83], 2, s[44:45]
	s_waitcnt vmcnt(1)
	v_pk_fma_f32 v[72:73], v[72:73], v[144:145], v[76:77]
	v_pk_fma_f32 v[70:71], v[70:71], v[142:143], v[74:75]
	s_waitcnt vmcnt(0)
	v_pk_fma_f32 v[74:75], v[68:69], v[140:141], v[80:81]
	v_pk_fma_f32 v[68:69], v[66:67], v[138:139], v[78:79]
	v_cvt_pk_f16_f32 v66, v70, v71
	v_cvt_pk_f16_f32 v67, v72, v73
	v_cvt_pk_f16_f32 v68, v68, v69
	v_cvt_pk_f16_f32 v69, v74, v75
	global_store_dwordx4 v[90:91], v[66:69], off offset:256
	global_load_dwordx4 v[66:69], v[84:85], off
	global_load_dwordx4 v[70:73], v[84:85], off offset:16
	v_lshl_add_u64 v[74:75], v[82:83], 1, s[66:67]
	s_waitcnt vmcnt(1)
	v_pk_fma_f32 v[64:65], v[64:65], v[132:133], v[68:69]
	v_pk_fma_f32 v[62:63], v[62:63], v[130:131], v[66:67]
	s_waitcnt vmcnt(0)
; #define GM_BAR __builtin_amdgcn_s_barrier()
;     __device__ __forceinline__ void operator()(const Acc& acc, const Unit& u, int wr, int wc, int fr, int fq) const {
;     ...
;         for (int ai = 0; ai < 2; ++ai)
; #pragma unroll
;             for (int m = 0; m < 4; ++m) { const size_t off = (size_t)(u.pm * BM + ai * HALF + wr * 64 + m * 16 + fr) * DM + col0;
; #pragma unroll
;                 for (int bj = 0; bj < 2; ++bj) { f32x4 b0, b1;
;                     if constexpr (BASE16) { const f16x8 bv = *(const f16x8*)((const f16*)base + off + bj * HALF);
;                         b0 = (f32x4){(float)bv[0], (float)bv[1], (float)bv[2], (float)bv[3]}; b1 = (f32x4){(float)bv[4], (float)bv[5], (float)bv[6], (float)bv[7]}; }
;                     else { b0 = *(const f32x4*)((const float*)base + off + bj * HALF); b1 = *(const f32x4*)((const float*)base + off + bj * HALF + 4); }
;                     const f32x4 v0 = b0 + gv[bj][0] * acc[ai][bj][m][0], v1 = b1 + gv[bj][1] * acc[ai][bj][m][1];
;                     u32x4 w; w.x = pkh(v0[0], v0[1]); w.y = pkh(v0[2], v0[3]); w.z = pkh(v1[0], v1[1]); w.w = pkh(v1[2], v1[3]);
;                     *(u32x4*)(out + off + bj * HALF) = w; }
;                 if (m & 1) asm volatile("" ::: "memory"); }
; template <bool BF, bool GATHER = false, class Epi, class Hook>
; __device__ __forceinline__ void gemm_phase(LAS unsigned char* lds, const Gemm g, const Order& S, const Epi& E, Hook& HK) {
;     ...
;         if (!has_next) break;
; #pragma unroll
;         for (int a = 0; a < 2; ++a)
; #pragma unroll
;             for (int b = 0; b < 2; ++b)
; #pragma unroll
;                 for (int m = 0; m < 4; ++m)
; #pragma unroll
;                     for (int n = 0; n < 2; ++n) acc[a][b][m][n] = (f32x4){0.f, 0.f, 0.f, 0.f};
;         cur = nxt; cA = nA; cB = nB; ++ui;
;         if constexpr (GATHER) { gA0[0] = nA0[0]; gA0[1] = nA0[1]; gA1[0] = nA1[0]; gA1[1] = nA1[1]; }
;         if (wr == 1) GM_BAR;
	v_pk_fma_f32 v[66:67], v[60:61], v[136:137], v[72:73]
	v_pk_fma_f32 v[60:61], v[58:59], v[134:135], v[70:71]
	v_cvt_pk_f16_f32 v58, v62, v63
	v_cvt_pk_f16_f32 v59, v64, v65
	v_cvt_pk_f16_f32 v60, v60, v61
	v_cvt_pk_f16_f32 v61, v66, v67
	global_store_dwordx4 v[74:75], v[58:61], off
	global_load_dwordx4 v[58:61], v[84:85], off offset:512
	s_nop 0
	global_load_dwordx4 v[62:65], v[84:85], off offset:528
	v_add_u32_e32 v66, 0x90, v164
	v_ashrrev_i32_e32 v67, 31, v66
	v_lshlrev_b64 v[66:67], 10, v[66:67]
	v_lshl_add_u64 v[66:67], v[66:67], 0, v[162:163]
	v_lshl_add_u64 v[68:69], v[66:67], 2, s[44:45]
	s_waitcnt vmcnt(1)
	v_pk_fma_f32 v[56:57], v[56:57], v[144:145], v[60:61]
	v_pk_fma_f32 v[54:55], v[54:55], v[142:143], v[58:59]
	s_waitcnt vmcnt(0)
	v_pk_fma_f32 v[58:59], v[52:53], v[140:141], v[64:65]
	v_pk_fma_f32 v[52:53], v[50:51], v[138:139], v[62:63]
	v_cvt_pk_f16_f32 v50, v54, v55
	v_cvt_pk_f16_f32 v51, v56, v57
	v_cvt_pk_f16_f32 v52, v52, v53
	v_cvt_pk_f16_f32 v53, v58, v59
	global_store_dwordx4 v[74:75], v[50:53], off offset:256
	global_load_dwordx4 v[50:53], v[68:69], off
	s_nop 0
	global_load_dwordx4 v[54:57], v[68:69], off offset:16
	v_lshl_add_u64 v[58:59], v[66:67], 1, s[66:67]
	s_waitcnt vmcnt(1)
	v_pk_fma_f32 v[48:49], v[48:49], v[132:133], v[52:53]
	v_pk_fma_f32 v[46:47], v[46:47], v[130:131], v[50:51]
	s_waitcnt vmcnt(0)
	v_pk_fma_f32 v[50:51], v[44:45], v[136:137], v[56:57]
	v_pk_fma_f32 v[44:45], v[42:43], v[134:135], v[54:55]
	v_cvt_pk_f16_f32 v42, v46, v47
	v_cvt_pk_f16_f32 v43, v48, v49
	v_cvt_pk_f16_f32 v44, v44, v45
	v_cvt_pk_f16_f32 v45, v50, v51
	global_store_dwordx4 v[58:59], v[42:45], off
	global_load_dwordx4 v[42:45], v[68:69], off offset:512
	s_nop 0
	global_load_dwordx4 v[46:49], v[68:69], off offset:528
	v_add_u32_e32 v50, 0xa0, v164
	v_ashrrev_i32_e32 v51, 31, v50
	v_lshlrev_b64 v[50:51], 10, v[50:51]
	v_lshl_add_u64 v[50:51], v[50:51], 0, v[162:163]
	v_lshl_add_u64 v[52:53], v[50:51], 2, s[44:45]
	s_waitcnt vmcnt(1)
	v_pk_fma_f32 v[40:41], v[40:41], v[144:145], v[44:45]
	v_pk_fma_f32 v[38:39], v[38:39], v[142:143], v[42:43]
	s_waitcnt vmcnt(0)
	v_pk_fma_f32 v[42:43], v[36:37], v[140:141], v[48:49]
	v_pk_fma_f32 v[36:37], v[34:35], v[138:139], v[46:47]
	v_cvt_pk_f16_f32 v34, v38, v39
	v_cvt_pk_f16_f32 v35, v40, v41
	v_cvt_pk_f16_f32 v36, v36, v37
	v_cvt_pk_f16_f32 v37, v42, v43
	global_store_dwordx4 v[58:59], v[34:37], off offset:256
	global_load_dwordx4 v[34:37], v[52:53], off
	global_load_dwordx4 v[38:41], v[52:53], off offset:16
	v_lshl_add_u64 v[42:43], v[50:51], 1, s[66:67]
	s_waitcnt vmcnt(1)
	v_pk_fma_f32 v[32:33], v[32:33], v[132:133], v[36:37]
	v_pk_fma_f32 v[30:31], v[30:31], v[130:131], v[34:35]
	s_waitcnt vmcnt(0)
	v_pk_fma_f32 v[34:35], v[28:29], v[136:137], v[40:41]
	v_pk_fma_f32 v[28:29], v[26:27], v[134:135], v[38:39]
	v_cvt_pk_f16_f32 v26, v30, v31
	v_cvt_pk_f16_f32 v27, v32, v33
	v_cvt_pk_f16_f32 v28, v28, v29
	v_cvt_pk_f16_f32 v29, v34, v35
	global_store_dwordx4 v[42:43], v[26:29], off
	global_load_dwordx4 v[26:29], v[52:53], off offset:512
	s_nop 0
	global_load_dwordx4 v[30:33], v[52:53], off offset:528
	v_add_u32_e32 v34, 0xb0, v164
	v_ashrrev_i32_e32 v35, 31, v34
	v_lshlrev_b64 v[34:35], 10, v[34:35]
	v_lshl_add_u64 v[34:35], v[34:35], 0, v[162:163]
	v_lshl_add_u64 v[36:37], v[34:35], 2, s[44:45]
	s_waitcnt vmcnt(1)
	v_pk_fma_f32 v[24:25], v[24:25], v[144:145], v[28:29]
	v_pk_fma_f32 v[22:23], v[22:23], v[142:143], v[26:27]
	s_waitcnt vmcnt(0)
	v_pk_fma_f32 v[26:27], v[20:21], v[140:141], v[32:33]
	v_pk_fma_f32 v[20:21], v[18:19], v[138:139], v[30:31]
	v_cvt_pk_f16_f32 v18, v22, v23
	v_cvt_pk_f16_f32 v19, v24, v25
	v_cvt_pk_f16_f32 v20, v20, v21
	v_cvt_pk_f16_f32 v21, v26, v27
	global_store_dwordx4 v[42:43], v[18:21], off offset:256
	global_load_dwordx4 v[18:21], v[36:37], off
	s_nop 0
	global_load_dwordx4 v[22:25], v[36:37], off offset:16
	v_lshl_add_u64 v[26:27], v[34:35], 1, s[66:67]
	s_waitcnt vmcnt(1)
	v_pk_fma_f32 v[16:17], v[16:17], v[132:133], v[20:21]
	v_pk_fma_f32 v[14:15], v[14:15], v[130:131], v[18:19]
	s_waitcnt vmcnt(0)
	v_pk_fma_f32 v[18:19], v[12:13], v[136:137], v[24:25]
	v_pk_fma_f32 v[12:13], v[10:11], v[134:135], v[22:23]
	v_cvt_pk_f16_f32 v10, v14, v15
	v_cvt_pk_f16_f32 v11, v16, v17
	v_cvt_pk_f16_f32 v12, v12, v13
	v_cvt_pk_f16_f32 v13, v18, v19
	global_store_dwordx4 v[26:27], v[10:13], off
	global_load_dwordx4 v[10:13], v[36:37], off offset:512
	s_nop 0
	global_load_dwordx4 v[14:17], v[36:37], off offset:528
	s_waitcnt vmcnt(1)
	v_pk_fma_f32 v[8:9], v[8:9], v[144:145], v[12:13]
	v_pk_fma_f32 v[6:7], v[6:7], v[142:143], v[10:11]
	s_waitcnt vmcnt(0)
	v_pk_fma_f32 v[10:11], v[4:5], v[140:141], v[16:17]
	v_pk_fma_f32 v[4:5], v[2:3], v[138:139], v[14:15]
	v_cvt_pk_f16_f32 v2, v6, v7
	v_cvt_pk_f16_f32 v3, v8, v9
	v_cvt_pk_f16_f32 v4, v4, v5
	v_cvt_pk_f16_f32 v5, v10, v11
	global_store_dwordx4 v[26:27], v[2:5], off offset:256
	s_cbranch_vccnz .LBB0_707
	s_andn2_b64 vcc, exec, s[6:7]
	s_cbranch_vccnz .LBB0_706
	s_barrier
	s_branch .LBB0_706

; #define GM_STAGE(bufoff, gbase, voff) do { _Pragma("unroll") for (int _i = 0; _i < 2; ++_i) \
;         __builtin_amdgcn_global_load_lds((const unsigned*)((const char*)(gbase) + (voff)[_i]), (LAS unsigned*)(lds + (bufoff) + ldsw + _i * 8192), 16, 0, 0); } while (0)
; #define GM_LDA(dst, b, h) do { _Pragma("unroll") for (int m = 0; m < 4; ++m) _Pragma("unroll") for (int k = 0; k < 2; ++k) dst[m][k] = *(const LAS s16x8*)(lds + GM_SA(b, h) + aoff + m * 2048 + k * 1024); } while (0)
; #define GM_LDB(dst, b, h) do { _Pragma("unroll") for (int n = 0; n < 2; ++n) _Pragma("unroll") for (int k = 0; k < 2; ++k) dst[n][k] = *(const LAS s16x8*)(lds + GM_SB(b, h) + boff + n * 2048 + k * 1024); } while (0)
; #define GM_MMA(ai, bj, At, Bt) do { __builtin_amdgcn_s_setprio(1); _Pragma("unroll") for (int m = 0; m < 4; ++m) _Pragma("unroll") for (int n = 0; n < 2; ++n) _Pragma("unroll") for (int k = 0; k < 2; ++k) \
;         acc[ai][bj][m][n] = mma16<BF>(Bt[n][k], At[m][k], acc[ai][bj][m][n]); __builtin_amdgcn_s_setprio(0); } while (0)
; #define GM_WAIT_V(n) asm volatile("s_waitcnt vmcnt(" #n ")" ::: "memory")
; #define GM_BAR __builtin_amdgcn_s_barrier()
; template <bool BF, bool GATHER = false, class Epi, class Hook>
; __device__ __forceinline__ void gemm_phase(LAS unsigned char* lds, const Gemm g, const Order& S, const Epi& E, Hook& HK) {
;     ...
;         for (int t = 0; t < nt; t += 2) {
;             const bool last = (t == nt - 2);
;             const char* a1 = cA + (size_t)(t + 1) * kstep;
;             const char* a2 = last ? nA : cA + (size_t)(t + 2) * kstep; const char* b2 = last ? nB : cB + (size_t)(t + 2) * kstep;
;             const char* a3 = a2 + kstep; const char* b3 = b2 + kstep;
;             unsigned s0[2], s1[2];
;             if constexpr (GATHER) { s0[0] = last ? nA0[0] : gA0[0]; s0[1] = last ? nA0[1] : gA0[1]; s1[0] = last ? nA1[0] : gA1[0]; s1[1] = last ? nA1[1] : gA1[1]; }
;             GM_LDB(B0, 0, 0); GM_LDB(B1, 0, 1); GM_SCHED; GM_LDA(At, 0, 0); GM_STA_H1(GM_SA(1, 1), a1, gA1);
;             GM_WAIT_V(8); GM_WAIT_L(0); GM_BAR; GM_MMA(0, 0, At, B0); GM_MMA(0, 1, At, B1); GM_BAR; GM_SCHED;
;             GM_LDA(At, 0, 1); GM_STAGE(GM_SB(0, 0), b2, voffB); GM_STAGE(GM_SB(0, 1), b2 + hstepB, voffB); GM_STA_H0(GM_SA(0, 0), a2, s0);
;             GM_WAIT_V(8); GM_WAIT_L(0); GM_BAR; GM_MMA(1, 0, At, B0); GM_MMA(1, 1, At, B1); GM_BAR; GM_SCHED;
.LBB0_1011:
	s_add_u32 s22, s90, s2
	s_addc_u32 s23, s91, s3
	s_add_u32 s24, s22, 0x11e00100
	s_addc_u32 s25, s23, 0
	s_add_u32 s44, s21, s2
	s_addc_u32 s45, s42, s3
	s_cmpk_eq_i32 s2, 0x700
	s_cselect_b64 vcc, -1, 0
	s_and_b64 s[22:23], vcc, exec
	v_cndmask_b32_e32 v134, v142, v159, vcc
	s_cselect_b32 s25, s69, s25
	s_cselect_b32 s24, s68, s24
	v_cndmask_b32_e32 v228, v146, v162, vcc
	v_cndmask_b32_e32 v141, v158, v160, vcc
	v_cndmask_b32_e32 v145, v157, v161, vcc
	s_cselect_b32 s23, s1, s45
	s_cselect_b32 s22, s0, s44
	v_lshl_add_u64 v[230:231], v[150:151], 0, s[2:3]
	s_add_i32 m0, s28, 0xc000
	global_load_lds_dwordx4 v[230:231], off
	v_lshl_add_u64 v[230:231], v[148:149], 0, s[2:3]
	s_add_i32 m0, s28, 0xe000
	s_nop 0
	global_load_lds_dwordx4 v[230:231], off
	v_add_u32_e32 v244, s35, v156
	ds_read_b128 v[164:167], v244
	ds_read_b128 v[168:171], v244 offset:1024
	ds_read_b128 v[172:175], v244 offset:2048
	ds_read_b128 v[176:179], v244 offset:3072
	v_add_u32_e32 v244, s36, v156
	ds_read_b128 v[180:183], v244
	ds_read_b128 v[184:187], v244 offset:1024
	ds_read_b128 v[188:191], v244 offset:2048
	ds_read_b128 v[192:195], v244 offset:3072
	ds_read_b128 v[196:199], v147
	ds_read_b128 v[200:203], v147 offset:1024
	ds_read_b128 v[204:207], v147 offset:2048
	ds_read_b128 v[208:211], v147 offset:3072
	ds_read_b128 v[212:215], v147 offset:4096
	ds_read_b128 v[216:219], v147 offset:5120
	ds_read_b128 v[220:223], v147 offset:6144
	ds_read_b128 v[224:227], v147 offset:7168
	s_waitcnt vmcnt(8)
	s_waitcnt lgkmcnt(0)
	s_barrier
	s_setprio 1
	s_waitcnt lgkmcnt(0)
	v_mfma_f32_16x16x32_bf16 v[98:101], v[164:167], v[196:199], v[98:101]
	v_mfma_f32_16x16x32_bf16 v[94:97], v[172:175], v[196:199], v[94:97]
	v_mfma_f32_16x16x32_bf16 v[90:93], v[164:167], v[204:207], v[90:93]
	v_mfma_f32_16x16x32_bf16 v[86:89], v[172:175], v[204:207], v[86:89]
	v_mfma_f32_16x16x32_bf16 v[82:85], v[164:167], v[212:215], v[82:85]
	v_mfma_f32_16x16x32_bf16 v[78:81], v[172:175], v[212:215], v[78:81]
	v_mfma_f32_16x16x32_bf16 v[74:77], v[164:167], v[220:223], v[74:77]
	v_mfma_f32_16x16x32_bf16 v[70:73], v[172:175], v[220:223], v[70:73]
	v_mfma_f32_16x16x32_bf16 v[98:101], v[168:171], v[200:203], v[98:101]
	v_mfma_f32_16x16x32_bf16 v[94:97], v[176:179], v[200:203], v[94:97]
	v_mfma_f32_16x16x32_bf16 v[90:93], v[168:171], v[208:211], v[90:93]
	v_mfma_f32_16x16x32_bf16 v[86:89], v[176:179], v[208:211], v[86:89]
	v_mfma_f32_16x16x32_bf16 v[82:85], v[168:171], v[216:219], v[82:85]
	v_mfma_f32_16x16x32_bf16 v[78:81], v[176:179], v[216:219], v[78:81]
	v_mfma_f32_16x16x32_bf16 v[74:77], v[168:171], v[224:227], v[74:77]
	v_mfma_f32_16x16x32_bf16 v[70:73], v[176:179], v[224:227], v[70:73]
	s_setprio 0
	s_setprio 1
	v_mfma_f32_16x16x32_bf16 v[66:69], v[180:183], v[196:199], v[66:69]
	v_mfma_f32_16x16x32_bf16 v[62:65], v[188:191], v[196:199], v[62:65]
	v_mfma_f32_16x16x32_bf16 v[58:61], v[180:183], v[204:207], v[58:61]
	v_mfma_f32_16x16x32_bf16 v[54:57], v[188:191], v[204:207], v[54:57]
	v_mfma_f32_16x16x32_bf16 v[50:53], v[180:183], v[212:215], v[50:53]
	v_mfma_f32_16x16x32_bf16 v[46:49], v[188:191], v[212:215], v[46:49]
	v_mfma_f32_16x16x32_bf16 v[42:45], v[180:183], v[220:223], v[42:45]
	v_mfma_f32_16x16x32_bf16 v[38:41], v[188:191], v[220:223], v[38:41]
	v_mfma_f32_16x16x32_bf16 v[66:69], v[184:187], v[200:203], v[66:69]
	v_mfma_f32_16x16x32_bf16 v[62:65], v[192:195], v[200:203], v[62:65]
	v_mfma_f32_16x16x32_bf16 v[58:61], v[184:187], v[208:211], v[58:61]
	v_mfma_f32_16x16x32_bf16 v[54:57], v[192:195], v[208:211], v[54:57]
	v_mfma_f32_16x16x32_bf16 v[50:53], v[184:187], v[216:219], v[50:53]
	v_mfma_f32_16x16x32_bf16 v[46:49], v[192:195], v[216:219], v[46:49]
	v_mfma_f32_16x16x32_bf16 v[42:45], v[184:187], v[224:227], v[42:45]
	v_mfma_f32_16x16x32_bf16 v[38:41], v[192:195], v[224:227], v[38:41]
	s_setprio 0
	s_barrier
	s_add_i32 s44, s35, s11
	v_lshl_add_u64 v[230:231], s[22:23], 0, v[130:131]
	s_mov_b32 m0, s44
	global_load_lds_dwordx4 v[230:231], off
	s_add_i32 m0, s44, 0x2000
	s_add_u32 s44, s22, 0x40000
	v_lshl_add_u64 v[232:233], s[22:23], 0, v[132:133]
	s_addc_u32 s45, s23, 0
	s_add_i32 s46, s36, s11
	global_load_lds_dwordx4 v[232:233], off
	v_lshl_add_u64 v[234:235], s[44:45], 0, v[130:131]
	s_mov_b32 m0, s46
	v_mov_b32_e32 v229, v135
	global_load_lds_dwordx4 v[234:235], off
	v_lshl_add_u64 v[234:235], s[44:45], 0, v[132:133]
	s_add_i32 m0, s46, 0x2000
	s_nop 0
	global_load_lds_dwordx4 v[234:235], off
	s_mov_b32 m0, s28
	v_lshl_add_u64 v[234:235], s[24:25], 0, v[134:135]
	global_load_lds_dwordx4 v134, s[24:25]
	s_mov_b32 m0, s29
	s_nop 0
	global_load_lds_dwordx4 v228, s[24:25]
	v_lshl_add_u64 v[228:229], s[24:25], 0, v[228:229]
	ds_read_b128 v[196:199], v147 offset:16384
	ds_read_b128 v[200:203], v147 offset:17408
	ds_read_b128 v[204:207], v147 offset:18432
	ds_read_b128 v[208:211], v147 offset:19456
	ds_read_b128 v[212:215], v147 offset:20480
	ds_read_b128 v[216:219], v147 offset:21504
	ds_read_b128 v[220:223], v147 offset:22528
	ds_read_b128 v[224:227], v147 offset:23552
	s_waitcnt vmcnt(8)
	s_waitcnt lgkmcnt(0)
	s_barrier
; #define GM_LDA(dst, b, h) do { _Pragma("unroll") for (int m = 0; m < 4; ++m) _Pragma("unroll") for (int k = 0; k < 2; ++k) dst[m][k] = *(const LAS s16x8*)(lds + GM_SA(b, h) + aoff + m * 2048 + k * 1024); } while (0)
; #define GM_LDB(dst, b, h) do { _Pragma("unroll") for (int n = 0; n < 2; ++n) _Pragma("unroll") for (int k = 0; k < 2; ++k) dst[n][k] = *(const LAS s16x8*)(lds + GM_SB(b, h) + boff + n * 2048 + k * 1024); } while (0)
; #define GM_MMA(ai, bj, At, Bt) do { __builtin_amdgcn_s_setprio(1); _Pragma("unroll") for (int m = 0; m < 4; ++m) _Pragma("unroll") for (int n = 0; n < 2; ++n) _Pragma("unroll") for (int k = 0; k < 2; ++k) \
;         acc[ai][bj][m][n] = mma16<BF>(Bt[n][k], At[m][k], acc[ai][bj][m][n]); __builtin_amdgcn_s_setprio(0); } while (0)
; #define GM_WAIT_V(n) asm volatile("s_waitcnt vmcnt(" #n ")" ::: "memory")
; #define GM_WAIT_L(n) asm volatile("s_waitcnt lgkmcnt(" #n ")" ::: "memory")
; #define GM_BAR __builtin_amdgcn_s_barrier()
; #define GM_SCHED __builtin_amdgcn_sched_barrier(0)
; #define GM_STA_H1(buf, p, o1) do { if constexpr (GATHER) GM_STAGE(buf, p, o1); else GM_STAGE(buf, (p) + hstepB, voffA); } while (0)
; template <bool BF, bool GATHER = false, class Epi, class Hook>
; __device__ __forceinline__ void gemm_phase(LAS unsigned char* lds, const Gemm g, const Order& S, const Epi& E, Hook& HK) {
;     ...
;             GM_WAIT_V(8); GM_WAIT_L(0); GM_BAR; GM_MMA(1, 0, At, B0); GM_MMA(1, 1, At, B1); GM_BAR; GM_SCHED;
;             GM_LDB(B0, 1, 0); GM_LDB(B1, 1, 1); GM_SCHED; GM_LDA(At, 1, 0); GM_STA_H1(GM_SA(0, 1), a2, s1);
;             GM_WAIT_V(8); GM_WAIT_L(0); GM_BAR; GM_MMA(0, 0, At, B0); GM_MMA(0, 1, At, B1); GM_BAR; GM_SCHED;
	s_setprio 1
	s_waitcnt lgkmcnt(0)
	v_mfma_f32_16x16x32_bf16 v[34:37], v[164:167], v[196:199], v[34:37]
	v_mfma_f32_16x16x32_bf16 v[30:33], v[172:175], v[196:199], v[30:33]
	v_mfma_f32_16x16x32_bf16 v[26:29], v[164:167], v[204:207], v[26:29]
	v_mfma_f32_16x16x32_bf16 v[22:25], v[172:175], v[204:207], v[22:25]
	v_mfma_f32_16x16x32_bf16 v[18:21], v[164:167], v[212:215], v[18:21]
	v_mfma_f32_16x16x32_bf16 v[14:17], v[172:175], v[212:215], v[14:17]
	v_mfma_f32_16x16x32_bf16 v[10:13], v[164:167], v[220:223], v[10:13]
	v_mfma_f32_16x16x32_bf16 v[6:9], v[172:175], v[220:223], v[6:9]
	v_mfma_f32_16x16x32_bf16 v[34:37], v[168:171], v[200:203], v[34:37]
	v_mfma_f32_16x16x32_bf16 v[30:33], v[176:179], v[200:203], v[30:33]
	v_mfma_f32_16x16x32_bf16 v[26:29], v[168:171], v[208:211], v[26:29]
	v_mfma_f32_16x16x32_bf16 v[22:25], v[176:179], v[208:211], v[22:25]
	v_mfma_f32_16x16x32_bf16 v[18:21], v[168:171], v[216:219], v[18:21]
	v_mfma_f32_16x16x32_bf16 v[14:17], v[176:179], v[216:219], v[14:17]
	v_mfma_f32_16x16x32_bf16 v[10:13], v[168:171], v[224:227], v[10:13]
	v_mfma_f32_16x16x32_bf16 v[6:9], v[176:179], v[224:227], v[6:9]
	s_setprio 0
	s_setprio 1
	v_mfma_f32_16x16x32_bf16 v[2:5], v[180:183], v[196:199], v[2:5]
	v_mfma_f32_16x16x32_bf16 v[102:105], v[188:191], v[196:199], v[102:105]
	v_mfma_f32_16x16x32_bf16 v[106:109], v[180:183], v[204:207], v[106:109]
	v_mfma_f32_16x16x32_bf16 v[110:113], v[188:191], v[204:207], v[110:113]
	v_mfma_f32_16x16x32_bf16 v[114:117], v[180:183], v[212:215], v[114:117]
	v_mfma_f32_16x16x32_bf16 v[118:121], v[188:191], v[212:215], v[118:121]
	v_mfma_f32_16x16x32_bf16 v[122:125], v[180:183], v[220:223], v[122:125]
	v_mfma_f32_16x16x32_bf16 v[126:129], v[188:191], v[220:223], v[126:129]
	v_mfma_f32_16x16x32_bf16 v[2:5], v[184:187], v[200:203], v[2:5]
	v_mfma_f32_16x16x32_bf16 v[102:105], v[192:195], v[200:203], v[102:105]
	v_mfma_f32_16x16x32_bf16 v[106:109], v[184:187], v[208:211], v[106:109]
	v_mfma_f32_16x16x32_bf16 v[110:113], v[192:195], v[208:211], v[110:113]
	v_mfma_f32_16x16x32_bf16 v[114:117], v[184:187], v[216:219], v[114:117]
	v_mfma_f32_16x16x32_bf16 v[118:121], v[192:195], v[216:219], v[118:121]
	v_mfma_f32_16x16x32_bf16 v[122:125], v[184:187], v[224:227], v[122:125]
	v_mfma_f32_16x16x32_bf16 v[126:129], v[192:195], v[224:227], v[126:129]
	s_setprio 0
	s_barrier
	s_mov_b32 m0, s30
	global_load_lds_dwordx4 v141, s[24:25]
	s_mov_b32 m0, s31
	s_nop 0
	global_load_lds_dwordx4 v145, s[24:25]
	s_mov_b32 s45, 0x1c000
	s_mov_b32 s44, 0x18000
	v_add_u32_e32 v245, s44, v156
	ds_read_b128 v[164:167], v245
	ds_read_b128 v[168:171], v245 offset:1024
	ds_read_b128 v[172:175], v245 offset:2048
	ds_read_b128 v[176:179], v245 offset:3072
	v_add_u32_e32 v245, s45, v156
	ds_read_b128 v[180:183], v245
	ds_read_b128 v[184:187], v245 offset:1024
	ds_read_b128 v[188:191], v245 offset:2048
	ds_read_b128 v[192:195], v245 offset:3072
	ds_read_b128 v[196:199], v147 offset:32768
	ds_read_b128 v[200:203], v147 offset:33792
	ds_read_b128 v[204:207], v147 offset:34816
	ds_read_b128 v[208:211], v147 offset:35840
	ds_read_b128 v[212:215], v147 offset:36864
	ds_read_b128 v[216:219], v147 offset:37888
	ds_read_b128 v[220:223], v147 offset:38912
	ds_read_b128 v[224:227], v147 offset:39936
	s_waitcnt vmcnt(8)
	s_waitcnt lgkmcnt(0)
	s_barrier
	s_setprio 1
	s_waitcnt lgkmcnt(0)
	v_mfma_f32_16x16x32_bf16 v[98:101], v[164:167], v[196:199], v[98:101]
	v_mfma_f32_16x16x32_bf16 v[94:97], v[172:175], v[196:199], v[94:97]
	v_mfma_f32_16x16x32_bf16 v[90:93], v[164:167], v[204:207], v[90:93]
	v_mfma_f32_16x16x32_bf16 v[86:89], v[172:175], v[204:207], v[86:89]
	v_mfma_f32_16x16x32_bf16 v[82:85], v[164:167], v[212:215], v[82:85]
	v_mfma_f32_16x16x32_bf16 v[78:81], v[172:175], v[212:215], v[78:81]
	v_mfma_f32_16x16x32_bf16 v[74:77], v[164:167], v[220:223], v[74:77]
	v_mfma_f32_16x16x32_bf16 v[70:73], v[172:175], v[220:223], v[70:73]
	v_mfma_f32_16x16x32_bf16 v[98:101], v[168:171], v[200:203], v[98:101]
	v_mfma_f32_16x16x32_bf16 v[94:97], v[176:179], v[200:203], v[94:97]
	v_mfma_f32_16x16x32_bf16 v[90:93], v[168:171], v[208:211], v[90:93]
	v_mfma_f32_16x16x32_bf16 v[86:89], v[176:179], v[208:211], v[86:89]
	v_mfma_f32_16x16x32_bf16 v[82:85], v[168:171], v[216:219], v[82:85]
	v_mfma_f32_16x16x32_bf16 v[78:81], v[176:179], v[216:219], v[78:81]
	v_mfma_f32_16x16x32_bf16 v[74:77], v[168:171], v[224:227], v[74:77]
	v_mfma_f32_16x16x32_bf16 v[70:73], v[176:179], v[224:227], v[70:73]
	s_setprio 0
	s_setprio 1
	v_mfma_f32_16x16x32_bf16 v[66:69], v[180:183], v[196:199], v[66:69]
	v_mfma_f32_16x16x32_bf16 v[62:65], v[188:191], v[196:199], v[62:65]
	v_mfma_f32_16x16x32_bf16 v[58:61], v[180:183], v[204:207], v[58:61]
	v_mfma_f32_16x16x32_bf16 v[54:57], v[188:191], v[204:207], v[54:57]
	v_mfma_f32_16x16x32_bf16 v[50:53], v[180:183], v[212:215], v[50:53]
	v_mfma_f32_16x16x32_bf16 v[46:49], v[188:191], v[212:215], v[46:49]
	v_mfma_f32_16x16x32_bf16 v[42:45], v[180:183], v[220:223], v[42:45]
	v_mfma_f32_16x16x32_bf16 v[38:41], v[188:191], v[220:223], v[38:41]
	v_mfma_f32_16x16x32_bf16 v[66:69], v[184:187], v[200:203], v[66:69]
	v_mfma_f32_16x16x32_bf16 v[62:65], v[192:195], v[200:203], v[62:65]
	v_mfma_f32_16x16x32_bf16 v[58:61], v[184:187], v[208:211], v[58:61]
	v_mfma_f32_16x16x32_bf16 v[54:57], v[192:195], v[208:211], v[54:57]
	v_mfma_f32_16x16x32_bf16 v[50:53], v[184:187], v[216:219], v[50:53]
	v_mfma_f32_16x16x32_bf16 v[46:49], v[192:195], v[216:219], v[46:49]
	v_mfma_f32_16x16x32_bf16 v[42:45], v[184:187], v[224:227], v[42:45]
	v_mfma_f32_16x16x32_bf16 v[38:41], v[192:195], v[224:227], v[38:41]
	s_setprio 0
	s_barrier
; #define GM_STAGE(bufoff, gbase, voff) do { _Pragma("unroll") for (int _i = 0; _i < 2; ++_i) \
;         __builtin_amdgcn_global_load_lds((const unsigned*)((const char*)(gbase) + (voff)[_i]), (LAS unsigned*)(lds + (bufoff) + ldsw + _i * 8192), 16, 0, 0); } while (0)
; #define GM_LDA(dst, b, h) do { _Pragma("unroll") for (int m = 0; m < 4; ++m) _Pragma("unroll") for (int k = 0; k < 2; ++k) dst[m][k] = *(const LAS s16x8*)(lds + GM_SA(b, h) + aoff + m * 2048 + k * 1024); } while (0)
; #define GM_MMA(ai, bj, At, Bt) do { __builtin_amdgcn_s_setprio(1); _Pragma("unroll") for (int m = 0; m < 4; ++m) _Pragma("unroll") for (int n = 0; n < 2; ++n) _Pragma("unroll") for (int k = 0; k < 2; ++k) \
;         acc[ai][bj][m][n] = mma16<BF>(Bt[n][k], At[m][k], acc[ai][bj][m][n]); __builtin_amdgcn_s_setprio(0); } while (0)
; #define GM_WAIT_V(n) asm volatile("s_waitcnt vmcnt(" #n ")" ::: "memory")
; #define GM_WAIT_L(n) asm volatile("s_waitcnt lgkmcnt(" #n ")" ::: "memory")
; #define GM_BAR __builtin_amdgcn_s_barrier()
; #define GM_SCHED __builtin_amdgcn_sched_barrier(0)
; #define GM_STA_H0(buf, p, o0) do { if constexpr (GATHER) GM_STAGE(buf, p, o0); else GM_STAGE(buf, p, voffA); } while (0)
; template <bool BF, bool GATHER = false, class Epi, class Hook>
; __device__ __forceinline__ void gemm_phase(LAS unsigned char* lds, const Gemm g, const Order& S, const Epi& E, Hook& HK) {
;     ...
;             GM_LDA(At, 1, 1); GM_STAGE(GM_SB(1, 0), b3, voffB); GM_STAGE(GM_SB(1, 1), b3 + hstepB, voffB); GM_STA_H0(GM_SA(1, 0), a3, s0);
;             GM_WAIT_V(8); GM_WAIT_L(0); GM_BAR; GM_MMA(1, 0, At, B0); GM_MMA(1, 1, At, B1); GM_BAR; GM_SCHED;
;         }
;         if (wr == 0) GM_BAR;
	s_add_i32 s24, s44, s11
	v_lshl_add_u64 v[230:231], v[230:231], 0, s[14:15]
	s_mov_b32 m0, s24
	global_load_lds_dwordx4 v[230:231], off
	s_add_i32 m0, s24, 0x2000
	s_add_u32 s22, s22, 0x40080
	v_lshl_add_u64 v[230:231], v[232:233], 0, s[14:15]
	s_addc_u32 s23, s23, 0
	s_add_i32 s24, s45, s11
	global_load_lds_dwordx4 v[230:231], off
	v_lshl_add_u64 v[230:231], s[22:23], 0, v[130:131]
	s_mov_b32 m0, s24
	v_lshl_add_u64 v[228:229], v[228:229], 0, s[14:15]
	global_load_lds_dwordx4 v[230:231], off
	v_lshl_add_u64 v[230:231], s[22:23], 0, v[132:133]
	s_add_i32 m0, s24, 0x2000
	s_nop 0
	global_load_lds_dwordx4 v[230:231], off
	v_lshl_add_u64 v[230:231], v[234:235], 0, s[14:15]
	s_mov_b32 m0, s33
	s_nop 0
	global_load_lds_dwordx4 v[230:231], off
	s_mov_b32 m0, s34
	s_nop 0
	global_load_lds_dwordx4 v[228:229], off
	ds_read_b128 v[196:199], v147 offset:49152
	ds_read_b128 v[200:203], v147 offset:50176
	ds_read_b128 v[204:207], v147 offset:51200
	ds_read_b128 v[208:211], v147 offset:52224
	ds_read_b128 v[212:215], v147 offset:53248
	ds_read_b128 v[216:219], v147 offset:54272
	ds_read_b128 v[220:223], v147 offset:55296
	ds_read_b128 v[224:227], v147 offset:56320
	s_waitcnt vmcnt(8)
	s_waitcnt lgkmcnt(0)
	s_barrier
	s_setprio 1
	s_waitcnt lgkmcnt(0)
	v_mfma_f32_16x16x32_bf16 v[34:37], v[164:167], v[196:199], v[34:37]
	v_mfma_f32_16x16x32_bf16 v[30:33], v[172:175], v[196:199], v[30:33]
	v_mfma_f32_16x16x32_bf16 v[26:29], v[164:167], v[204:207], v[26:29]
	v_mfma_f32_16x16x32_bf16 v[22:25], v[172:175], v[204:207], v[22:25]
	v_mfma_f32_16x16x32_bf16 v[18:21], v[164:167], v[212:215], v[18:21]
	v_mfma_f32_16x16x32_bf16 v[14:17], v[172:175], v[212:215], v[14:17]
	v_mfma_f32_16x16x32_bf16 v[10:13], v[164:167], v[220:223], v[10:13]
	v_mfma_f32_16x16x32_bf16 v[6:9], v[172:175], v[220:223], v[6:9]
	v_mfma_f32_16x16x32_bf16 v[34:37], v[168:171], v[200:203], v[34:37]
	v_mfma_f32_16x16x32_bf16 v[30:33], v[176:179], v[200:203], v[30:33]
	v_mfma_f32_16x16x32_bf16 v[26:29], v[168:171], v[208:211], v[26:29]
	v_mfma_f32_16x16x32_bf16 v[22:25], v[176:179], v[208:211], v[22:25]
	v_mfma_f32_16x16x32_bf16 v[18:21], v[168:171], v[216:219], v[18:21]
	v_mfma_f32_16x16x32_bf16 v[14:17], v[176:179], v[216:219], v[14:17]
	v_mfma_f32_16x16x32_bf16 v[10:13], v[168:171], v[224:227], v[10:13]
	v_mfma_f32_16x16x32_bf16 v[6:9], v[176:179], v[224:227], v[6:9]
	s_setprio 0
	s_setprio 1
	v_mfma_f32_16x16x32_bf16 v[2:5], v[180:183], v[196:199], v[2:5]
	v_mfma_f32_16x16x32_bf16 v[102:105], v[188:191], v[196:199], v[102:105]
	v_mfma_f32_16x16x32_bf16 v[106:109], v[180:183], v[204:207], v[106:109]
	v_mfma_f32_16x16x32_bf16 v[110:113], v[188:191], v[204:207], v[110:113]
	v_mfma_f32_16x16x32_bf16 v[114:117], v[180:183], v[212:215], v[114:117]
	v_mfma_f32_16x16x32_bf16 v[118:121], v[188:191], v[212:215], v[118:121]
	v_mfma_f32_16x16x32_bf16 v[122:125], v[180:183], v[220:223], v[122:125]
	v_mfma_f32_16x16x32_bf16 v[126:129], v[188:191], v[220:223], v[126:129]
	v_mfma_f32_16x16x32_bf16 v[2:5], v[184:187], v[200:203], v[2:5]
	v_mfma_f32_16x16x32_bf16 v[102:105], v[192:195], v[200:203], v[102:105]
	v_mfma_f32_16x16x32_bf16 v[106:109], v[184:187], v[208:211], v[106:109]
	v_mfma_f32_16x16x32_bf16 v[110:113], v[192:195], v[208:211], v[110:113]
	v_mfma_f32_16x16x32_bf16 v[114:117], v[184:187], v[216:219], v[114:117]
	v_mfma_f32_16x16x32_bf16 v[118:121], v[192:195], v[216:219], v[118:121]
	v_mfma_f32_16x16x32_bf16 v[122:125], v[184:187], v[224:227], v[122:125]
	v_mfma_f32_16x16x32_bf16 v[126:129], v[192:195], v[224:227], v[126:129]
	s_setprio 0
	s_barrier
	s_add_i32 s43, s43, 2
	s_add_u32 s2, s2, 0x100
	s_addc_u32 s3, s3, 0
	s_cmp_gt_u32 s43, 13
	s_cbranch_scc0 .LBB0_1011
	s_and_b64 vcc, exec, s[18:19]
	s_cbranch_vccz .LBB0_1014
	s_barrier

; #define GM_STAGE(bufoff, gbase, voff) do { _Pragma("unroll") for (int _i = 0; _i < 2; ++_i) \
;         __builtin_amdgcn_global_load_lds((const unsigned*)((const char*)(gbase) + (voff)[_i]), (LAS unsigned*)(lds + (bufoff) + ldsw + _i * 8192), 16, 0, 0); } while (0)
; #define GM_LDA(dst, b, h) do { _Pragma("unroll") for (int m = 0; m < 4; ++m) _Pragma("unroll") for (int k = 0; k < 2; ++k) dst[m][k] = *(const LAS s16x8*)(lds + GM_SA(b, h) + aoff + m * 2048 + k * 1024); } while (0)
; #define GM_LDB(dst, b, h) do { _Pragma("unroll") for (int n = 0; n < 2; ++n) _Pragma("unroll") for (int k = 0; k < 2; ++k) dst[n][k] = *(const LAS s16x8*)(lds + GM_SB(b, h) + boff + n * 2048 + k * 1024); } while (0)
; #define GM_MMA(ai, bj, At, Bt) do { __builtin_amdgcn_s_setprio(1); _Pragma("unroll") for (int m = 0; m < 4; ++m) _Pragma("unroll") for (int n = 0; n < 2; ++n) _Pragma("unroll") for (int k = 0; k < 2; ++k) \
;         acc[ai][bj][m][n] = mma16<BF>(Bt[n][k], At[m][k], acc[ai][bj][m][n]); __builtin_amdgcn_s_setprio(0); } while (0)
; #define GM_WAIT_V(n) asm volatile("s_waitcnt vmcnt(" #n ")" ::: "memory")
; #define GM_BAR __builtin_amdgcn_s_barrier()
; template <bool BF, bool GATHER = false, class Epi, class Hook>
; __device__ __forceinline__ void gemm_phase(LAS unsigned char* lds, const Gemm g, const Order& S, const Epi& E, Hook& HK) {
;     ...
;         for (int t = 0; t < nt; t += 2) {
;             const bool last = (t == nt - 2);
;             const char* a1 = cA + (size_t)(t + 1) * kstep;
;             const char* a2 = last ? nA : cA + (size_t)(t + 2) * kstep; const char* b2 = last ? nB : cB + (size_t)(t + 2) * kstep;
;             const char* a3 = a2 + kstep; const char* b3 = b2 + kstep;
;             unsigned s0[2], s1[2];
;             if constexpr (GATHER) { s0[0] = last ? nA0[0] : gA0[0]; s0[1] = last ? nA0[1] : gA0[1]; s1[0] = last ? nA1[0] : gA1[0]; s1[1] = last ? nA1[1] : gA1[1]; }
;             GM_LDB(B0, 0, 0); GM_LDB(B1, 0, 1); GM_SCHED; GM_LDA(At, 0, 0); GM_STA_H1(GM_SA(1, 1), a1, gA1);
;             GM_WAIT_V(8); GM_WAIT_L(0); GM_BAR; GM_MMA(0, 0, At, B0); GM_MMA(0, 1, At, B1); GM_BAR; GM_SCHED;
;             GM_LDA(At, 0, 1); GM_STAGE(GM_SB(0, 0), b2, voffB); GM_STAGE(GM_SB(0, 1), b2 + hstepB, voffB); GM_STA_H0(GM_SA(0, 0), a2, s0);
;             GM_WAIT_V(8); GM_WAIT_L(0); GM_BAR; GM_MMA(1, 0, At, B0); GM_MMA(1, 1, At, B1); GM_BAR; GM_SCHED;
.LBB0_1102:
	s_add_u32 s22, s2, 0x100
	s_addc_u32 s23, s3, 0
	s_cmp_eq_u32 s51, 40
	s_cselect_b32 s27, s7, s23
	s_cselect_b32 s26, s6, s22
	s_cselect_b32 s25, s21, s50
	s_cselect_b32 s24, s20, s49
	v_lshl_add_u64 v[216:217], s[2:3], 0, v[138:139]
	s_add_i32 m0, s29, 0xc000
	global_load_lds_dwordx4 v[216:217], off
	v_lshl_add_u64 v[216:217], s[2:3], 0, v[140:141]
	s_add_i32 m0, s29, 0xe000
	s_nop 0
	global_load_lds_dwordx4 v[216:217], off
	ds_read_b128 v[146:149], v153
	ds_read_b128 v[156:159], v153 offset:1024
	ds_read_b128 v[160:163], v153 offset:2048
	ds_read_b128 v[164:167], v153 offset:3072
	ds_read_b128 v[168:171], v154
	ds_read_b128 v[172:175], v154 offset:1024
	ds_read_b128 v[176:179], v154 offset:2048
	ds_read_b128 v[180:183], v154 offset:3072
	ds_read_b128 v[184:187], v155
	ds_read_b128 v[188:191], v155 offset:1024
	ds_read_b128 v[192:195], v155 offset:2048
	ds_read_b128 v[196:199], v155 offset:3072
	ds_read_b128 v[200:203], v155 offset:4096
	ds_read_b128 v[204:207], v155 offset:5120
	ds_read_b128 v[208:211], v155 offset:6144
	ds_read_b128 v[212:215], v155 offset:7168
	s_waitcnt vmcnt(8)
	s_waitcnt lgkmcnt(0)
	s_barrier
	s_setprio 1
	s_waitcnt lgkmcnt(0)
	v_mfma_f32_16x16x32_bf16 v[126:129], v[146:149], v[184:187], v[126:129]
	v_mfma_f32_16x16x32_bf16 v[122:125], v[160:163], v[184:187], v[122:125]
	v_mfma_f32_16x16x32_bf16 v[110:113], v[146:149], v[192:195], v[110:113]
	v_mfma_f32_16x16x32_bf16 v[106:109], v[160:163], v[192:195], v[106:109]
	v_mfma_f32_16x16x32_bf16 v[94:97], v[146:149], v[200:203], v[94:97]
	v_mfma_f32_16x16x32_bf16 v[90:93], v[160:163], v[200:203], v[90:93]
	v_mfma_f32_16x16x32_bf16 v[78:81], v[146:149], v[208:211], v[78:81]
	v_mfma_f32_16x16x32_bf16 v[74:77], v[160:163], v[208:211], v[74:77]
	v_mfma_f32_16x16x32_bf16 v[126:129], v[156:159], v[188:191], v[126:129]
	v_mfma_f32_16x16x32_bf16 v[122:125], v[164:167], v[188:191], v[122:125]
	v_mfma_f32_16x16x32_bf16 v[110:113], v[156:159], v[196:199], v[110:113]
	v_mfma_f32_16x16x32_bf16 v[106:109], v[164:167], v[196:199], v[106:109]
	v_mfma_f32_16x16x32_bf16 v[94:97], v[156:159], v[204:207], v[94:97]
	v_mfma_f32_16x16x32_bf16 v[90:93], v[164:167], v[204:207], v[90:93]
	v_mfma_f32_16x16x32_bf16 v[78:81], v[156:159], v[212:215], v[78:81]
	v_mfma_f32_16x16x32_bf16 v[74:77], v[164:167], v[212:215], v[74:77]
	s_setprio 0
	s_setprio 1
	v_mfma_f32_16x16x32_bf16 v[118:121], v[168:171], v[184:187], v[118:121]
	v_mfma_f32_16x16x32_bf16 v[114:117], v[176:179], v[184:187], v[114:117]
	v_mfma_f32_16x16x32_bf16 v[102:105], v[168:171], v[192:195], v[102:105]
	v_mfma_f32_16x16x32_bf16 v[98:101], v[176:179], v[192:195], v[98:101]
	v_mfma_f32_16x16x32_bf16 v[86:89], v[168:171], v[200:203], v[86:89]
	v_mfma_f32_16x16x32_bf16 v[82:85], v[176:179], v[200:203], v[82:85]
	v_mfma_f32_16x16x32_bf16 v[70:73], v[168:171], v[208:211], v[70:73]
	v_mfma_f32_16x16x32_bf16 v[66:69], v[176:179], v[208:211], v[66:69]
	v_mfma_f32_16x16x32_bf16 v[118:121], v[172:175], v[188:191], v[118:121]
	v_mfma_f32_16x16x32_bf16 v[114:117], v[180:183], v[188:191], v[114:117]
	v_mfma_f32_16x16x32_bf16 v[102:105], v[172:175], v[196:199], v[102:105]
	v_mfma_f32_16x16x32_bf16 v[98:101], v[180:183], v[196:199], v[98:101]
	v_mfma_f32_16x16x32_bf16 v[86:89], v[172:175], v[204:207], v[86:89]
	v_mfma_f32_16x16x32_bf16 v[82:85], v[180:183], v[204:207], v[82:85]
	v_mfma_f32_16x16x32_bf16 v[70:73], v[172:175], v[212:215], v[70:73]
	v_mfma_f32_16x16x32_bf16 v[66:69], v[180:183], v[212:215], v[66:69]
	s_setprio 0
	s_barrier
	s_add_i32 s2, s42, s28
	v_lshl_add_u64 v[216:217], s[24:25], 0, v[132:133]
	s_mov_b32 m0, s2
	global_load_lds_dwordx4 v[216:217], off
	s_add_i32 m0, s2, 0x2000
	s_add_u32 s2, s24, 0xb0000
	v_lshl_add_u64 v[218:219], s[24:25], 0, v[136:137]
	s_addc_u32 s3, s25, 0
	s_add_i32 s52, s43, s28
	global_load_lds_dwordx4 v[218:219], off
	v_lshl_add_u64 v[220:221], s[2:3], 0, v[132:133]
	s_mov_b32 m0, s52
	v_lshl_add_u64 v[222:223], s[26:27], 0, v[134:135]
	global_load_lds_dwordx4 v[220:221], off
	v_lshl_add_u64 v[220:221], s[2:3], 0, v[136:137]
	s_add_i32 m0, s52, 0x2000
	s_nop 0
	global_load_lds_dwordx4 v[220:221], off
	v_lshl_add_u64 v[220:221], s[26:27], 0, v[130:131]
	s_mov_b32 m0, s29
	s_nop 0
	global_load_lds_dwordx4 v[220:221], off
	s_mov_b32 m0, s30
	s_nop 0
	global_load_lds_dwordx4 v[222:223], off
	ds_read_b128 v[184:187], v155 offset:16384
	ds_read_b128 v[188:191], v155 offset:17408
	ds_read_b128 v[192:195], v155 offset:18432
	ds_read_b128 v[196:199], v155 offset:19456
	ds_read_b128 v[200:203], v155 offset:20480
	ds_read_b128 v[204:207], v155 offset:21504
	ds_read_b128 v[208:211], v155 offset:22528
	ds_read_b128 v[212:215], v155 offset:23552
	s_waitcnt vmcnt(8)
	s_waitcnt lgkmcnt(0)
	s_barrier
; #define GM_LDA(dst, b, h) do { _Pragma("unroll") for (int m = 0; m < 4; ++m) _Pragma("unroll") for (int k = 0; k < 2; ++k) dst[m][k] = *(const LAS s16x8*)(lds + GM_SA(b, h) + aoff + m * 2048 + k * 1024); } while (0)
; #define GM_LDB(dst, b, h) do { _Pragma("unroll") for (int n = 0; n < 2; ++n) _Pragma("unroll") for (int k = 0; k < 2; ++k) dst[n][k] = *(const LAS s16x8*)(lds + GM_SB(b, h) + boff + n * 2048 + k * 1024); } while (0)
; #define GM_MMA(ai, bj, At, Bt) do { __builtin_amdgcn_s_setprio(1); _Pragma("unroll") for (int m = 0; m < 4; ++m) _Pragma("unroll") for (int n = 0; n < 2; ++n) _Pragma("unroll") for (int k = 0; k < 2; ++k) \
;         acc[ai][bj][m][n] = mma16<BF>(Bt[n][k], At[m][k], acc[ai][bj][m][n]); __builtin_amdgcn_s_setprio(0); } while (0)
; #define GM_WAIT_V(n) asm volatile("s_waitcnt vmcnt(" #n ")" ::: "memory")
; #define GM_WAIT_L(n) asm volatile("s_waitcnt lgkmcnt(" #n ")" ::: "memory")
; #define GM_BAR __builtin_amdgcn_s_barrier()
; #define GM_SCHED __builtin_amdgcn_sched_barrier(0)
; #define GM_STA_H1(buf, p, o1) do { if constexpr (GATHER) GM_STAGE(buf, p, o1); else GM_STAGE(buf, (p) + hstepB, voffA); } while (0)
; template <bool BF, bool GATHER = false, class Epi, class Hook>
; __device__ __forceinline__ void gemm_phase(LAS unsigned char* lds, const Gemm g, const Order& S, const Epi& E, Hook& HK) {
;     ...
;             GM_WAIT_V(8); GM_WAIT_L(0); GM_BAR; GM_MMA(1, 0, At, B0); GM_MMA(1, 1, At, B1); GM_BAR; GM_SCHED;
;             GM_LDB(B0, 1, 0); GM_LDB(B1, 1, 1); GM_SCHED; GM_LDA(At, 1, 0); GM_STA_H1(GM_SA(0, 1), a2, s1);
;             GM_WAIT_V(8); GM_WAIT_L(0); GM_BAR; GM_MMA(0, 0, At, B0); GM_MMA(0, 1, At, B1); GM_BAR; GM_SCHED;
	s_setprio 1
	s_waitcnt lgkmcnt(0)
	v_mfma_f32_16x16x32_bf16 v[62:65], v[146:149], v[184:187], v[62:65]
	v_mfma_f32_16x16x32_bf16 v[58:61], v[160:163], v[184:187], v[58:61]
	v_mfma_f32_16x16x32_bf16 v[46:49], v[146:149], v[192:195], v[46:49]
	v_mfma_f32_16x16x32_bf16 v[42:45], v[160:163], v[192:195], v[42:45]
	v_mfma_f32_16x16x32_bf16 v[30:33], v[146:149], v[200:203], v[30:33]
	v_mfma_f32_16x16x32_bf16 v[26:29], v[160:163], v[200:203], v[26:29]
	v_mfma_f32_16x16x32_bf16 v[14:17], v[146:149], v[208:211], v[14:17]
	v_mfma_f32_16x16x32_bf16 v[10:13], v[160:163], v[208:211], v[10:13]
	v_mfma_f32_16x16x32_bf16 v[62:65], v[156:159], v[188:191], v[62:65]
	v_mfma_f32_16x16x32_bf16 v[58:61], v[164:167], v[188:191], v[58:61]
	v_mfma_f32_16x16x32_bf16 v[46:49], v[156:159], v[196:199], v[46:49]
	v_mfma_f32_16x16x32_bf16 v[42:45], v[164:167], v[196:199], v[42:45]
	v_mfma_f32_16x16x32_bf16 v[30:33], v[156:159], v[204:207], v[30:33]
	v_mfma_f32_16x16x32_bf16 v[26:29], v[164:167], v[204:207], v[26:29]
	v_mfma_f32_16x16x32_bf16 v[14:17], v[156:159], v[212:215], v[14:17]
	v_mfma_f32_16x16x32_bf16 v[10:13], v[164:167], v[212:215], v[10:13]
	s_setprio 0
	s_setprio 1
	v_mfma_f32_16x16x32_bf16 v[54:57], v[168:171], v[184:187], v[54:57]
	v_mfma_f32_16x16x32_bf16 v[50:53], v[176:179], v[184:187], v[50:53]
	v_mfma_f32_16x16x32_bf16 v[38:41], v[168:171], v[192:195], v[38:41]
	v_mfma_f32_16x16x32_bf16 v[34:37], v[176:179], v[192:195], v[34:37]
	v_mfma_f32_16x16x32_bf16 v[22:25], v[168:171], v[200:203], v[22:25]
	v_mfma_f32_16x16x32_bf16 v[18:21], v[176:179], v[200:203], v[18:21]
	v_mfma_f32_16x16x32_bf16 v[6:9], v[168:171], v[208:211], v[6:9]
	v_mfma_f32_16x16x32_bf16 v[2:5], v[176:179], v[208:211], v[2:5]
	v_mfma_f32_16x16x32_bf16 v[54:57], v[172:175], v[188:191], v[54:57]
	v_mfma_f32_16x16x32_bf16 v[50:53], v[180:183], v[188:191], v[50:53]
	v_mfma_f32_16x16x32_bf16 v[38:41], v[172:175], v[196:199], v[38:41]
	v_mfma_f32_16x16x32_bf16 v[34:37], v[180:183], v[196:199], v[34:37]
	v_mfma_f32_16x16x32_bf16 v[22:25], v[172:175], v[204:207], v[22:25]
	v_mfma_f32_16x16x32_bf16 v[18:21], v[180:183], v[204:207], v[18:21]
	v_mfma_f32_16x16x32_bf16 v[6:9], v[172:175], v[212:215], v[6:9]
	v_mfma_f32_16x16x32_bf16 v[2:5], v[180:183], v[212:215], v[2:5]
	s_setprio 0
	s_barrier
	s_add_u32 s2, s26, 0xb0000
	s_addc_u32 s3, s27, 0
	s_mov_b32 m0, s31
	v_lshl_add_u64 v[224:225], s[2:3], 0, v[130:131]
	global_load_lds_dwordx4 v[224:225], off
	v_lshl_add_u64 v[224:225], s[2:3], 0, v[134:135]
	s_mov_b32 m0, s33
	s_nop 0
	global_load_lds_dwordx4 v[224:225], off
	s_mov_b32 s53, 0x1c000
	s_mov_b32 s52, 0x18000
	v_add_u32_e32 v244, s52, v150
	v_add_u32_e32 v245, s53, v150
	ds_read_b128 v[146:149], v244
	ds_read_b128 v[156:159], v244 offset:1024
	ds_read_b128 v[160:163], v244 offset:2048
	ds_read_b128 v[164:167], v244 offset:3072
	ds_read_b128 v[168:171], v245
	ds_read_b128 v[172:175], v245 offset:1024
	ds_read_b128 v[176:179], v245 offset:2048
	ds_read_b128 v[180:183], v245 offset:3072
	ds_read_b128 v[184:187], v155 offset:32768
	ds_read_b128 v[188:191], v155 offset:33792
	ds_read_b128 v[192:195], v155 offset:34816
	ds_read_b128 v[196:199], v155 offset:35840
	ds_read_b128 v[200:203], v155 offset:36864
	ds_read_b128 v[204:207], v155 offset:37888
	ds_read_b128 v[208:211], v155 offset:38912
	ds_read_b128 v[212:215], v155 offset:39936
	s_waitcnt vmcnt(8)
	s_waitcnt lgkmcnt(0)
	s_barrier
	s_setprio 1
	s_waitcnt lgkmcnt(0)
	v_mfma_f32_16x16x32_bf16 v[126:129], v[146:149], v[184:187], v[126:129]
	v_mfma_f32_16x16x32_bf16 v[122:125], v[160:163], v[184:187], v[122:125]
	v_mfma_f32_16x16x32_bf16 v[110:113], v[146:149], v[192:195], v[110:113]
	v_mfma_f32_16x16x32_bf16 v[106:109], v[160:163], v[192:195], v[106:109]
	v_mfma_f32_16x16x32_bf16 v[94:97], v[146:149], v[200:203], v[94:97]
	v_mfma_f32_16x16x32_bf16 v[90:93], v[160:163], v[200:203], v[90:93]
	v_mfma_f32_16x16x32_bf16 v[78:81], v[146:149], v[208:211], v[78:81]
	v_mfma_f32_16x16x32_bf16 v[74:77], v[160:163], v[208:211], v[74:77]
	v_mfma_f32_16x16x32_bf16 v[126:129], v[156:159], v[188:191], v[126:129]
	v_mfma_f32_16x16x32_bf16 v[122:125], v[164:167], v[188:191], v[122:125]
	v_mfma_f32_16x16x32_bf16 v[110:113], v[156:159], v[196:199], v[110:113]
	v_mfma_f32_16x16x32_bf16 v[106:109], v[164:167], v[196:199], v[106:109]
	v_mfma_f32_16x16x32_bf16 v[94:97], v[156:159], v[204:207], v[94:97]
	v_mfma_f32_16x16x32_bf16 v[90:93], v[164:167], v[204:207], v[90:93]
	v_mfma_f32_16x16x32_bf16 v[78:81], v[156:159], v[212:215], v[78:81]
	v_mfma_f32_16x16x32_bf16 v[74:77], v[164:167], v[212:215], v[74:77]
	s_setprio 0
	s_setprio 1
	v_mfma_f32_16x16x32_bf16 v[118:121], v[168:171], v[184:187], v[118:121]
	v_mfma_f32_16x16x32_bf16 v[114:117], v[176:179], v[184:187], v[114:117]
	v_mfma_f32_16x16x32_bf16 v[102:105], v[168:171], v[192:195], v[102:105]
	v_mfma_f32_16x16x32_bf16 v[98:101], v[176:179], v[192:195], v[98:101]
	v_mfma_f32_16x16x32_bf16 v[86:89], v[168:171], v[200:203], v[86:89]
	v_mfma_f32_16x16x32_bf16 v[82:85], v[176:179], v[200:203], v[82:85]
	v_mfma_f32_16x16x32_bf16 v[70:73], v[168:171], v[208:211], v[70:73]
	v_mfma_f32_16x16x32_bf16 v[66:69], v[176:179], v[208:211], v[66:69]
	v_mfma_f32_16x16x32_bf16 v[118:121], v[172:175], v[188:191], v[118:121]
	v_mfma_f32_16x16x32_bf16 v[114:117], v[180:183], v[188:191], v[114:117]
	v_mfma_f32_16x16x32_bf16 v[102:105], v[172:175], v[196:199], v[102:105]
	v_mfma_f32_16x16x32_bf16 v[98:101], v[180:183], v[196:199], v[98:101]
	v_mfma_f32_16x16x32_bf16 v[86:89], v[172:175], v[204:207], v[86:89]
	v_mfma_f32_16x16x32_bf16 v[82:85], v[180:183], v[204:207], v[82:85]
	v_mfma_f32_16x16x32_bf16 v[70:73], v[172:175], v[212:215], v[70:73]
	v_mfma_f32_16x16x32_bf16 v[66:69], v[180:183], v[212:215], v[66:69]
	s_setprio 0
	s_barrier
; #define GM_STAGE(bufoff, gbase, voff) do { _Pragma("unroll") for (int _i = 0; _i < 2; ++_i) \
;         __builtin_amdgcn_global_load_lds((const unsigned*)((const char*)(gbase) + (voff)[_i]), (LAS unsigned*)(lds + (bufoff) + ldsw + _i * 8192), 16, 0, 0); } while (0)
; #define GM_LDA(dst, b, h) do { _Pragma("unroll") for (int m = 0; m < 4; ++m) _Pragma("unroll") for (int k = 0; k < 2; ++k) dst[m][k] = *(const LAS s16x8*)(lds + GM_SA(b, h) + aoff + m * 2048 + k * 1024); } while (0)
; #define GM_MMA(ai, bj, At, Bt) do { __builtin_amdgcn_s_setprio(1); _Pragma("unroll") for (int m = 0; m < 4; ++m) _Pragma("unroll") for (int n = 0; n < 2; ++n) _Pragma("unroll") for (int k = 0; k < 2; ++k) \
;         acc[ai][bj][m][n] = mma16<BF>(Bt[n][k], At[m][k], acc[ai][bj][m][n]); __builtin_amdgcn_s_setprio(0); } while (0)
; #define GM_WAIT_V(n) asm volatile("s_waitcnt vmcnt(" #n ")" ::: "memory")
; #define GM_WAIT_L(n) asm volatile("s_waitcnt lgkmcnt(" #n ")" ::: "memory")
; #define GM_BAR __builtin_amdgcn_s_barrier()
; #define GM_SCHED __builtin_amdgcn_sched_barrier(0)
; #define GM_STA_H0(buf, p, o0) do { if constexpr (GATHER) GM_STAGE(buf, p, o0); else GM_STAGE(buf, p, voffA); } while (0)
; template <bool BF, bool GATHER = false, class Epi, class Hook>
; __device__ __forceinline__ void gemm_phase(LAS unsigned char* lds, const Gemm g, const Order& S, const Epi& E, Hook& HK) {
;     ...
;             GM_LDA(At, 1, 1); GM_STAGE(GM_SB(1, 0), b3, voffB); GM_STAGE(GM_SB(1, 1), b3 + hstepB, voffB); GM_STA_H0(GM_SA(1, 0), a3, s0);
;             GM_WAIT_V(8); GM_WAIT_L(0); GM_BAR; GM_MMA(1, 0, At, B0); GM_MMA(1, 1, At, B1); GM_BAR; GM_SCHED;
;         }
;         if (wr == 0) GM_BAR;
	s_add_i32 s2, s52, s28
	v_lshl_add_u64 v[216:217], v[216:217], 0, s[12:13]
	s_mov_b32 m0, s2
	global_load_lds_dwordx4 v[216:217], off
	s_add_i32 m0, s2, 0x2000
	s_add_u32 s2, s24, 0xb0080
	v_lshl_add_u64 v[216:217], v[218:219], 0, s[12:13]
	s_addc_u32 s3, s25, 0
	s_add_i32 s24, s53, s28
	global_load_lds_dwordx4 v[216:217], off
	v_lshl_add_u64 v[216:217], s[2:3], 0, v[132:133]
	s_mov_b32 m0, s24
	s_nop 0
	global_load_lds_dwordx4 v[216:217], off
	v_lshl_add_u64 v[216:217], s[2:3], 0, v[136:137]
	s_add_i32 m0, s24, 0x2000
	s_nop 0
	global_load_lds_dwordx4 v[216:217], off
	v_lshl_add_u64 v[216:217], v[220:221], 0, s[12:13]
	s_mov_b32 m0, s36
	s_nop 0
	global_load_lds_dwordx4 v[216:217], off
	v_lshl_add_u64 v[216:217], v[222:223], 0, s[12:13]
	s_mov_b32 m0, s37
	s_nop 0
	global_load_lds_dwordx4 v[216:217], off
	ds_read_b128 v[184:187], v155 offset:49152
	ds_read_b128 v[188:191], v155 offset:50176
	ds_read_b128 v[192:195], v155 offset:51200
	ds_read_b128 v[196:199], v155 offset:52224
	ds_read_b128 v[200:203], v155 offset:53248
	ds_read_b128 v[204:207], v155 offset:54272
	ds_read_b128 v[208:211], v155 offset:55296
	ds_read_b128 v[212:215], v155 offset:56320
	s_waitcnt vmcnt(8)
	s_waitcnt lgkmcnt(0)
	s_barrier
	s_setprio 1
	s_waitcnt lgkmcnt(0)
	v_mfma_f32_16x16x32_bf16 v[62:65], v[146:149], v[184:187], v[62:65]
	v_mfma_f32_16x16x32_bf16 v[58:61], v[160:163], v[184:187], v[58:61]
	v_mfma_f32_16x16x32_bf16 v[46:49], v[146:149], v[192:195], v[46:49]
	v_mfma_f32_16x16x32_bf16 v[42:45], v[160:163], v[192:195], v[42:45]
	v_mfma_f32_16x16x32_bf16 v[30:33], v[146:149], v[200:203], v[30:33]
	v_mfma_f32_16x16x32_bf16 v[26:29], v[160:163], v[200:203], v[26:29]
	v_mfma_f32_16x16x32_bf16 v[14:17], v[146:149], v[208:211], v[14:17]
	v_mfma_f32_16x16x32_bf16 v[10:13], v[160:163], v[208:211], v[10:13]
	v_mfma_f32_16x16x32_bf16 v[62:65], v[156:159], v[188:191], v[62:65]
	v_mfma_f32_16x16x32_bf16 v[58:61], v[164:167], v[188:191], v[58:61]
	v_mfma_f32_16x16x32_bf16 v[46:49], v[156:159], v[196:199], v[46:49]
	v_mfma_f32_16x16x32_bf16 v[42:45], v[164:167], v[196:199], v[42:45]
	v_mfma_f32_16x16x32_bf16 v[30:33], v[156:159], v[204:207], v[30:33]
	v_mfma_f32_16x16x32_bf16 v[26:29], v[164:167], v[204:207], v[26:29]
	v_mfma_f32_16x16x32_bf16 v[14:17], v[156:159], v[212:215], v[14:17]
	v_mfma_f32_16x16x32_bf16 v[10:13], v[164:167], v[212:215], v[10:13]
	s_setprio 0
	s_setprio 1
	v_mfma_f32_16x16x32_bf16 v[54:57], v[168:171], v[184:187], v[54:57]
	v_mfma_f32_16x16x32_bf16 v[50:53], v[176:179], v[184:187], v[50:53]
	v_mfma_f32_16x16x32_bf16 v[38:41], v[168:171], v[192:195], v[38:41]
	v_mfma_f32_16x16x32_bf16 v[34:37], v[176:179], v[192:195], v[34:37]
	v_mfma_f32_16x16x32_bf16 v[22:25], v[168:171], v[200:203], v[22:25]
	v_mfma_f32_16x16x32_bf16 v[18:21], v[176:179], v[200:203], v[18:21]
	v_mfma_f32_16x16x32_bf16 v[6:9], v[168:171], v[208:211], v[6:9]
	v_mfma_f32_16x16x32_bf16 v[2:5], v[176:179], v[208:211], v[2:5]
	v_mfma_f32_16x16x32_bf16 v[54:57], v[172:175], v[188:191], v[54:57]
	v_mfma_f32_16x16x32_bf16 v[50:53], v[180:183], v[188:191], v[50:53]
	v_mfma_f32_16x16x32_bf16 v[38:41], v[172:175], v[196:199], v[38:41]
	v_mfma_f32_16x16x32_bf16 v[34:37], v[180:183], v[196:199], v[34:37]
	v_mfma_f32_16x16x32_bf16 v[22:25], v[172:175], v[204:207], v[22:25]
	v_mfma_f32_16x16x32_bf16 v[18:21], v[180:183], v[204:207], v[18:21]
	v_mfma_f32_16x16x32_bf16 v[6:9], v[172:175], v[212:215], v[6:9]
	v_mfma_f32_16x16x32_bf16 v[2:5], v[180:183], v[212:215], v[2:5]
	s_setprio 0
	s_barrier
	s_add_i32 s51, s51, 2
	s_add_u32 s49, s49, 0x100
	s_addc_u32 s50, s50, 0
	s_cmp_gt_u32 s51, 41
	s_mov_b64 s[2:3], s[22:23]
	s_cbranch_scc0 .LBB0_1102
	s_and_b64 vcc, exec, s[14:15]
	s_cbranch_vccz .LBB0_1105
	s_barrier

; #define GM_STAGE(bufoff, gbase, voff) do { _Pragma("unroll") for (int _i = 0; _i < 2; ++_i) \
;         __builtin_amdgcn_global_load_lds((const unsigned*)((const char*)(gbase) + (voff)[_i]), (LAS unsigned*)(lds + (bufoff) + ldsw + _i * 8192), 16, 0, 0); } while (0)
; #define GM_LDA(dst, b, h) do { _Pragma("unroll") for (int m = 0; m < 4; ++m) _Pragma("unroll") for (int k = 0; k < 2; ++k) dst[m][k] = *(const LAS s16x8*)(lds + GM_SA(b, h) + aoff + m * 2048 + k * 1024); } while (0)
; #define GM_LDB(dst, b, h) do { _Pragma("unroll") for (int n = 0; n < 2; ++n) _Pragma("unroll") for (int k = 0; k < 2; ++k) dst[n][k] = *(const LAS s16x8*)(lds + GM_SB(b, h) + boff + n * 2048 + k * 1024); } while (0)
; #define GM_MMA(ai, bj, At, Bt) do { __builtin_amdgcn_s_setprio(1); _Pragma("unroll") for (int m = 0; m < 4; ++m) _Pragma("unroll") for (int n = 0; n < 2; ++n) _Pragma("unroll") for (int k = 0; k < 2; ++k) \
;         acc[ai][bj][m][n] = mma16<BF>(Bt[n][k], At[m][k], acc[ai][bj][m][n]); __builtin_amdgcn_s_setprio(0); } while (0)
; #define GM_WAIT_V(n) asm volatile("s_waitcnt vmcnt(" #n ")" ::: "memory")
; #define GM_BAR __builtin_amdgcn_s_barrier()
; template <bool BF, bool GATHER = false, class Epi, class Hook>
; __device__ __forceinline__ void gemm_phase(LAS unsigned char* lds, const Gemm g, const Order& S, const Epi& E, Hook& HK) {
;     ...
;         for (int t = 0; t < nt; t += 2) {
;             const bool last = (t == nt - 2);
;             const char* a1 = cA + (size_t)(t + 1) * kstep;
;             const char* a2 = last ? nA : cA + (size_t)(t + 2) * kstep; const char* b2 = last ? nB : cB + (size_t)(t + 2) * kstep;
;             const char* a3 = a2 + kstep; const char* b3 = b2 + kstep;
;             unsigned s0[2], s1[2];
;             if constexpr (GATHER) { s0[0] = last ? nA0[0] : gA0[0]; s0[1] = last ? nA0[1] : gA0[1]; s1[0] = last ? nA1[0] : gA1[0]; s1[1] = last ? nA1[1] : gA1[1]; }
;             GM_LDB(B0, 0, 0); GM_LDB(B1, 0, 1); GM_SCHED; GM_LDA(At, 0, 0); GM_STA_H1(GM_SA(1, 1), a1, gA1);
;             GM_WAIT_V(8); GM_WAIT_L(0); GM_BAR; GM_MMA(0, 0, At, B0); GM_MMA(0, 1, At, B1); GM_BAR; GM_SCHED;
;             GM_LDA(At, 0, 1); GM_STAGE(GM_SB(0, 0), b2, voffB); GM_STAGE(GM_SB(0, 1), b2 + hstepB, voffB); GM_STA_H0(GM_SA(0, 0), a2, s0);
;             GM_WAIT_V(8); GM_WAIT_L(0); GM_BAR; GM_MMA(1, 0, At, B0); GM_MMA(1, 1, At, B1); GM_BAR; GM_SCHED;
.LBB0_1281:
	s_add_u32 s22, s20, 0xfffc0080
	s_addc_u32 s23, s21, -1
	s_cmp_eq_u32 s47, 12
	s_cselect_b32 s25, s3, s23
	s_cselect_b32 s24, s13, s22
	s_cselect_b32 s23, s15, s46
	s_cselect_b32 s22, s44, s45
	v_lshl_add_u64 v[218:219], s[20:21], 0, v[140:141]
	s_add_i32 m0, s30, 0xc000
	global_load_lds_dwordx4 v[218:219], off
	v_lshl_add_u64 v[218:219], s[20:21], 0, v[142:143]
	s_add_i32 m0, s30, 0xe000
	s_nop 0
	global_load_lds_dwordx4 v[218:219], off
	ds_read_b128 v[154:157], v151
	ds_read_b128 v[158:161], v151 offset:1024
	ds_read_b128 v[162:165], v151 offset:2048
	ds_read_b128 v[166:169], v151 offset:3072
	ds_read_b128 v[170:173], v152
	ds_read_b128 v[174:177], v152 offset:1024
	ds_read_b128 v[178:181], v152 offset:2048
	ds_read_b128 v[182:185], v152 offset:3072
	ds_read_b128 v[186:189], v153
	ds_read_b128 v[190:193], v153 offset:1024
	ds_read_b128 v[194:197], v153 offset:2048
	ds_read_b128 v[198:201], v153 offset:3072
	ds_read_b128 v[202:205], v153 offset:4096
	ds_read_b128 v[206:209], v153 offset:5120
	ds_read_b128 v[210:213], v153 offset:6144
	ds_read_b128 v[214:217], v153 offset:7168
	s_waitcnt vmcnt(8)
	s_waitcnt lgkmcnt(0)
	s_barrier
	s_setprio 1
	s_waitcnt lgkmcnt(0)
	v_mfma_f32_16x16x32_f16 v[126:129], v[154:157], v[186:189], v[126:129]
	v_mfma_f32_16x16x32_f16 v[118:121], v[162:165], v[186:189], v[118:121]
	v_mfma_f32_16x16x32_f16 v[110:113], v[154:157], v[194:197], v[110:113]
	v_mfma_f32_16x16x32_f16 v[102:105], v[162:165], v[194:197], v[102:105]
	v_mfma_f32_16x16x32_f16 v[94:97], v[154:157], v[202:205], v[94:97]
	v_mfma_f32_16x16x32_f16 v[86:89], v[162:165], v[202:205], v[86:89]
	v_mfma_f32_16x16x32_f16 v[78:81], v[154:157], v[210:213], v[78:81]
	v_mfma_f32_16x16x32_f16 v[70:73], v[162:165], v[210:213], v[70:73]
	v_mfma_f32_16x16x32_f16 v[126:129], v[158:161], v[190:193], v[126:129]
	v_mfma_f32_16x16x32_f16 v[118:121], v[166:169], v[190:193], v[118:121]
	v_mfma_f32_16x16x32_f16 v[110:113], v[158:161], v[198:201], v[110:113]
	v_mfma_f32_16x16x32_f16 v[102:105], v[166:169], v[198:201], v[102:105]
	v_mfma_f32_16x16x32_f16 v[94:97], v[158:161], v[206:209], v[94:97]
	v_mfma_f32_16x16x32_f16 v[86:89], v[166:169], v[206:209], v[86:89]
	v_mfma_f32_16x16x32_f16 v[78:81], v[158:161], v[214:217], v[78:81]
	v_mfma_f32_16x16x32_f16 v[70:73], v[166:169], v[214:217], v[70:73]
	s_setprio 0
	s_setprio 1
	v_mfma_f32_16x16x32_f16 v[122:125], v[170:173], v[186:189], v[122:125]
	v_mfma_f32_16x16x32_f16 v[114:117], v[178:181], v[186:189], v[114:117]
	v_mfma_f32_16x16x32_f16 v[106:109], v[170:173], v[194:197], v[106:109]
	v_mfma_f32_16x16x32_f16 v[98:101], v[178:181], v[194:197], v[98:101]
	v_mfma_f32_16x16x32_f16 v[90:93], v[170:173], v[202:205], v[90:93]
	v_mfma_f32_16x16x32_f16 v[82:85], v[178:181], v[202:205], v[82:85]
	v_mfma_f32_16x16x32_f16 v[74:77], v[170:173], v[210:213], v[74:77]
	v_mfma_f32_16x16x32_f16 v[66:69], v[178:181], v[210:213], v[66:69]
	v_mfma_f32_16x16x32_f16 v[122:125], v[174:177], v[190:193], v[122:125]
	v_mfma_f32_16x16x32_f16 v[114:117], v[182:185], v[190:193], v[114:117]
	v_mfma_f32_16x16x32_f16 v[106:109], v[174:177], v[198:201], v[106:109]
	v_mfma_f32_16x16x32_f16 v[98:101], v[182:185], v[198:201], v[98:101]
	v_mfma_f32_16x16x32_f16 v[90:93], v[174:177], v[206:209], v[90:93]
	v_mfma_f32_16x16x32_f16 v[82:85], v[182:185], v[206:209], v[82:85]
	v_mfma_f32_16x16x32_f16 v[74:77], v[174:177], v[214:217], v[74:77]
	v_mfma_f32_16x16x32_f16 v[66:69], v[182:185], v[214:217], v[66:69]
	s_setprio 0
	s_barrier
	s_add_i32 s48, s40, s28
	v_lshl_add_u64 v[218:219], s[22:23], 0, v[134:135]
	s_mov_b32 m0, s48
	global_load_lds_dwordx4 v[218:219], off
	s_add_i32 m0, s48, 0x2000
	s_add_u32 s48, s22, 0x40000
	v_lshl_add_u64 v[220:221], s[22:23], 0, v[130:131]
	s_addc_u32 s49, s23, 0
	s_add_i32 s50, s41, s28
	global_load_lds_dwordx4 v[220:221], off
	v_lshl_add_u64 v[222:223], s[48:49], 0, v[134:135]
	s_mov_b32 m0, s50
	v_lshl_add_u64 v[224:225], s[24:25], 0, v[132:133]
	global_load_lds_dwordx4 v[222:223], off
	v_lshl_add_u64 v[222:223], s[48:49], 0, v[130:131]
	s_add_i32 m0, s50, 0x2000
	s_nop 0
	global_load_lds_dwordx4 v[222:223], off
	v_lshl_add_u64 v[222:223], s[24:25], 0, v[136:137]
	s_mov_b32 m0, s30
	s_nop 0
	global_load_lds_dwordx4 v[222:223], off
	s_mov_b32 m0, s31
	s_nop 0
	global_load_lds_dwordx4 v[224:225], off
	ds_read_b128 v[186:189], v153 offset:16384
	ds_read_b128 v[190:193], v153 offset:17408
	ds_read_b128 v[194:197], v153 offset:18432
	ds_read_b128 v[198:201], v153 offset:19456
	ds_read_b128 v[202:205], v153 offset:20480
	ds_read_b128 v[206:209], v153 offset:21504
	ds_read_b128 v[210:213], v153 offset:22528
	ds_read_b128 v[214:217], v153 offset:23552
	s_waitcnt vmcnt(8)
	s_waitcnt lgkmcnt(0)
	s_barrier
; #define GM_LDA(dst, b, h) do { _Pragma("unroll") for (int m = 0; m < 4; ++m) _Pragma("unroll") for (int k = 0; k < 2; ++k) dst[m][k] = *(const LAS s16x8*)(lds + GM_SA(b, h) + aoff + m * 2048 + k * 1024); } while (0)
; #define GM_LDB(dst, b, h) do { _Pragma("unroll") for (int n = 0; n < 2; ++n) _Pragma("unroll") for (int k = 0; k < 2; ++k) dst[n][k] = *(const LAS s16x8*)(lds + GM_SB(b, h) + boff + n * 2048 + k * 1024); } while (0)
; #define GM_MMA(ai, bj, At, Bt) do { __builtin_amdgcn_s_setprio(1); _Pragma("unroll") for (int m = 0; m < 4; ++m) _Pragma("unroll") for (int n = 0; n < 2; ++n) _Pragma("unroll") for (int k = 0; k < 2; ++k) \
;         acc[ai][bj][m][n] = mma16<BF>(Bt[n][k], At[m][k], acc[ai][bj][m][n]); __builtin_amdgcn_s_setprio(0); } while (0)
; #define GM_WAIT_V(n) asm volatile("s_waitcnt vmcnt(" #n ")" ::: "memory")
; #define GM_WAIT_L(n) asm volatile("s_waitcnt lgkmcnt(" #n ")" ::: "memory")
; #define GM_BAR __builtin_amdgcn_s_barrier()
; #define GM_SCHED __builtin_amdgcn_sched_barrier(0)
; #define GM_STA_H1(buf, p, o1) do { if constexpr (GATHER) GM_STAGE(buf, p, o1); else GM_STAGE(buf, (p) + hstepB, voffA); } while (0)
; template <bool BF, bool GATHER = false, class Epi, class Hook>
; __device__ __forceinline__ void gemm_phase(LAS unsigned char* lds, const Gemm g, const Order& S, const Epi& E, Hook& HK) {
;     ...
;             GM_WAIT_V(8); GM_WAIT_L(0); GM_BAR; GM_MMA(1, 0, At, B0); GM_MMA(1, 1, At, B1); GM_BAR; GM_SCHED;
;             GM_LDB(B0, 1, 0); GM_LDB(B1, 1, 1); GM_SCHED; GM_LDA(At, 1, 0); GM_STA_H1(GM_SA(0, 1), a2, s1);
;             GM_WAIT_V(8); GM_WAIT_L(0); GM_BAR; GM_MMA(0, 0, At, B0); GM_MMA(0, 1, At, B1); GM_BAR; GM_SCHED;
	s_setprio 1
	s_waitcnt lgkmcnt(0)
	v_mfma_f32_16x16x32_f16 v[62:65], v[154:157], v[186:189], v[62:65]
	v_mfma_f32_16x16x32_f16 v[54:57], v[162:165], v[186:189], v[54:57]
	v_mfma_f32_16x16x32_f16 v[46:49], v[154:157], v[194:197], v[46:49]
	v_mfma_f32_16x16x32_f16 v[38:41], v[162:165], v[194:197], v[38:41]
	v_mfma_f32_16x16x32_f16 v[30:33], v[154:157], v[202:205], v[30:33]
	v_mfma_f32_16x16x32_f16 v[22:25], v[162:165], v[202:205], v[22:25]
	v_mfma_f32_16x16x32_f16 v[14:17], v[154:157], v[210:213], v[14:17]
	v_mfma_f32_16x16x32_f16 v[6:9], v[162:165], v[210:213], v[6:9]
	v_mfma_f32_16x16x32_f16 v[62:65], v[158:161], v[190:193], v[62:65]
	v_mfma_f32_16x16x32_f16 v[54:57], v[166:169], v[190:193], v[54:57]
	v_mfma_f32_16x16x32_f16 v[46:49], v[158:161], v[198:201], v[46:49]
	v_mfma_f32_16x16x32_f16 v[38:41], v[166:169], v[198:201], v[38:41]
	v_mfma_f32_16x16x32_f16 v[30:33], v[158:161], v[206:209], v[30:33]
	v_mfma_f32_16x16x32_f16 v[22:25], v[166:169], v[206:209], v[22:25]
	v_mfma_f32_16x16x32_f16 v[14:17], v[158:161], v[214:217], v[14:17]
	v_mfma_f32_16x16x32_f16 v[6:9], v[166:169], v[214:217], v[6:9]
	s_setprio 0
	s_setprio 1
	v_mfma_f32_16x16x32_f16 v[58:61], v[170:173], v[186:189], v[58:61]
	v_mfma_f32_16x16x32_f16 v[50:53], v[178:181], v[186:189], v[50:53]
	v_mfma_f32_16x16x32_f16 v[42:45], v[170:173], v[194:197], v[42:45]
	v_mfma_f32_16x16x32_f16 v[34:37], v[178:181], v[194:197], v[34:37]
	v_mfma_f32_16x16x32_f16 v[26:29], v[170:173], v[202:205], v[26:29]
	v_mfma_f32_16x16x32_f16 v[18:21], v[178:181], v[202:205], v[18:21]
	v_mfma_f32_16x16x32_f16 v[10:13], v[170:173], v[210:213], v[10:13]
	v_mfma_f32_16x16x32_f16 v[2:5], v[178:181], v[210:213], v[2:5]
	v_mfma_f32_16x16x32_f16 v[58:61], v[174:177], v[190:193], v[58:61]
	v_mfma_f32_16x16x32_f16 v[50:53], v[182:185], v[190:193], v[50:53]
	v_mfma_f32_16x16x32_f16 v[42:45], v[174:177], v[198:201], v[42:45]
	v_mfma_f32_16x16x32_f16 v[34:37], v[182:185], v[198:201], v[34:37]
	v_mfma_f32_16x16x32_f16 v[26:29], v[174:177], v[206:209], v[26:29]
	v_mfma_f32_16x16x32_f16 v[18:21], v[182:185], v[206:209], v[18:21]
	v_mfma_f32_16x16x32_f16 v[10:13], v[174:177], v[214:217], v[10:13]
	v_mfma_f32_16x16x32_f16 v[2:5], v[182:185], v[214:217], v[2:5]
	s_setprio 0
	s_barrier
	s_add_u32 s24, s24, 0x40000
	s_addc_u32 s25, s25, 0
	s_mov_b32 m0, s33
	v_lshl_add_u64 v[226:227], s[24:25], 0, v[136:137]
	global_load_lds_dwordx4 v[226:227], off
	v_lshl_add_u64 v[226:227], s[24:25], 0, v[132:133]
	s_mov_b32 m0, s34
	s_nop 0
	global_load_lds_dwordx4 v[226:227], off
	s_mov_b32 s49, 0x1c000
	s_mov_b32 s48, 0x18000
	v_add_u32_e32 v244, s48, v148
	ds_read_b128 v[154:157], v244
	ds_read_b128 v[158:161], v244 offset:1024
	ds_read_b128 v[162:165], v244 offset:2048
	ds_read_b128 v[166:169], v244 offset:3072
	v_add_u32_e32 v244, s49, v148
	ds_read_b128 v[170:173], v244
	ds_read_b128 v[174:177], v244 offset:1024
	ds_read_b128 v[178:181], v244 offset:2048
	ds_read_b128 v[182:185], v244 offset:3072
	ds_read_b128 v[186:189], v153 offset:32768
	ds_read_b128 v[190:193], v153 offset:33792
	ds_read_b128 v[194:197], v153 offset:34816
	ds_read_b128 v[198:201], v153 offset:35840
	ds_read_b128 v[202:205], v153 offset:36864
	ds_read_b128 v[206:209], v153 offset:37888
	ds_read_b128 v[210:213], v153 offset:38912
	ds_read_b128 v[214:217], v153 offset:39936
	s_waitcnt vmcnt(8)
	s_waitcnt lgkmcnt(0)
	s_barrier
	s_setprio 1
	s_waitcnt lgkmcnt(0)
	v_mfma_f32_16x16x32_f16 v[126:129], v[154:157], v[186:189], v[126:129]
	v_mfma_f32_16x16x32_f16 v[118:121], v[162:165], v[186:189], v[118:121]
	v_mfma_f32_16x16x32_f16 v[110:113], v[154:157], v[194:197], v[110:113]
	v_mfma_f32_16x16x32_f16 v[102:105], v[162:165], v[194:197], v[102:105]
	v_mfma_f32_16x16x32_f16 v[94:97], v[154:157], v[202:205], v[94:97]
	v_mfma_f32_16x16x32_f16 v[86:89], v[162:165], v[202:205], v[86:89]
	v_mfma_f32_16x16x32_f16 v[78:81], v[154:157], v[210:213], v[78:81]
	v_mfma_f32_16x16x32_f16 v[70:73], v[162:165], v[210:213], v[70:73]
	v_mfma_f32_16x16x32_f16 v[126:129], v[158:161], v[190:193], v[126:129]
	v_mfma_f32_16x16x32_f16 v[118:121], v[166:169], v[190:193], v[118:121]
	v_mfma_f32_16x16x32_f16 v[110:113], v[158:161], v[198:201], v[110:113]
	v_mfma_f32_16x16x32_f16 v[102:105], v[166:169], v[198:201], v[102:105]
	v_mfma_f32_16x16x32_f16 v[94:97], v[158:161], v[206:209], v[94:97]
	v_mfma_f32_16x16x32_f16 v[86:89], v[166:169], v[206:209], v[86:89]
	v_mfma_f32_16x16x32_f16 v[78:81], v[158:161], v[214:217], v[78:81]
	v_mfma_f32_16x16x32_f16 v[70:73], v[166:169], v[214:217], v[70:73]
	s_setprio 0
	s_setprio 1
	v_mfma_f32_16x16x32_f16 v[122:125], v[170:173], v[186:189], v[122:125]
	v_mfma_f32_16x16x32_f16 v[114:117], v[178:181], v[186:189], v[114:117]
	v_mfma_f32_16x16x32_f16 v[106:109], v[170:173], v[194:197], v[106:109]
	v_mfma_f32_16x16x32_f16 v[98:101], v[178:181], v[194:197], v[98:101]
	v_mfma_f32_16x16x32_f16 v[90:93], v[170:173], v[202:205], v[90:93]
	v_mfma_f32_16x16x32_f16 v[82:85], v[178:181], v[202:205], v[82:85]
	v_mfma_f32_16x16x32_f16 v[74:77], v[170:173], v[210:213], v[74:77]
	v_mfma_f32_16x16x32_f16 v[66:69], v[178:181], v[210:213], v[66:69]
	v_mfma_f32_16x16x32_f16 v[122:125], v[174:177], v[190:193], v[122:125]
	v_mfma_f32_16x16x32_f16 v[114:117], v[182:185], v[190:193], v[114:117]
	v_mfma_f32_16x16x32_f16 v[106:109], v[174:177], v[198:201], v[106:109]
	v_mfma_f32_16x16x32_f16 v[98:101], v[182:185], v[198:201], v[98:101]
	v_mfma_f32_16x16x32_f16 v[90:93], v[174:177], v[206:209], v[90:93]
	v_mfma_f32_16x16x32_f16 v[82:85], v[182:185], v[206:209], v[82:85]
	v_mfma_f32_16x16x32_f16 v[74:77], v[174:177], v[214:217], v[74:77]
	v_mfma_f32_16x16x32_f16 v[66:69], v[182:185], v[214:217], v[66:69]
	s_setprio 0
	s_barrier
; #define GM_STAGE(bufoff, gbase, voff) do { _Pragma("unroll") for (int _i = 0; _i < 2; ++_i) \
;         __builtin_amdgcn_global_load_lds((const unsigned*)((const char*)(gbase) + (voff)[_i]), (LAS unsigned*)(lds + (bufoff) + ldsw + _i * 8192), 16, 0, 0); } while (0)
; #define GM_LDA(dst, b, h) do { _Pragma("unroll") for (int m = 0; m < 4; ++m) _Pragma("unroll") for (int k = 0; k < 2; ++k) dst[m][k] = *(const LAS s16x8*)(lds + GM_SA(b, h) + aoff + m * 2048 + k * 1024); } while (0)
; #define GM_MMA(ai, bj, At, Bt) do { __builtin_amdgcn_s_setprio(1); _Pragma("unroll") for (int m = 0; m < 4; ++m) _Pragma("unroll") for (int n = 0; n < 2; ++n) _Pragma("unroll") for (int k = 0; k < 2; ++k) \
;         acc[ai][bj][m][n] = mma16<BF>(Bt[n][k], At[m][k], acc[ai][bj][m][n]); __builtin_amdgcn_s_setprio(0); } while (0)
; #define GM_WAIT_V(n) asm volatile("s_waitcnt vmcnt(" #n ")" ::: "memory")
; #define GM_WAIT_L(n) asm volatile("s_waitcnt lgkmcnt(" #n ")" ::: "memory")
; #define GM_BAR __builtin_amdgcn_s_barrier()
; #define GM_SCHED __builtin_amdgcn_sched_barrier(0)
; #define GM_STA_H0(buf, p, o0) do { if constexpr (GATHER) GM_STAGE(buf, p, o0); else GM_STAGE(buf, p, voffA); } while (0)
;     __device__ __forceinline__ void operator()(const Acc& acc, const Unit& u, int wr, int wc, int fr, int fq) const {
;         const int row0 = u.pm * BM + wr * 64 + fr;
;         if (u.pn < 8) {
;             const int col0 = (u.pn < 4 ? 0 : 512) + 128 * (u.pn & 3) + wc * 32 + 8 * fq; const bool glu = u.pn >= 4;
; template <bool BF, bool GATHER = false, class Epi, class Hook>
; __device__ __forceinline__ void gemm_phase(LAS unsigned char* lds, const Gemm g, const Order& S, const Epi& E, Hook& HK) {
;     ...
;             GM_LDA(At, 1, 1); GM_STAGE(GM_SB(1, 0), b3, voffB); GM_STAGE(GM_SB(1, 1), b3 + hstepB, voffB); GM_STA_H0(GM_SA(1, 0), a3, s0);
;             GM_WAIT_V(8); GM_WAIT_L(0); GM_BAR; GM_MMA(1, 0, At, B0); GM_MMA(1, 1, At, B1); GM_BAR; GM_SCHED;
;         }
;         if (wr == 0) GM_BAR;
	s_add_i32 s24, s48, s28
	v_lshl_add_u64 v[218:219], v[218:219], 0, s[8:9]
	s_mov_b32 m0, s24
	global_load_lds_dwordx4 v[218:219], off
	s_add_i32 m0, s24, 0x2000
	s_add_u32 s22, s22, 0x40080
	v_lshl_add_u64 v[218:219], v[220:221], 0, s[8:9]
	s_addc_u32 s23, s23, 0
	s_add_i32 s24, s49, s28
	global_load_lds_dwordx4 v[218:219], off
	v_lshl_add_u64 v[218:219], s[22:23], 0, v[134:135]
	s_mov_b32 m0, s24
	s_nop 0
	global_load_lds_dwordx4 v[218:219], off
	v_lshl_add_u64 v[218:219], s[22:23], 0, v[130:131]
	s_add_i32 m0, s24, 0x2000
	s_nop 0
	global_load_lds_dwordx4 v[218:219], off
	v_lshl_add_u64 v[218:219], v[222:223], 0, s[8:9]
	s_mov_b32 m0, s37
	s_nop 0
	global_load_lds_dwordx4 v[218:219], off
	v_lshl_add_u64 v[218:219], v[224:225], 0, s[8:9]
	s_mov_b32 m0, s38
	s_nop 0
	global_load_lds_dwordx4 v[218:219], off
	ds_read_b128 v[186:189], v153 offset:49152
	ds_read_b128 v[190:193], v153 offset:50176
	ds_read_b128 v[194:197], v153 offset:51200
	ds_read_b128 v[198:201], v153 offset:52224
	ds_read_b128 v[202:205], v153 offset:53248
	ds_read_b128 v[206:209], v153 offset:54272
	ds_read_b128 v[210:213], v153 offset:55296
	ds_read_b128 v[214:217], v153 offset:56320
	s_waitcnt vmcnt(8)
	s_waitcnt lgkmcnt(0)
	s_barrier
	s_setprio 1
	s_waitcnt lgkmcnt(0)
	v_mfma_f32_16x16x32_f16 v[62:65], v[154:157], v[186:189], v[62:65]
	v_mfma_f32_16x16x32_f16 v[54:57], v[162:165], v[186:189], v[54:57]
	v_mfma_f32_16x16x32_f16 v[46:49], v[154:157], v[194:197], v[46:49]
	v_mfma_f32_16x16x32_f16 v[38:41], v[162:165], v[194:197], v[38:41]
	v_mfma_f32_16x16x32_f16 v[30:33], v[154:157], v[202:205], v[30:33]
	v_mfma_f32_16x16x32_f16 v[22:25], v[162:165], v[202:205], v[22:25]
	v_mfma_f32_16x16x32_f16 v[14:17], v[154:157], v[210:213], v[14:17]
	v_mfma_f32_16x16x32_f16 v[6:9], v[162:165], v[210:213], v[6:9]
	v_mfma_f32_16x16x32_f16 v[62:65], v[158:161], v[190:193], v[62:65]
	v_mfma_f32_16x16x32_f16 v[54:57], v[166:169], v[190:193], v[54:57]
	v_mfma_f32_16x16x32_f16 v[46:49], v[158:161], v[198:201], v[46:49]
	v_mfma_f32_16x16x32_f16 v[38:41], v[166:169], v[198:201], v[38:41]
	v_mfma_f32_16x16x32_f16 v[30:33], v[158:161], v[206:209], v[30:33]
	v_mfma_f32_16x16x32_f16 v[22:25], v[166:169], v[206:209], v[22:25]
	v_mfma_f32_16x16x32_f16 v[14:17], v[158:161], v[214:217], v[14:17]
	v_mfma_f32_16x16x32_f16 v[6:9], v[166:169], v[214:217], v[6:9]
	s_setprio 0
	s_setprio 1
	v_mfma_f32_16x16x32_f16 v[58:61], v[170:173], v[186:189], v[58:61]
	v_mfma_f32_16x16x32_f16 v[50:53], v[178:181], v[186:189], v[50:53]
	v_mfma_f32_16x16x32_f16 v[42:45], v[170:173], v[194:197], v[42:45]
	v_mfma_f32_16x16x32_f16 v[34:37], v[178:181], v[194:197], v[34:37]
	v_mfma_f32_16x16x32_f16 v[26:29], v[170:173], v[202:205], v[26:29]
	v_mfma_f32_16x16x32_f16 v[18:21], v[178:181], v[202:205], v[18:21]
	v_mfma_f32_16x16x32_f16 v[10:13], v[170:173], v[210:213], v[10:13]
	v_mfma_f32_16x16x32_f16 v[2:5], v[178:181], v[210:213], v[2:5]
	v_mfma_f32_16x16x32_f16 v[58:61], v[174:177], v[190:193], v[58:61]
	v_mfma_f32_16x16x32_f16 v[50:53], v[182:185], v[190:193], v[50:53]
	v_mfma_f32_16x16x32_f16 v[42:45], v[174:177], v[198:201], v[42:45]
	v_mfma_f32_16x16x32_f16 v[34:37], v[182:185], v[198:201], v[34:37]
	v_mfma_f32_16x16x32_f16 v[26:29], v[174:177], v[206:209], v[26:29]
	v_mfma_f32_16x16x32_f16 v[18:21], v[182:185], v[206:209], v[18:21]
	v_mfma_f32_16x16x32_f16 v[10:13], v[174:177], v[214:217], v[10:13]
	v_mfma_f32_16x16x32_f16 v[2:5], v[182:185], v[214:217], v[2:5]
	s_setprio 0
	s_barrier
	s_add_i32 s47, s47, 2
	s_add_u32 s20, s20, 0x100
	s_addc_u32 s21, s21, 0
	s_add_u32 s45, s45, 0x100
	s_addc_u32 s46, s46, 0
	s_cmp_gt_u32 s47, 13
	s_cbranch_scc0 .LBB0_1281
	s_and_b64 vcc, exec, s[10:11]
	s_cbranch_vccnz .LBB0_1286
	v_lshl_add_u32 v154, s2, 8, v1
	s_cmp_gt_i32 s43, 7
	s_mov_b64 s[2:3], -1
	s_cbranch_scc1 .LBB0_1287

; #define GM_STAGE(bufoff, gbase, voff) do { _Pragma("unroll") for (int _i = 0; _i < 2; ++_i) \
;         __builtin_amdgcn_global_load_lds((const unsigned*)((const char*)(gbase) + (voff)[_i]), (LAS unsigned*)(lds + (bufoff) + ldsw + _i * 8192), 16, 0, 0); } while (0)
; #define GM_LDA(dst, b, h) do { _Pragma("unroll") for (int m = 0; m < 4; ++m) _Pragma("unroll") for (int k = 0; k < 2; ++k) dst[m][k] = *(const LAS s16x8*)(lds + GM_SA(b, h) + aoff + m * 2048 + k * 1024); } while (0)
; #define GM_LDB(dst, b, h) do { _Pragma("unroll") for (int n = 0; n < 2; ++n) _Pragma("unroll") for (int k = 0; k < 2; ++k) dst[n][k] = *(const LAS s16x8*)(lds + GM_SB(b, h) + boff + n * 2048 + k * 1024); } while (0)
; #define GM_MMA(ai, bj, At, Bt) do { __builtin_amdgcn_s_setprio(1); _Pragma("unroll") for (int m = 0; m < 4; ++m) _Pragma("unroll") for (int n = 0; n < 2; ++n) _Pragma("unroll") for (int k = 0; k < 2; ++k) \
;         acc[ai][bj][m][n] = mma16<BF>(Bt[n][k], At[m][k], acc[ai][bj][m][n]); __builtin_amdgcn_s_setprio(0); } while (0)
; #define GM_WAIT_V(n) asm volatile("s_waitcnt vmcnt(" #n ")" ::: "memory")
; #define GM_BAR __builtin_amdgcn_s_barrier()
; template <bool BF, bool GATHER = false, class Epi, class Hook>
; __device__ __forceinline__ void gemm_phase(LAS unsigned char* lds, const Gemm g, const Order& S, const Epi& E, Hook& HK) {
;     ...
;         for (int t = 0; t < nt; t += 2) {
;             const bool last = (t == nt - 2);
;             const char* a1 = cA + (size_t)(t + 1) * kstep;
;             const char* a2 = last ? nA : cA + (size_t)(t + 2) * kstep; const char* b2 = last ? nB : cB + (size_t)(t + 2) * kstep;
;             const char* a3 = a2 + kstep; const char* b3 = b2 + kstep;
;             unsigned s0[2], s1[2];
;             if constexpr (GATHER) { s0[0] = last ? nA0[0] : gA0[0]; s0[1] = last ? nA0[1] : gA0[1]; s1[0] = last ? nA1[0] : gA1[0]; s1[1] = last ? nA1[1] : gA1[1]; }
;             GM_LDB(B0, 0, 0); GM_LDB(B1, 0, 1); GM_SCHED; GM_LDA(At, 0, 0); GM_STA_H1(GM_SA(1, 1), a1, gA1);
;             GM_WAIT_V(8); GM_WAIT_L(0); GM_BAR; GM_MMA(0, 0, At, B0); GM_MMA(0, 1, At, B1); GM_BAR; GM_SCHED;
;             GM_LDA(At, 0, 1); GM_STAGE(GM_SB(0, 0), b2, voffB); GM_STAGE(GM_SB(0, 1), b2 + hstepB, voffB); GM_STA_H0(GM_SA(0, 0), a2, s0);
;             GM_WAIT_V(8); GM_WAIT_L(0); GM_BAR; GM_MMA(1, 0, At, B0); GM_MMA(1, 1, At, B1); GM_BAR; GM_SCHED;
.LBB0_1480:
	s_add_u32 s24, s22, 0xfffc0080
	s_addc_u32 s25, s23, -1
	s_cmp_eq_u32 s49, 12
	s_cselect_b32 s27, s15, s25
	s_cselect_b32 s26, s45, s24
	s_cselect_b32 s25, s17, s48
	s_cselect_b32 s24, s46, s47
	v_lshl_add_u64 v[216:217], s[22:23], 0, v[154:155]
	s_add_i32 m0, s33, 0xc000
	global_load_lds_dwordx4 v[216:217], off
	v_lshl_add_u64 v[216:217], s[22:23], 0, v[156:157]
	s_add_i32 m0, s33, 0xe000
	s_nop 0
	global_load_lds_dwordx4 v[216:217], off
	ds_read_b128 v[122:125], v168
	ds_read_b128 v[126:129], v168 offset:1024
	ds_read_b128 v[130:133], v168 offset:2048
	ds_read_b128 v[134:137], v168 offset:3072
	ds_read_b128 v[162:165], v169
	ds_read_b128 v[172:175], v169 offset:1024
	ds_read_b128 v[176:179], v169 offset:2048
	ds_read_b128 v[180:183], v169 offset:3072
	ds_read_b128 v[184:187], v170
	ds_read_b128 v[188:191], v170 offset:1024
	ds_read_b128 v[192:195], v170 offset:2048
	ds_read_b128 v[196:199], v170 offset:3072
	ds_read_b128 v[200:203], v170 offset:4096
	ds_read_b128 v[204:207], v170 offset:5120
	ds_read_b128 v[208:211], v170 offset:6144
	ds_read_b128 v[212:215], v170 offset:7168
	s_waitcnt vmcnt(8)
	s_waitcnt lgkmcnt(0)
	s_barrier
	s_setprio 1
	s_waitcnt lgkmcnt(0)
	v_mfma_f32_16x16x32_f16 v[142:145], v[122:125], v[184:187], v[142:145]
	v_mfma_f32_16x16x32_f16 v[138:141], v[130:133], v[184:187], v[138:141]
	v_mfma_f32_16x16x32_f16 v[110:113], v[122:125], v[192:195], v[110:113]
	v_mfma_f32_16x16x32_f16 v[106:109], v[130:133], v[192:195], v[106:109]
	v_mfma_f32_16x16x32_f16 v[94:97], v[122:125], v[200:203], v[94:97]
	v_mfma_f32_16x16x32_f16 v[90:93], v[130:133], v[200:203], v[90:93]
	v_mfma_f32_16x16x32_f16 v[78:81], v[122:125], v[208:211], v[78:81]
	v_mfma_f32_16x16x32_f16 v[74:77], v[130:133], v[208:211], v[74:77]
	v_mfma_f32_16x16x32_f16 v[142:145], v[126:129], v[188:191], v[142:145]
	v_mfma_f32_16x16x32_f16 v[138:141], v[134:137], v[188:191], v[138:141]
	v_mfma_f32_16x16x32_f16 v[110:113], v[126:129], v[196:199], v[110:113]
	v_mfma_f32_16x16x32_f16 v[106:109], v[134:137], v[196:199], v[106:109]
	v_mfma_f32_16x16x32_f16 v[94:97], v[126:129], v[204:207], v[94:97]
	v_mfma_f32_16x16x32_f16 v[90:93], v[134:137], v[204:207], v[90:93]
	v_mfma_f32_16x16x32_f16 v[78:81], v[126:129], v[212:215], v[78:81]
	v_mfma_f32_16x16x32_f16 v[74:77], v[134:137], v[212:215], v[74:77]
	s_setprio 0
	s_setprio 1
	v_mfma_f32_16x16x32_f16 v[118:121], v[162:165], v[184:187], v[118:121]
	v_mfma_f32_16x16x32_f16 v[114:117], v[176:179], v[184:187], v[114:117]
	v_mfma_f32_16x16x32_f16 v[102:105], v[162:165], v[192:195], v[102:105]
	v_mfma_f32_16x16x32_f16 v[98:101], v[176:179], v[192:195], v[98:101]
	v_mfma_f32_16x16x32_f16 v[86:89], v[162:165], v[200:203], v[86:89]
	v_mfma_f32_16x16x32_f16 v[82:85], v[176:179], v[200:203], v[82:85]
	v_mfma_f32_16x16x32_f16 v[70:73], v[162:165], v[208:211], v[70:73]
	v_mfma_f32_16x16x32_f16 v[66:69], v[176:179], v[208:211], v[66:69]
	v_mfma_f32_16x16x32_f16 v[118:121], v[172:175], v[188:191], v[118:121]
	v_mfma_f32_16x16x32_f16 v[114:117], v[180:183], v[188:191], v[114:117]
	v_mfma_f32_16x16x32_f16 v[102:105], v[172:175], v[196:199], v[102:105]
	v_mfma_f32_16x16x32_f16 v[98:101], v[180:183], v[196:199], v[98:101]
	v_mfma_f32_16x16x32_f16 v[86:89], v[172:175], v[204:207], v[86:89]
	v_mfma_f32_16x16x32_f16 v[82:85], v[180:183], v[204:207], v[82:85]
	v_mfma_f32_16x16x32_f16 v[70:73], v[172:175], v[212:215], v[70:73]
	v_mfma_f32_16x16x32_f16 v[66:69], v[180:183], v[212:215], v[66:69]
	s_setprio 0
	s_barrier
	s_add_i32 s50, s43, s31
	v_lshl_add_u64 v[216:217], s[24:25], 0, v[148:149]
	s_mov_b32 m0, s50
	global_load_lds_dwordx4 v[216:217], off
	s_add_i32 m0, s50, 0x2000
	s_add_u32 s50, s24, 0x40000
	v_lshl_add_u64 v[218:219], s[24:25], 0, v[152:153]
	s_addc_u32 s51, s25, 0
	s_add_i32 s52, s44, s31
	global_load_lds_dwordx4 v[218:219], off
	v_lshl_add_u64 v[220:221], s[50:51], 0, v[148:149]
	s_mov_b32 m0, s52
	v_lshl_add_u64 v[222:223], s[26:27], 0, v[150:151]
	global_load_lds_dwordx4 v[220:221], off
	v_lshl_add_u64 v[220:221], s[50:51], 0, v[152:153]
	s_add_i32 m0, s52, 0x2000
	s_nop 0
	global_load_lds_dwordx4 v[220:221], off
	v_lshl_add_u64 v[220:221], s[26:27], 0, v[146:147]
	s_mov_b32 m0, s33
	s_nop 0
	global_load_lds_dwordx4 v[220:221], off
	s_mov_b32 m0, s34
	s_nop 0
	global_load_lds_dwordx4 v[222:223], off
	ds_read_b128 v[184:187], v170 offset:16384
	ds_read_b128 v[188:191], v170 offset:17408
	ds_read_b128 v[192:195], v170 offset:18432
	ds_read_b128 v[196:199], v170 offset:19456
	ds_read_b128 v[200:203], v170 offset:20480
	ds_read_b128 v[204:207], v170 offset:21504
	ds_read_b128 v[208:211], v170 offset:22528
	ds_read_b128 v[212:215], v170 offset:23552
	s_waitcnt vmcnt(8)
	s_waitcnt lgkmcnt(0)
	s_barrier
; #define GM_LDA(dst, b, h) do { _Pragma("unroll") for (int m = 0; m < 4; ++m) _Pragma("unroll") for (int k = 0; k < 2; ++k) dst[m][k] = *(const LAS s16x8*)(lds + GM_SA(b, h) + aoff + m * 2048 + k * 1024); } while (0)
; #define GM_LDB(dst, b, h) do { _Pragma("unroll") for (int n = 0; n < 2; ++n) _Pragma("unroll") for (int k = 0; k < 2; ++k) dst[n][k] = *(const LAS s16x8*)(lds + GM_SB(b, h) + boff + n * 2048 + k * 1024); } while (0)
; #define GM_MMA(ai, bj, At, Bt) do { __builtin_amdgcn_s_setprio(1); _Pragma("unroll") for (int m = 0; m < 4; ++m) _Pragma("unroll") for (int n = 0; n < 2; ++n) _Pragma("unroll") for (int k = 0; k < 2; ++k) \
;         acc[ai][bj][m][n] = mma16<BF>(Bt[n][k], At[m][k], acc[ai][bj][m][n]); __builtin_amdgcn_s_setprio(0); } while (0)
; #define GM_WAIT_V(n) asm volatile("s_waitcnt vmcnt(" #n ")" ::: "memory")
; #define GM_WAIT_L(n) asm volatile("s_waitcnt lgkmcnt(" #n ")" ::: "memory")
; #define GM_BAR __builtin_amdgcn_s_barrier()
; #define GM_SCHED __builtin_amdgcn_sched_barrier(0)
; #define GM_STA_H1(buf, p, o1) do { if constexpr (GATHER) GM_STAGE(buf, p, o1); else GM_STAGE(buf, (p) + hstepB, voffA); } while (0)
; template <bool BF, bool GATHER = false, class Epi, class Hook>
; __device__ __forceinline__ void gemm_phase(LAS unsigned char* lds, const Gemm g, const Order& S, const Epi& E, Hook& HK) {
;     ...
;             GM_WAIT_V(8); GM_WAIT_L(0); GM_BAR; GM_MMA(1, 0, At, B0); GM_MMA(1, 1, At, B1); GM_BAR; GM_SCHED;
;             GM_LDB(B0, 1, 0); GM_LDB(B1, 1, 1); GM_SCHED; GM_LDA(At, 1, 0); GM_STA_H1(GM_SA(0, 1), a2, s1);
;             GM_WAIT_V(8); GM_WAIT_L(0); GM_BAR; GM_MMA(0, 0, At, B0); GM_MMA(0, 1, At, B1); GM_BAR; GM_SCHED;
	s_setprio 1
	s_waitcnt lgkmcnt(0)
	v_mfma_f32_16x16x32_f16 v[62:65], v[122:125], v[184:187], v[62:65]
	v_mfma_f32_16x16x32_f16 v[58:61], v[130:133], v[184:187], v[58:61]
	v_mfma_f32_16x16x32_f16 v[46:49], v[122:125], v[192:195], v[46:49]
	v_mfma_f32_16x16x32_f16 v[42:45], v[130:133], v[192:195], v[42:45]
	v_mfma_f32_16x16x32_f16 v[30:33], v[122:125], v[200:203], v[30:33]
	v_mfma_f32_16x16x32_f16 v[26:29], v[130:133], v[200:203], v[26:29]
	v_mfma_f32_16x16x32_f16 v[14:17], v[122:125], v[208:211], v[14:17]
	v_mfma_f32_16x16x32_f16 v[10:13], v[130:133], v[208:211], v[10:13]
	v_mfma_f32_16x16x32_f16 v[62:65], v[126:129], v[188:191], v[62:65]
	v_mfma_f32_16x16x32_f16 v[58:61], v[134:137], v[188:191], v[58:61]
	v_mfma_f32_16x16x32_f16 v[46:49], v[126:129], v[196:199], v[46:49]
	v_mfma_f32_16x16x32_f16 v[42:45], v[134:137], v[196:199], v[42:45]
	v_mfma_f32_16x16x32_f16 v[30:33], v[126:129], v[204:207], v[30:33]
	v_mfma_f32_16x16x32_f16 v[26:29], v[134:137], v[204:207], v[26:29]
	v_mfma_f32_16x16x32_f16 v[14:17], v[126:129], v[212:215], v[14:17]
	v_mfma_f32_16x16x32_f16 v[10:13], v[134:137], v[212:215], v[10:13]
	s_setprio 0
	s_setprio 1
	v_mfma_f32_16x16x32_f16 v[54:57], v[162:165], v[184:187], v[54:57]
	v_mfma_f32_16x16x32_f16 v[50:53], v[176:179], v[184:187], v[50:53]
	v_mfma_f32_16x16x32_f16 v[38:41], v[162:165], v[192:195], v[38:41]
	v_mfma_f32_16x16x32_f16 v[34:37], v[176:179], v[192:195], v[34:37]
	v_mfma_f32_16x16x32_f16 v[22:25], v[162:165], v[200:203], v[22:25]
	v_mfma_f32_16x16x32_f16 v[18:21], v[176:179], v[200:203], v[18:21]
	v_mfma_f32_16x16x32_f16 v[6:9], v[162:165], v[208:211], v[6:9]
	v_mfma_f32_16x16x32_f16 v[2:5], v[176:179], v[208:211], v[2:5]
	v_mfma_f32_16x16x32_f16 v[54:57], v[172:175], v[188:191], v[54:57]
	v_mfma_f32_16x16x32_f16 v[50:53], v[180:183], v[188:191], v[50:53]
	v_mfma_f32_16x16x32_f16 v[38:41], v[172:175], v[196:199], v[38:41]
	v_mfma_f32_16x16x32_f16 v[34:37], v[180:183], v[196:199], v[34:37]
	v_mfma_f32_16x16x32_f16 v[22:25], v[172:175], v[204:207], v[22:25]
	v_mfma_f32_16x16x32_f16 v[18:21], v[180:183], v[204:207], v[18:21]
	v_mfma_f32_16x16x32_f16 v[6:9], v[172:175], v[212:215], v[6:9]
	v_mfma_f32_16x16x32_f16 v[2:5], v[180:183], v[212:215], v[2:5]
	s_setprio 0
	s_barrier
	s_add_u32 s26, s26, 0x40000
	s_addc_u32 s27, s27, 0
	s_mov_b32 m0, s35
	v_lshl_add_u64 v[224:225], s[26:27], 0, v[146:147]
	global_load_lds_dwordx4 v[224:225], off
	v_lshl_add_u64 v[224:225], s[26:27], 0, v[150:151]
	s_mov_b32 m0, s36
	s_nop 0
	global_load_lds_dwordx4 v[224:225], off
	s_mov_b32 s51, 0x1c000
	s_mov_b32 s50, 0x18000
	v_add_u32_e32 v244, s50, v166
	v_add_u32_e32 v245, s51, v166
	ds_read_b128 v[122:125], v244
	ds_read_b128 v[126:129], v244 offset:1024
	ds_read_b128 v[130:133], v244 offset:2048
	ds_read_b128 v[134:137], v244 offset:3072
	ds_read_b128 v[162:165], v245
	ds_read_b128 v[172:175], v245 offset:1024
	ds_read_b128 v[176:179], v245 offset:2048
	ds_read_b128 v[180:183], v245 offset:3072
	ds_read_b128 v[184:187], v170 offset:32768
	ds_read_b128 v[188:191], v170 offset:33792
	ds_read_b128 v[192:195], v170 offset:34816
	ds_read_b128 v[196:199], v170 offset:35840
	ds_read_b128 v[200:203], v170 offset:36864
	ds_read_b128 v[204:207], v170 offset:37888
	ds_read_b128 v[208:211], v170 offset:38912
	ds_read_b128 v[212:215], v170 offset:39936
	s_waitcnt vmcnt(8)
	s_waitcnt lgkmcnt(0)
	s_barrier
	s_setprio 1
	s_waitcnt lgkmcnt(0)
	v_mfma_f32_16x16x32_f16 v[142:145], v[122:125], v[184:187], v[142:145]
	v_mfma_f32_16x16x32_f16 v[138:141], v[130:133], v[184:187], v[138:141]
	v_mfma_f32_16x16x32_f16 v[110:113], v[122:125], v[192:195], v[110:113]
	v_mfma_f32_16x16x32_f16 v[106:109], v[130:133], v[192:195], v[106:109]
	v_mfma_f32_16x16x32_f16 v[94:97], v[122:125], v[200:203], v[94:97]
	v_mfma_f32_16x16x32_f16 v[90:93], v[130:133], v[200:203], v[90:93]
	v_mfma_f32_16x16x32_f16 v[78:81], v[122:125], v[208:211], v[78:81]
	v_mfma_f32_16x16x32_f16 v[74:77], v[130:133], v[208:211], v[74:77]
	v_mfma_f32_16x16x32_f16 v[142:145], v[126:129], v[188:191], v[142:145]
	v_mfma_f32_16x16x32_f16 v[138:141], v[134:137], v[188:191], v[138:141]
	v_mfma_f32_16x16x32_f16 v[110:113], v[126:129], v[196:199], v[110:113]
	v_mfma_f32_16x16x32_f16 v[106:109], v[134:137], v[196:199], v[106:109]
	v_mfma_f32_16x16x32_f16 v[94:97], v[126:129], v[204:207], v[94:97]
	v_mfma_f32_16x16x32_f16 v[90:93], v[134:137], v[204:207], v[90:93]
	v_mfma_f32_16x16x32_f16 v[78:81], v[126:129], v[212:215], v[78:81]
	v_mfma_f32_16x16x32_f16 v[74:77], v[134:137], v[212:215], v[74:77]
	s_setprio 0
	s_setprio 1
	v_mfma_f32_16x16x32_f16 v[118:121], v[162:165], v[184:187], v[118:121]
	v_mfma_f32_16x16x32_f16 v[114:117], v[176:179], v[184:187], v[114:117]
	v_mfma_f32_16x16x32_f16 v[102:105], v[162:165], v[192:195], v[102:105]
	v_mfma_f32_16x16x32_f16 v[98:101], v[176:179], v[192:195], v[98:101]
	v_mfma_f32_16x16x32_f16 v[86:89], v[162:165], v[200:203], v[86:89]
	v_mfma_f32_16x16x32_f16 v[82:85], v[176:179], v[200:203], v[82:85]
	v_mfma_f32_16x16x32_f16 v[70:73], v[162:165], v[208:211], v[70:73]
	v_mfma_f32_16x16x32_f16 v[66:69], v[176:179], v[208:211], v[66:69]
	v_mfma_f32_16x16x32_f16 v[118:121], v[172:175], v[188:191], v[118:121]
	v_mfma_f32_16x16x32_f16 v[114:117], v[180:183], v[188:191], v[114:117]
	v_mfma_f32_16x16x32_f16 v[102:105], v[172:175], v[196:199], v[102:105]
	v_mfma_f32_16x16x32_f16 v[98:101], v[180:183], v[196:199], v[98:101]
	v_mfma_f32_16x16x32_f16 v[86:89], v[172:175], v[204:207], v[86:89]
	v_mfma_f32_16x16x32_f16 v[82:85], v[180:183], v[204:207], v[82:85]
	v_mfma_f32_16x16x32_f16 v[70:73], v[172:175], v[212:215], v[70:73]
	v_mfma_f32_16x16x32_f16 v[66:69], v[180:183], v[212:215], v[66:69]
	s_setprio 0
	s_barrier
; #define GM_STAGE(bufoff, gbase, voff) do { _Pragma("unroll") for (int _i = 0; _i < 2; ++_i) \
;         __builtin_amdgcn_global_load_lds((const unsigned*)((const char*)(gbase) + (voff)[_i]), (LAS unsigned*)(lds + (bufoff) + ldsw + _i * 8192), 16, 0, 0); } while (0)
; #define GM_LDA(dst, b, h) do { _Pragma("unroll") for (int m = 0; m < 4; ++m) _Pragma("unroll") for (int k = 0; k < 2; ++k) dst[m][k] = *(const LAS s16x8*)(lds + GM_SA(b, h) + aoff + m * 2048 + k * 1024); } while (0)
; #define GM_MMA(ai, bj, At, Bt) do { __builtin_amdgcn_s_setprio(1); _Pragma("unroll") for (int m = 0; m < 4; ++m) _Pragma("unroll") for (int n = 0; n < 2; ++n) _Pragma("unroll") for (int k = 0; k < 2; ++k) \
;         acc[ai][bj][m][n] = mma16<BF>(Bt[n][k], At[m][k], acc[ai][bj][m][n]); __builtin_amdgcn_s_setprio(0); } while (0)
; #define GM_WAIT_V(n) asm volatile("s_waitcnt vmcnt(" #n ")" ::: "memory")
; #define GM_WAIT_L(n) asm volatile("s_waitcnt lgkmcnt(" #n ")" ::: "memory")
; #define GM_BAR __builtin_amdgcn_s_barrier()
; #define GM_SCHED __builtin_amdgcn_sched_barrier(0)
; #define GM_STA_H0(buf, p, o0) do { if constexpr (GATHER) GM_STAGE(buf, p, o0); else GM_STAGE(buf, p, voffA); } while (0)
; template <bool BF, bool GATHER = false, class Epi, class Hook>
; __device__ __forceinline__ void gemm_phase(LAS unsigned char* lds, const Gemm g, const Order& S, const Epi& E, Hook& HK) {
;     ...
;             GM_LDA(At, 1, 1); GM_STAGE(GM_SB(1, 0), b3, voffB); GM_STAGE(GM_SB(1, 1), b3 + hstepB, voffB); GM_STA_H0(GM_SA(1, 0), a3, s0);
;             GM_WAIT_V(8); GM_WAIT_L(0); GM_BAR; GM_MMA(1, 0, At, B0); GM_MMA(1, 1, At, B1); GM_BAR; GM_SCHED;
;         }
;         if (wr == 0) GM_BAR;
	s_add_i32 s26, s50, s31
	v_lshl_add_u64 v[216:217], v[216:217], 0, s[10:11]
	s_mov_b32 m0, s26
	global_load_lds_dwordx4 v[216:217], off
	s_add_i32 m0, s26, 0x2000
	s_add_u32 s24, s24, 0x40080
	v_lshl_add_u64 v[216:217], v[218:219], 0, s[10:11]
	s_addc_u32 s25, s25, 0
	s_add_i32 s26, s51, s31
	global_load_lds_dwordx4 v[216:217], off
	v_lshl_add_u64 v[216:217], s[24:25], 0, v[148:149]
	s_mov_b32 m0, s26
	s_nop 0
	global_load_lds_dwordx4 v[216:217], off
	v_lshl_add_u64 v[216:217], s[24:25], 0, v[152:153]
	s_add_i32 m0, s26, 0x2000
	s_nop 0
	global_load_lds_dwordx4 v[216:217], off
	v_lshl_add_u64 v[216:217], v[220:221], 0, s[10:11]
	s_mov_b32 m0, s40
	s_nop 0
	global_load_lds_dwordx4 v[216:217], off
	v_lshl_add_u64 v[216:217], v[222:223], 0, s[10:11]
	s_mov_b32 m0, s41
	s_nop 0
	global_load_lds_dwordx4 v[216:217], off
	ds_read_b128 v[184:187], v170 offset:49152
	ds_read_b128 v[188:191], v170 offset:50176
	ds_read_b128 v[192:195], v170 offset:51200
	ds_read_b128 v[196:199], v170 offset:52224
	ds_read_b128 v[200:203], v170 offset:53248
	ds_read_b128 v[204:207], v170 offset:54272
	ds_read_b128 v[208:211], v170 offset:55296
	ds_read_b128 v[212:215], v170 offset:56320
	s_waitcnt vmcnt(8)
	s_waitcnt lgkmcnt(0)
	s_barrier
	s_setprio 1
	s_waitcnt lgkmcnt(0)
	v_mfma_f32_16x16x32_f16 v[62:65], v[122:125], v[184:187], v[62:65]
	v_mfma_f32_16x16x32_f16 v[58:61], v[130:133], v[184:187], v[58:61]
	v_mfma_f32_16x16x32_f16 v[46:49], v[122:125], v[192:195], v[46:49]
	v_mfma_f32_16x16x32_f16 v[42:45], v[130:133], v[192:195], v[42:45]
	v_mfma_f32_16x16x32_f16 v[30:33], v[122:125], v[200:203], v[30:33]
	v_mfma_f32_16x16x32_f16 v[26:29], v[130:133], v[200:203], v[26:29]
	v_mfma_f32_16x16x32_f16 v[14:17], v[122:125], v[208:211], v[14:17]
	v_mfma_f32_16x16x32_f16 v[10:13], v[130:133], v[208:211], v[10:13]
	v_mfma_f32_16x16x32_f16 v[62:65], v[126:129], v[188:191], v[62:65]
	v_mfma_f32_16x16x32_f16 v[58:61], v[134:137], v[188:191], v[58:61]
	v_mfma_f32_16x16x32_f16 v[46:49], v[126:129], v[196:199], v[46:49]
	v_mfma_f32_16x16x32_f16 v[42:45], v[134:137], v[196:199], v[42:45]
	v_mfma_f32_16x16x32_f16 v[30:33], v[126:129], v[204:207], v[30:33]
	v_mfma_f32_16x16x32_f16 v[26:29], v[134:137], v[204:207], v[26:29]
	v_mfma_f32_16x16x32_f16 v[14:17], v[126:129], v[212:215], v[14:17]
	v_mfma_f32_16x16x32_f16 v[10:13], v[134:137], v[212:215], v[10:13]
	s_setprio 0
	s_setprio 1
	v_mfma_f32_16x16x32_f16 v[54:57], v[162:165], v[184:187], v[54:57]
	v_mfma_f32_16x16x32_f16 v[50:53], v[176:179], v[184:187], v[50:53]
	v_mfma_f32_16x16x32_f16 v[38:41], v[162:165], v[192:195], v[38:41]
	v_mfma_f32_16x16x32_f16 v[34:37], v[176:179], v[192:195], v[34:37]
	v_mfma_f32_16x16x32_f16 v[22:25], v[162:165], v[200:203], v[22:25]
	v_mfma_f32_16x16x32_f16 v[18:21], v[176:179], v[200:203], v[18:21]
	v_mfma_f32_16x16x32_f16 v[6:9], v[162:165], v[208:211], v[6:9]
	v_mfma_f32_16x16x32_f16 v[2:5], v[176:179], v[208:211], v[2:5]
	v_mfma_f32_16x16x32_f16 v[54:57], v[172:175], v[188:191], v[54:57]
	v_mfma_f32_16x16x32_f16 v[50:53], v[180:183], v[188:191], v[50:53]
	v_mfma_f32_16x16x32_f16 v[38:41], v[172:175], v[196:199], v[38:41]
	v_mfma_f32_16x16x32_f16 v[34:37], v[180:183], v[196:199], v[34:37]
	v_mfma_f32_16x16x32_f16 v[22:25], v[172:175], v[204:207], v[22:25]
	v_mfma_f32_16x16x32_f16 v[18:21], v[180:183], v[204:207], v[18:21]
	v_mfma_f32_16x16x32_f16 v[6:9], v[172:175], v[212:215], v[6:9]
	v_mfma_f32_16x16x32_f16 v[2:5], v[180:183], v[212:215], v[2:5]
	s_setprio 0
	s_barrier
	s_add_i32 s49, s49, 2
	s_add_u32 s22, s22, 0x100
	s_addc_u32 s23, s23, 0
	s_add_u32 s47, s47, 0x100
	s_addc_u32 s48, s48, 0
	s_cmp_gt_u32 s49, 13
	s_cbranch_scc0 .LBB0_1480
	s_and_b64 vcc, exec, s[12:13]
	s_cbranch_vccz .LBB0_1483
	s_barrier

; #define GM_STAGE(bufoff, gbase, voff) do { _Pragma("unroll") for (int _i = 0; _i < 2; ++_i) \
;         __builtin_amdgcn_global_load_lds((const unsigned*)((const char*)(gbase) + (voff)[_i]), (LAS unsigned*)(lds + (bufoff) + ldsw + _i * 8192), 16, 0, 0); } while (0)
; #define GM_LDA(dst, b, h) do { _Pragma("unroll") for (int m = 0; m < 4; ++m) _Pragma("unroll") for (int k = 0; k < 2; ++k) dst[m][k] = *(const LAS s16x8*)(lds + GM_SA(b, h) + aoff + m * 2048 + k * 1024); } while (0)
; #define GM_LDB(dst, b, h) do { _Pragma("unroll") for (int n = 0; n < 2; ++n) _Pragma("unroll") for (int k = 0; k < 2; ++k) dst[n][k] = *(const LAS s16x8*)(lds + GM_SB(b, h) + boff + n * 2048 + k * 1024); } while (0)
; #define GM_MMA(ai, bj, At, Bt) do { __builtin_amdgcn_s_setprio(1); _Pragma("unroll") for (int m = 0; m < 4; ++m) _Pragma("unroll") for (int n = 0; n < 2; ++n) _Pragma("unroll") for (int k = 0; k < 2; ++k) \
;         acc[ai][bj][m][n] = mma16<BF>(Bt[n][k], At[m][k], acc[ai][bj][m][n]); __builtin_amdgcn_s_setprio(0); } while (0)
; #define GM_WAIT_V(n) asm volatile("s_waitcnt vmcnt(" #n ")" ::: "memory")
; #define GM_BAR __builtin_amdgcn_s_barrier()
; template <bool BF, bool GATHER = false, class Epi, class Hook>
; __device__ __forceinline__ void gemm_phase(LAS unsigned char* lds, const Gemm g, const Order& S, const Epi& E, Hook& HK) {
;     ...
;         for (int t = 0; t < nt; t += 2) {
;             const bool last = (t == nt - 2);
;             const char* a1 = cA + (size_t)(t + 1) * kstep;
;             const char* a2 = last ? nA : cA + (size_t)(t + 2) * kstep; const char* b2 = last ? nB : cB + (size_t)(t + 2) * kstep;
;             const char* a3 = a2 + kstep; const char* b3 = b2 + kstep;
;             unsigned s0[2], s1[2];
;             if constexpr (GATHER) { s0[0] = last ? nA0[0] : gA0[0]; s0[1] = last ? nA0[1] : gA0[1]; s1[0] = last ? nA1[0] : gA1[0]; s1[1] = last ? nA1[1] : gA1[1]; }
;             GM_LDB(B0, 0, 0); GM_LDB(B1, 0, 1); GM_SCHED; GM_LDA(At, 0, 0); GM_STA_H1(GM_SA(1, 1), a1, gA1);
;             GM_WAIT_V(8); GM_WAIT_L(0); GM_BAR; GM_MMA(0, 0, At, B0); GM_MMA(0, 1, At, B1); GM_BAR; GM_SCHED;
;             GM_LDA(At, 0, 1); GM_STAGE(GM_SB(0, 0), b2, voffB); GM_STAGE(GM_SB(0, 1), b2 + hstepB, voffB); GM_STA_H0(GM_SA(0, 0), a2, s0);
;             GM_WAIT_V(8); GM_WAIT_L(0); GM_BAR; GM_MMA(1, 0, At, B0); GM_MMA(1, 1, At, B1); GM_BAR; GM_SCHED;
.LBB0_1867:
	s_add_u32 s22, s2, 0x100
	s_addc_u32 s23, s3, 0
	s_cmp_eq_u32 s52, 40
	s_cselect_b32 s27, s7, s23
	s_cselect_b32 s26, s6, s22
	s_cselect_b32 s25, s21, s51
	s_cselect_b32 s24, s20, s50
	v_lshl_add_u64 v[216:217], s[2:3], 0, v[138:139]
	s_add_i32 m0, s29, 0xc000
	global_load_lds_dwordx4 v[216:217], off
	v_lshl_add_u64 v[216:217], s[2:3], 0, v[140:141]
	s_add_i32 m0, s29, 0xe000
	s_nop 0
	global_load_lds_dwordx4 v[216:217], off
	ds_read_b128 v[146:149], v153
	ds_read_b128 v[156:159], v153 offset:1024
	ds_read_b128 v[160:163], v153 offset:2048
	ds_read_b128 v[164:167], v153 offset:3072
	ds_read_b128 v[168:171], v154
	ds_read_b128 v[172:175], v154 offset:1024
	ds_read_b128 v[176:179], v154 offset:2048
	ds_read_b128 v[180:183], v154 offset:3072
	ds_read_b128 v[184:187], v155
	ds_read_b128 v[188:191], v155 offset:1024
	ds_read_b128 v[192:195], v155 offset:2048
	ds_read_b128 v[196:199], v155 offset:3072
	ds_read_b128 v[200:203], v155 offset:4096
	ds_read_b128 v[204:207], v155 offset:5120
	ds_read_b128 v[208:211], v155 offset:6144
	ds_read_b128 v[212:215], v155 offset:7168
	s_waitcnt vmcnt(8)
	s_waitcnt lgkmcnt(0)
	s_barrier
	s_setprio 1
	s_waitcnt lgkmcnt(0)
	v_mfma_f32_16x16x32_bf16 v[126:129], v[146:149], v[184:187], v[126:129]
	v_mfma_f32_16x16x32_bf16 v[122:125], v[160:163], v[184:187], v[122:125]
	v_mfma_f32_16x16x32_bf16 v[110:113], v[146:149], v[192:195], v[110:113]
	v_mfma_f32_16x16x32_bf16 v[106:109], v[160:163], v[192:195], v[106:109]
	v_mfma_f32_16x16x32_bf16 v[94:97], v[146:149], v[200:203], v[94:97]
	v_mfma_f32_16x16x32_bf16 v[90:93], v[160:163], v[200:203], v[90:93]
	v_mfma_f32_16x16x32_bf16 v[78:81], v[146:149], v[208:211], v[78:81]
	v_mfma_f32_16x16x32_bf16 v[74:77], v[160:163], v[208:211], v[74:77]
	v_mfma_f32_16x16x32_bf16 v[126:129], v[156:159], v[188:191], v[126:129]
	v_mfma_f32_16x16x32_bf16 v[122:125], v[164:167], v[188:191], v[122:125]
	v_mfma_f32_16x16x32_bf16 v[110:113], v[156:159], v[196:199], v[110:113]
	v_mfma_f32_16x16x32_bf16 v[106:109], v[164:167], v[196:199], v[106:109]
	v_mfma_f32_16x16x32_bf16 v[94:97], v[156:159], v[204:207], v[94:97]
	v_mfma_f32_16x16x32_bf16 v[90:93], v[164:167], v[204:207], v[90:93]
	v_mfma_f32_16x16x32_bf16 v[78:81], v[156:159], v[212:215], v[78:81]
	v_mfma_f32_16x16x32_bf16 v[74:77], v[164:167], v[212:215], v[74:77]
	s_setprio 0
	s_setprio 1
	v_mfma_f32_16x16x32_bf16 v[118:121], v[168:171], v[184:187], v[118:121]
	v_mfma_f32_16x16x32_bf16 v[114:117], v[176:179], v[184:187], v[114:117]
	v_mfma_f32_16x16x32_bf16 v[102:105], v[168:171], v[192:195], v[102:105]
	v_mfma_f32_16x16x32_bf16 v[98:101], v[176:179], v[192:195], v[98:101]
	v_mfma_f32_16x16x32_bf16 v[86:89], v[168:171], v[200:203], v[86:89]
	v_mfma_f32_16x16x32_bf16 v[82:85], v[176:179], v[200:203], v[82:85]
	v_mfma_f32_16x16x32_bf16 v[70:73], v[168:171], v[208:211], v[70:73]
	v_mfma_f32_16x16x32_bf16 v[66:69], v[176:179], v[208:211], v[66:69]
	v_mfma_f32_16x16x32_bf16 v[118:121], v[172:175], v[188:191], v[118:121]
	v_mfma_f32_16x16x32_bf16 v[114:117], v[180:183], v[188:191], v[114:117]
	v_mfma_f32_16x16x32_bf16 v[102:105], v[172:175], v[196:199], v[102:105]
	v_mfma_f32_16x16x32_bf16 v[98:101], v[180:183], v[196:199], v[98:101]
	v_mfma_f32_16x16x32_bf16 v[86:89], v[172:175], v[204:207], v[86:89]
	v_mfma_f32_16x16x32_bf16 v[82:85], v[180:183], v[204:207], v[82:85]
	v_mfma_f32_16x16x32_bf16 v[70:73], v[172:175], v[212:215], v[70:73]
	v_mfma_f32_16x16x32_bf16 v[66:69], v[180:183], v[212:215], v[66:69]
	s_setprio 0
	s_barrier
	s_add_i32 s2, s43, s28
	v_lshl_add_u64 v[216:217], s[24:25], 0, v[132:133]
	s_mov_b32 m0, s2
	global_load_lds_dwordx4 v[216:217], off
	s_add_i32 m0, s2, 0x2000
	s_add_u32 s2, s24, 0xb0000
	v_lshl_add_u64 v[218:219], s[24:25], 0, v[136:137]
	s_addc_u32 s3, s25, 0
	s_add_i32 s53, s44, s28
	global_load_lds_dwordx4 v[218:219], off
	v_lshl_add_u64 v[220:221], s[2:3], 0, v[132:133]
	s_mov_b32 m0, s53
	v_lshl_add_u64 v[222:223], s[26:27], 0, v[134:135]
	global_load_lds_dwordx4 v[220:221], off
	v_lshl_add_u64 v[220:221], s[2:3], 0, v[136:137]
	s_add_i32 m0, s53, 0x2000
	s_nop 0
	global_load_lds_dwordx4 v[220:221], off
	v_lshl_add_u64 v[220:221], s[26:27], 0, v[130:131]
	s_mov_b32 m0, s29
	s_nop 0
	global_load_lds_dwordx4 v[220:221], off
	s_mov_b32 m0, s30
	s_nop 0
	global_load_lds_dwordx4 v[222:223], off
	ds_read_b128 v[184:187], v155 offset:16384
	ds_read_b128 v[188:191], v155 offset:17408
	ds_read_b128 v[192:195], v155 offset:18432
	ds_read_b128 v[196:199], v155 offset:19456
	ds_read_b128 v[200:203], v155 offset:20480
	ds_read_b128 v[204:207], v155 offset:21504
	ds_read_b128 v[208:211], v155 offset:22528
	ds_read_b128 v[212:215], v155 offset:23552
	s_waitcnt vmcnt(8)
	s_waitcnt lgkmcnt(0)
	s_barrier
; #define GM_LDA(dst, b, h) do { _Pragma("unroll") for (int m = 0; m < 4; ++m) _Pragma("unroll") for (int k = 0; k < 2; ++k) dst[m][k] = *(const LAS s16x8*)(lds + GM_SA(b, h) + aoff + m * 2048 + k * 1024); } while (0)
; #define GM_LDB(dst, b, h) do { _Pragma("unroll") for (int n = 0; n < 2; ++n) _Pragma("unroll") for (int k = 0; k < 2; ++k) dst[n][k] = *(const LAS s16x8*)(lds + GM_SB(b, h) + boff + n * 2048 + k * 1024); } while (0)
; #define GM_MMA(ai, bj, At, Bt) do { __builtin_amdgcn_s_setprio(1); _Pragma("unroll") for (int m = 0; m < 4; ++m) _Pragma("unroll") for (int n = 0; n < 2; ++n) _Pragma("unroll") for (int k = 0; k < 2; ++k) \
;         acc[ai][bj][m][n] = mma16<BF>(Bt[n][k], At[m][k], acc[ai][bj][m][n]); __builtin_amdgcn_s_setprio(0); } while (0)
; #define GM_WAIT_V(n) asm volatile("s_waitcnt vmcnt(" #n ")" ::: "memory")
; #define GM_WAIT_L(n) asm volatile("s_waitcnt lgkmcnt(" #n ")" ::: "memory")
; #define GM_BAR __builtin_amdgcn_s_barrier()
; #define GM_SCHED __builtin_amdgcn_sched_barrier(0)
; #define GM_STA_H1(buf, p, o1) do { if constexpr (GATHER) GM_STAGE(buf, p, o1); else GM_STAGE(buf, (p) + hstepB, voffA); } while (0)
; template <bool BF, bool GATHER = false, class Epi, class Hook>
; __device__ __forceinline__ void gemm_phase(LAS unsigned char* lds, const Gemm g, const Order& S, const Epi& E, Hook& HK) {
;     ...
;             GM_WAIT_V(8); GM_WAIT_L(0); GM_BAR; GM_MMA(1, 0, At, B0); GM_MMA(1, 1, At, B1); GM_BAR; GM_SCHED;
;             GM_LDB(B0, 1, 0); GM_LDB(B1, 1, 1); GM_SCHED; GM_LDA(At, 1, 0); GM_STA_H1(GM_SA(0, 1), a2, s1);
;             GM_WAIT_V(8); GM_WAIT_L(0); GM_BAR; GM_MMA(0, 0, At, B0); GM_MMA(0, 1, At, B1); GM_BAR; GM_SCHED;
	s_setprio 1
	s_waitcnt lgkmcnt(0)
	v_mfma_f32_16x16x32_bf16 v[62:65], v[146:149], v[184:187], v[62:65]
	v_mfma_f32_16x16x32_bf16 v[58:61], v[160:163], v[184:187], v[58:61]
	v_mfma_f32_16x16x32_bf16 v[46:49], v[146:149], v[192:195], v[46:49]
	v_mfma_f32_16x16x32_bf16 v[42:45], v[160:163], v[192:195], v[42:45]
	v_mfma_f32_16x16x32_bf16 v[30:33], v[146:149], v[200:203], v[30:33]
	v_mfma_f32_16x16x32_bf16 v[26:29], v[160:163], v[200:203], v[26:29]
	v_mfma_f32_16x16x32_bf16 v[14:17], v[146:149], v[208:211], v[14:17]
	v_mfma_f32_16x16x32_bf16 v[10:13], v[160:163], v[208:211], v[10:13]
	v_mfma_f32_16x16x32_bf16 v[62:65], v[156:159], v[188:191], v[62:65]
	v_mfma_f32_16x16x32_bf16 v[58:61], v[164:167], v[188:191], v[58:61]
	v_mfma_f32_16x16x32_bf16 v[46:49], v[156:159], v[196:199], v[46:49]
	v_mfma_f32_16x16x32_bf16 v[42:45], v[164:167], v[196:199], v[42:45]
	v_mfma_f32_16x16x32_bf16 v[30:33], v[156:159], v[204:207], v[30:33]
	v_mfma_f32_16x16x32_bf16 v[26:29], v[164:167], v[204:207], v[26:29]
	v_mfma_f32_16x16x32_bf16 v[14:17], v[156:159], v[212:215], v[14:17]
	v_mfma_f32_16x16x32_bf16 v[10:13], v[164:167], v[212:215], v[10:13]
	s_setprio 0
	s_setprio 1
	v_mfma_f32_16x16x32_bf16 v[54:57], v[168:171], v[184:187], v[54:57]
	v_mfma_f32_16x16x32_bf16 v[50:53], v[176:179], v[184:187], v[50:53]
	v_mfma_f32_16x16x32_bf16 v[38:41], v[168:171], v[192:195], v[38:41]
	v_mfma_f32_16x16x32_bf16 v[34:37], v[176:179], v[192:195], v[34:37]
	v_mfma_f32_16x16x32_bf16 v[22:25], v[168:171], v[200:203], v[22:25]
	v_mfma_f32_16x16x32_bf16 v[18:21], v[176:179], v[200:203], v[18:21]
	v_mfma_f32_16x16x32_bf16 v[6:9], v[168:171], v[208:211], v[6:9]
	v_mfma_f32_16x16x32_bf16 v[2:5], v[176:179], v[208:211], v[2:5]
	v_mfma_f32_16x16x32_bf16 v[54:57], v[172:175], v[188:191], v[54:57]
	v_mfma_f32_16x16x32_bf16 v[50:53], v[180:183], v[188:191], v[50:53]
	v_mfma_f32_16x16x32_bf16 v[38:41], v[172:175], v[196:199], v[38:41]
	v_mfma_f32_16x16x32_bf16 v[34:37], v[180:183], v[196:199], v[34:37]
	v_mfma_f32_16x16x32_bf16 v[22:25], v[172:175], v[204:207], v[22:25]
	v_mfma_f32_16x16x32_bf16 v[18:21], v[180:183], v[204:207], v[18:21]
	v_mfma_f32_16x16x32_bf16 v[6:9], v[172:175], v[212:215], v[6:9]
	v_mfma_f32_16x16x32_bf16 v[2:5], v[180:183], v[212:215], v[2:5]
	s_setprio 0
	s_barrier
	s_add_u32 s2, s26, 0xb0000
	s_addc_u32 s3, s27, 0
	s_mov_b32 m0, s31
	v_lshl_add_u64 v[224:225], s[2:3], 0, v[130:131]
	global_load_lds_dwordx4 v[224:225], off
	v_lshl_add_u64 v[224:225], s[2:3], 0, v[134:135]
	s_mov_b32 m0, s33
	s_nop 0
	global_load_lds_dwordx4 v[224:225], off
	s_mov_b32 s54, 0x1c000
	s_mov_b32 s53, 0x18000
	v_add_u32_e32 v244, s53, v150
	v_add_u32_e32 v245, s54, v150
	ds_read_b128 v[146:149], v244
	ds_read_b128 v[156:159], v244 offset:1024
	ds_read_b128 v[160:163], v244 offset:2048
	ds_read_b128 v[164:167], v244 offset:3072
	ds_read_b128 v[168:171], v245
	ds_read_b128 v[172:175], v245 offset:1024
	ds_read_b128 v[176:179], v245 offset:2048
	ds_read_b128 v[180:183], v245 offset:3072
	ds_read_b128 v[184:187], v155 offset:32768
	ds_read_b128 v[188:191], v155 offset:33792
	ds_read_b128 v[192:195], v155 offset:34816
	ds_read_b128 v[196:199], v155 offset:35840
	ds_read_b128 v[200:203], v155 offset:36864
	ds_read_b128 v[204:207], v155 offset:37888
	ds_read_b128 v[208:211], v155 offset:38912
	ds_read_b128 v[212:215], v155 offset:39936
	s_waitcnt vmcnt(8)
	s_waitcnt lgkmcnt(0)
	s_barrier
	s_setprio 1
	s_waitcnt lgkmcnt(0)
	v_mfma_f32_16x16x32_bf16 v[126:129], v[146:149], v[184:187], v[126:129]
	v_mfma_f32_16x16x32_bf16 v[122:125], v[160:163], v[184:187], v[122:125]
	v_mfma_f32_16x16x32_bf16 v[110:113], v[146:149], v[192:195], v[110:113]
	v_mfma_f32_16x16x32_bf16 v[106:109], v[160:163], v[192:195], v[106:109]
	v_mfma_f32_16x16x32_bf16 v[94:97], v[146:149], v[200:203], v[94:97]
	v_mfma_f32_16x16x32_bf16 v[90:93], v[160:163], v[200:203], v[90:93]
	v_mfma_f32_16x16x32_bf16 v[78:81], v[146:149], v[208:211], v[78:81]
	v_mfma_f32_16x16x32_bf16 v[74:77], v[160:163], v[208:211], v[74:77]
	v_mfma_f32_16x16x32_bf16 v[126:129], v[156:159], v[188:191], v[126:129]
	v_mfma_f32_16x16x32_bf16 v[122:125], v[164:167], v[188:191], v[122:125]
	v_mfma_f32_16x16x32_bf16 v[110:113], v[156:159], v[196:199], v[110:113]
	v_mfma_f32_16x16x32_bf16 v[106:109], v[164:167], v[196:199], v[106:109]
	v_mfma_f32_16x16x32_bf16 v[94:97], v[156:159], v[204:207], v[94:97]
	v_mfma_f32_16x16x32_bf16 v[90:93], v[164:167], v[204:207], v[90:93]
	v_mfma_f32_16x16x32_bf16 v[78:81], v[156:159], v[212:215], v[78:81]
	v_mfma_f32_16x16x32_bf16 v[74:77], v[164:167], v[212:215], v[74:77]
	s_setprio 0
	s_setprio 1
	v_mfma_f32_16x16x32_bf16 v[118:121], v[168:171], v[184:187], v[118:121]
	v_mfma_f32_16x16x32_bf16 v[114:117], v[176:179], v[184:187], v[114:117]
	v_mfma_f32_16x16x32_bf16 v[102:105], v[168:171], v[192:195], v[102:105]
	v_mfma_f32_16x16x32_bf16 v[98:101], v[176:179], v[192:195], v[98:101]
	v_mfma_f32_16x16x32_bf16 v[86:89], v[168:171], v[200:203], v[86:89]
	v_mfma_f32_16x16x32_bf16 v[82:85], v[176:179], v[200:203], v[82:85]
	v_mfma_f32_16x16x32_bf16 v[70:73], v[168:171], v[208:211], v[70:73]
	v_mfma_f32_16x16x32_bf16 v[66:69], v[176:179], v[208:211], v[66:69]
	v_mfma_f32_16x16x32_bf16 v[118:121], v[172:175], v[188:191], v[118:121]
	v_mfma_f32_16x16x32_bf16 v[114:117], v[180:183], v[188:191], v[114:117]
	v_mfma_f32_16x16x32_bf16 v[102:105], v[172:175], v[196:199], v[102:105]
	v_mfma_f32_16x16x32_bf16 v[98:101], v[180:183], v[196:199], v[98:101]
	v_mfma_f32_16x16x32_bf16 v[86:89], v[172:175], v[204:207], v[86:89]
	v_mfma_f32_16x16x32_bf16 v[82:85], v[180:183], v[204:207], v[82:85]
	v_mfma_f32_16x16x32_bf16 v[70:73], v[172:175], v[212:215], v[70:73]
	v_mfma_f32_16x16x32_bf16 v[66:69], v[180:183], v[212:215], v[66:69]
	s_setprio 0
	s_barrier
; #define GM_STAGE(bufoff, gbase, voff) do { _Pragma("unroll") for (int _i = 0; _i < 2; ++_i) \
;         __builtin_amdgcn_global_load_lds((const unsigned*)((const char*)(gbase) + (voff)[_i]), (LAS unsigned*)(lds + (bufoff) + ldsw + _i * 8192), 16, 0, 0); } while (0)
; #define GM_LDA(dst, b, h) do { _Pragma("unroll") for (int m = 0; m < 4; ++m) _Pragma("unroll") for (int k = 0; k < 2; ++k) dst[m][k] = *(const LAS s16x8*)(lds + GM_SA(b, h) + aoff + m * 2048 + k * 1024); } while (0)
; #define GM_MMA(ai, bj, At, Bt) do { __builtin_amdgcn_s_setprio(1); _Pragma("unroll") for (int m = 0; m < 4; ++m) _Pragma("unroll") for (int n = 0; n < 2; ++n) _Pragma("unroll") for (int k = 0; k < 2; ++k) \
;         acc[ai][bj][m][n] = mma16<BF>(Bt[n][k], At[m][k], acc[ai][bj][m][n]); __builtin_amdgcn_s_setprio(0); } while (0)
; #define GM_WAIT_V(n) asm volatile("s_waitcnt vmcnt(" #n ")" ::: "memory")
; #define GM_WAIT_L(n) asm volatile("s_waitcnt lgkmcnt(" #n ")" ::: "memory")
; #define GM_BAR __builtin_amdgcn_s_barrier()
; #define GM_SCHED __builtin_amdgcn_sched_barrier(0)
; #define GM_STA_H0(buf, p, o0) do { if constexpr (GATHER) GM_STAGE(buf, p, o0); else GM_STAGE(buf, p, voffA); } while (0)
; template <bool BF, bool GATHER = false, class Epi, class Hook>
; __device__ __forceinline__ void gemm_phase(LAS unsigned char* lds, const Gemm g, const Order& S, const Epi& E, Hook& HK) {
;     ...
;             GM_LDA(At, 1, 1); GM_STAGE(GM_SB(1, 0), b3, voffB); GM_STAGE(GM_SB(1, 1), b3 + hstepB, voffB); GM_STA_H0(GM_SA(1, 0), a3, s0);
;             GM_WAIT_V(8); GM_WAIT_L(0); GM_BAR; GM_MMA(1, 0, At, B0); GM_MMA(1, 1, At, B1); GM_BAR; GM_SCHED;
;         }
	s_add_i32 s2, s53, s28
	v_lshl_add_u64 v[216:217], v[216:217], 0, s[12:13]
	s_mov_b32 m0, s2
	global_load_lds_dwordx4 v[216:217], off
	s_add_i32 m0, s2, 0x2000
	s_add_u32 s2, s24, 0xb0080
	v_lshl_add_u64 v[216:217], v[218:219], 0, s[12:13]
	s_addc_u32 s3, s25, 0
	s_add_i32 s24, s54, s28
	global_load_lds_dwordx4 v[216:217], off
	v_lshl_add_u64 v[216:217], s[2:3], 0, v[132:133]
	s_mov_b32 m0, s24
	s_nop 0
	global_load_lds_dwordx4 v[216:217], off
	v_lshl_add_u64 v[216:217], s[2:3], 0, v[136:137]
	s_add_i32 m0, s24, 0x2000
	s_nop 0
	global_load_lds_dwordx4 v[216:217], off
	v_lshl_add_u64 v[216:217], v[220:221], 0, s[12:13]
	s_mov_b32 m0, s36
	s_nop 0
	global_load_lds_dwordx4 v[216:217], off
	v_lshl_add_u64 v[216:217], v[222:223], 0, s[12:13]
	s_mov_b32 m0, s37
	s_nop 0
	global_load_lds_dwordx4 v[216:217], off
	ds_read_b128 v[184:187], v155 offset:49152
	ds_read_b128 v[188:191], v155 offset:50176
	ds_read_b128 v[192:195], v155 offset:51200
	ds_read_b128 v[196:199], v155 offset:52224
	ds_read_b128 v[200:203], v155 offset:53248
	ds_read_b128 v[204:207], v155 offset:54272
	ds_read_b128 v[208:211], v155 offset:55296
	ds_read_b128 v[212:215], v155 offset:56320
	s_waitcnt vmcnt(8)
	s_waitcnt lgkmcnt(0)
	s_barrier
	s_setprio 1
	s_waitcnt lgkmcnt(0)
	v_mfma_f32_16x16x32_bf16 v[62:65], v[146:149], v[184:187], v[62:65]
	v_mfma_f32_16x16x32_bf16 v[58:61], v[160:163], v[184:187], v[58:61]
	v_mfma_f32_16x16x32_bf16 v[46:49], v[146:149], v[192:195], v[46:49]
	v_mfma_f32_16x16x32_bf16 v[42:45], v[160:163], v[192:195], v[42:45]
	v_mfma_f32_16x16x32_bf16 v[30:33], v[146:149], v[200:203], v[30:33]
	v_mfma_f32_16x16x32_bf16 v[26:29], v[160:163], v[200:203], v[26:29]
	v_mfma_f32_16x16x32_bf16 v[14:17], v[146:149], v[208:211], v[14:17]
	v_mfma_f32_16x16x32_bf16 v[10:13], v[160:163], v[208:211], v[10:13]
	v_mfma_f32_16x16x32_bf16 v[62:65], v[156:159], v[188:191], v[62:65]
	v_mfma_f32_16x16x32_bf16 v[58:61], v[164:167], v[188:191], v[58:61]
	v_mfma_f32_16x16x32_bf16 v[46:49], v[156:159], v[196:199], v[46:49]
	v_mfma_f32_16x16x32_bf16 v[42:45], v[164:167], v[196:199], v[42:45]
	v_mfma_f32_16x16x32_bf16 v[30:33], v[156:159], v[204:207], v[30:33]
	v_mfma_f32_16x16x32_bf16 v[26:29], v[164:167], v[204:207], v[26:29]
	v_mfma_f32_16x16x32_bf16 v[14:17], v[156:159], v[212:215], v[14:17]
	v_mfma_f32_16x16x32_bf16 v[10:13], v[164:167], v[212:215], v[10:13]
	s_setprio 0
	s_setprio 1
	v_mfma_f32_16x16x32_bf16 v[54:57], v[168:171], v[184:187], v[54:57]
	v_mfma_f32_16x16x32_bf16 v[50:53], v[176:179], v[184:187], v[50:53]
	v_mfma_f32_16x16x32_bf16 v[38:41], v[168:171], v[192:195], v[38:41]
	v_mfma_f32_16x16x32_bf16 v[34:37], v[176:179], v[192:195], v[34:37]
	v_mfma_f32_16x16x32_bf16 v[22:25], v[168:171], v[200:203], v[22:25]
	v_mfma_f32_16x16x32_bf16 v[18:21], v[176:179], v[200:203], v[18:21]
	v_mfma_f32_16x16x32_bf16 v[6:9], v[168:171], v[208:211], v[6:9]
	v_mfma_f32_16x16x32_bf16 v[2:5], v[176:179], v[208:211], v[2:5]
	v_mfma_f32_16x16x32_bf16 v[54:57], v[172:175], v[188:191], v[54:57]
	v_mfma_f32_16x16x32_bf16 v[50:53], v[180:183], v[188:191], v[50:53]
	v_mfma_f32_16x16x32_bf16 v[38:41], v[172:175], v[196:199], v[38:41]
	v_mfma_f32_16x16x32_bf16 v[34:37], v[180:183], v[196:199], v[34:37]
	v_mfma_f32_16x16x32_bf16 v[22:25], v[172:175], v[204:207], v[22:25]
	v_mfma_f32_16x16x32_bf16 v[18:21], v[180:183], v[204:207], v[18:21]
	v_mfma_f32_16x16x32_bf16 v[6:9], v[172:175], v[212:215], v[6:9]
	v_mfma_f32_16x16x32_bf16 v[2:5], v[180:183], v[212:215], v[2:5]
	s_setprio 0
	s_barrier
	s_add_i32 s52, s52, 2
	s_add_u32 s50, s50, 0x100
	s_addc_u32 s51, s51, 0
	s_cmp_gt_u32 s52, 41
	s_mov_b64 s[2:3], s[22:23]
	s_cbranch_scc0 .LBB0_1867
	s_and_b64 vcc, exec, s[14:15]
	s_cbranch_vccz .LBB0_1870
	s_barrier
